# speedup vs baseline: 1.0199x; 1.0199x over previous
_Z12k1_colsum_q8PKfPjPfS2_:
	s_load_dwordx8 s[4:11], s[0:1], 0x0
	v_and_b32_e32 v1, 63, v0
	v_lshrrev_b32_e32 v41, 6, v0
	s_mul_i32 s12, s2, 0xc35
	s_lshr_b32 s12, s12, 4
	v_readfirstlane_b32 s14, v41
	s_add_i32 s13, s2, 1
	s_mul_i32 s13, s13, 0xc35
	s_lshr_b32 s13, s13, 4
	s_sub_u32 s13, s13, s12
	s_sub_u32 s15, s13, 0xc0
	s_cmp_lt_u32 s14, s15
	s_cselect_b32 s29, 1, 0
	v_lshlrev_b32_e32 v34, 4, v1
	v_min_u32_e32 v35, 57, v1
	v_lshlrev_b32_e32 v35, 4, v35
	v_cmp_gt_u32_e64 s[18:19], 58, v1
	s_lshl_b32 s35, s14, 13
	s_add_u32 s36, s35, 0x1000
	v_add_u32_e32 v38, s35, v34
	v_lshrrev_b32_e32 v41, 5, v1
	v_mov_b32_e32 v42, 0xc35000
	v_mul_lo_u32 v39, v41, v42
	v_and_b32_e32 v42, 31, v1
	v_lshl_add_u32 v39, v42, 2, v39
	v_mov_b32_e32 v2, 0
	v_mov_b32_e32 v3, 0
	v_mov_b32_e32 v4, 0
	v_mov_b32_e32 v5, 0
	v_mov_b32_e32 v6, 0
	v_mov_b32_e32 v7, 0
	v_mov_b32_e32 v8, 0
	v_mov_b32_e32 v9, 0
	v_mov_b32_e32 v10, 0
	v_mov_b32_e32 v11, 0
	v_mov_b32_e32 v12, 0
	v_mov_b32_e32 v13, 0
	v_mov_b32_e32 v14, 0
	v_mov_b32_e32 v15, 0
	v_mov_b32_e32 v16, 0
	v_mov_b32_e32 v17, 0
	v_mov_b32_e32 v40, 0
	v_mov_b32_e32 v47, 0x42fe0000
	s_mov_b32 s32, 0x42fe0000
	s_mov_b32 s33, 0xc0c0400
	s_mov_b32 s34, 0x4000c0c
	s_add_u32 s15, s12, s14
	s_mul_i32 s37, s15, 0xfa0
	s_lshl_b32 s15, s15, 7
	s_waitcnt lgkmcnt(0)
	s_add_u32 s16, s4, s37
	s_addc_u32 s17, s5, 0
	s_add_u32 s40, s6, s15
	s_addc_u32 s41, s7, 0
	s_add_u32 s20, s40, 0x4800
	s_addc_u32 s21, s41, 0
	s_add_u32 s22, s20, 0x186a000
	s_addc_u32 s23, s21, 0
	s_add_u32 s24, s22, 0x186a000
	s_addc_u32 s25, s23, 0
	s_add_u32 s26, s24, 0x186a000
	s_addc_u32 s27, s25, 0
	s_mov_b32 m0, s35
	s_nop 0
	global_load_lds_dwordx4 v34, s[16:17] nt
	global_load_lds_dwordx4 v34, s[16:17] offset:1024 nt
	global_load_lds_dwordx4 v34, s[16:17] offset:2048 nt
	global_load_lds_dwordx4 v35, s[16:17] offset:3072 nt
	s_add_u32 s16, s16, 0x7d00
	s_addc_u32 s17, s17, 0
	s_waitcnt vmcnt(0)
	ds_read_b128 v[18:21], v38 offset:0
	ds_read_b128 v[22:25], v38 offset:1024
	ds_read_b128 v[26:29], v38 offset:2048
	ds_read_b128 v[30:33], v38 offset:3072
	s_waitcnt lgkmcnt(0)
	s_mov_b32 m0, s36
	s_nop 0
	global_load_lds_dwordx4 v34, s[16:17] nt
	global_load_lds_dwordx4 v34, s[16:17] offset:1024 nt
	global_load_lds_dwordx4 v34, s[16:17] offset:2048 nt
	global_load_lds_dwordx4 v35, s[16:17] offset:3072 nt
	s_add_u32 s16, s16, 0x7d00
	s_addc_u32 s17, s17, 0
	v_cndmask_b32_e64 v30, 0, v30, s[18:19]
	v_cndmask_b32_e64 v31, 0, v31, s[18:19]
	v_cndmask_b32_e64 v32, 0, v32, s[18:19]
	v_cndmask_b32_e64 v33, 0, v33, s[18:19]
	v_max3_f32 v41, |v18|, |v19|, |v20|
	v_max3_f32 v42, |v21|, |v22|, |v23|
	v_max3_f32 v43, |v24|, |v25|, |v26|
	v_max3_f32 v44, |v27|, |v28|, |v29|
	v_max3_f32 v45, |v30|, |v31|, |v32|
	v_max3_f32 v41, v41, v42, |v33|
	v_max3_f32 v43, v43, v44, v45
	v_max_f32_e32 v41, v41, v43
	v_pk_add_f32 v[2:3], v[2:3], v[18:19]
	v_pk_add_f32 v[4:5], v[4:5], v[20:21]
	v_max_f32_dpp v41, v41, v41 quad_perm:[1,0,3,2] row_mask:0xf bank_mask:0xf
	v_pk_add_f32 v[6:7], v[6:7], v[22:23]
	v_pk_add_f32 v[8:9], v[8:9], v[24:25]
	v_max_f32_dpp v41, v41, v41 quad_perm:[2,3,0,1] row_mask:0xf bank_mask:0xf
	v_pk_add_f32 v[10:11], v[10:11], v[26:27]
	v_pk_add_f32 v[12:13], v[12:13], v[28:29]
	v_max_f32_dpp v41, v41, v41 row_half_mirror row_mask:0xf bank_mask:0xf
	v_pk_add_f32 v[14:15], v[14:15], v[30:31]
	v_pk_add_f32 v[16:17], v[16:17], v[32:33]
	v_max_f32_dpp v41, v41, v41 row_mirror row_mask:0xf bank_mask:0xf
	s_nop 1
	v_max_f32_dpp v41, v41, v41 row_bcast:15 row_mask:0xa bank_mask:0xf
	s_nop 1
	v_max_f32_dpp v41, v41, v41 row_bcast:31 row_mask:0xc bank_mask:0xf
	s_nop 1
	v_readlane_b32 s28, v41, 63
	s_nop 1
	v_div_scale_f32 v48, s[30:31], s28, s28, v47
	v_rcp_f32_e32 v49, v48
	s_nop 0
	v_fma_f32 v50, -v48, v49, 1.0
	v_fmac_f32_e32 v49, v50, v49
	v_mov_b32_e32 v50, s28
	v_div_scale_f32 v50, vcc, s32, v50, s32
	v_mul_f32_e32 v51, v50, v49
	v_fma_f32 v52, -v48, v51, v50
	v_fmac_f32_e32 v51, v52, v49
	v_fma_f32 v48, -v48, v51, v50
	v_div_fmas_f32 v48, v48, v49, v51
	v_div_fixup_f32 v48, v48, s28, v47
	v_cmp_gt_f32_e64 vcc, s28, 0
	v_writelane_b32 v40, s28, 0
	s_nop 0
	v_cndmask_b32_e32 v48, 0, v48, vcc
	v_fmaak_f32 v49, v18, v48, 0x4b400000
	v_fmaak_f32 v50, v19, v48, 0x4b400000
	v_fmaak_f32 v51, v20, v48, 0x4b400000
	v_fmaak_f32 v52, v21, v48, 0x4b400000
	v_perm_b32 v49, v50, v49, s33
	v_perm_b32 v51, v52, v51, s34
	v_or_b32_e32 v56, v49, v51
	v_fmaak_f32 v53, v22, v48, 0x4b400000
	v_fmaak_f32 v54, v23, v48, 0x4b400000
	v_fmaak_f32 v55, v24, v48, 0x4b400000
	v_fmaak_f32 v46, v25, v48, 0x4b400000
	v_perm_b32 v53, v54, v53, s33
	v_perm_b32 v55, v46, v55, s34
	v_or_b32_e32 v57, v53, v55
	v_fmaak_f32 v49, v26, v48, 0x4b400000
	v_fmaak_f32 v50, v27, v48, 0x4b400000
	v_fmaak_f32 v51, v28, v48, 0x4b400000
	v_fmaak_f32 v52, v29, v48, 0x4b400000
	v_perm_b32 v49, v50, v49, s33
	v_perm_b32 v51, v52, v51, s34
	v_or_b32_e32 v58, v49, v51
	v_fmaak_f32 v53, v30, v48, 0x4b400000
	v_fmaak_f32 v54, v31, v48, 0x4b400000
	v_fmaak_f32 v55, v32, v48, 0x4b400000
	v_fmaak_f32 v46, v33, v48, 0x4b400000
	v_perm_b32 v53, v54, v53, s33
	v_perm_b32 v55, v46, v55, s34
	v_or_b32_e32 v59, v53, v55
	s_waitcnt vmcnt(0)
	ds_read_b128 v[18:21], v38 offset:4096
	ds_read_b128 v[22:25], v38 offset:5120
	ds_read_b128 v[26:29], v38 offset:6144
	ds_read_b128 v[30:33], v38 offset:7168
	s_waitcnt lgkmcnt(0)
	s_mov_b32 m0, s35
	s_nop 0
	global_load_lds_dwordx4 v34, s[16:17] nt
	global_load_lds_dwordx4 v34, s[16:17] offset:1024 nt
	global_load_lds_dwordx4 v34, s[16:17] offset:2048 nt
	global_load_lds_dwordx4 v35, s[16:17] offset:3072 nt
	s_add_u32 s16, s16, 0x7d00
	s_addc_u32 s17, s17, 0
	v_cndmask_b32_e64 v30, 0, v30, s[18:19]
	v_cndmask_b32_e64 v31, 0, v31, s[18:19]
	v_cndmask_b32_e64 v32, 0, v32, s[18:19]
	v_cndmask_b32_e64 v33, 0, v33, s[18:19]
	v_max3_f32 v41, |v18|, |v19|, |v20|
	v_max3_f32 v42, |v21|, |v22|, |v23|
	v_max3_f32 v43, |v24|, |v25|, |v26|
	v_max3_f32 v44, |v27|, |v28|, |v29|
	v_max3_f32 v45, |v30|, |v31|, |v32|
	v_max3_f32 v41, v41, v42, |v33|
	v_max3_f32 v43, v43, v44, v45
	v_max_f32_e32 v41, v41, v43
	v_pk_add_f32 v[2:3], v[2:3], v[18:19]
	v_pk_add_f32 v[4:5], v[4:5], v[20:21]
	v_max_f32_dpp v41, v41, v41 quad_perm:[1,0,3,2] row_mask:0xf bank_mask:0xf
	v_pk_add_f32 v[6:7], v[6:7], v[22:23]
	v_pk_add_f32 v[8:9], v[8:9], v[24:25]
	v_max_f32_dpp v41, v41, v41 quad_perm:[2,3,0,1] row_mask:0xf bank_mask:0xf
	v_pk_add_f32 v[10:11], v[10:11], v[26:27]
	v_pk_add_f32 v[12:13], v[12:13], v[28:29]
	v_max_f32_dpp v41, v41, v41 row_half_mirror row_mask:0xf bank_mask:0xf
	v_pk_add_f32 v[14:15], v[14:15], v[30:31]
	v_pk_add_f32 v[16:17], v[16:17], v[32:33]
	v_max_f32_dpp v41, v41, v41 row_mirror row_mask:0xf bank_mask:0xf
	s_nop 1
	v_max_f32_dpp v41, v41, v41 row_bcast:15 row_mask:0xa bank_mask:0xf
	s_nop 1
	v_max_f32_dpp v41, v41, v41 row_bcast:31 row_mask:0xc bank_mask:0xf
	s_nop 1
	v_readlane_b32 s28, v41, 63
	s_nop 1
	v_div_scale_f32 v48, s[30:31], s28, s28, v47
	v_rcp_f32_e32 v49, v48
	s_nop 0
	v_fma_f32 v50, -v48, v49, 1.0
	v_fmac_f32_e32 v49, v50, v49
	v_mov_b32_e32 v50, s28
	v_div_scale_f32 v50, vcc, s32, v50, s32
	v_mul_f32_e32 v51, v50, v49
	v_fma_f32 v52, -v48, v51, v50
	v_fmac_f32_e32 v51, v52, v49
	v_fma_f32 v48, -v48, v51, v50
	v_div_fmas_f32 v48, v48, v49, v51
	v_div_fixup_f32 v48, v48, s28, v47
	v_cmp_gt_f32_e64 vcc, s28, 0
	v_writelane_b32 v40, s28, 1
	s_nop 0
	v_cndmask_b32_e32 v48, 0, v48, vcc
	v_fmaak_f32 v49, v18, v48, 0x4b400000
	v_fmaak_f32 v50, v19, v48, 0x4b400000
	v_fmaak_f32 v51, v20, v48, 0x4b400000
	v_fmaak_f32 v52, v21, v48, 0x4b400000
	v_perm_b32 v49, v50, v49, s33
	v_perm_b32 v51, v52, v51, s34
	v_or_b32_e32 v60, v49, v51
	v_fmaak_f32 v53, v22, v48, 0x4b400000
	v_fmaak_f32 v54, v23, v48, 0x4b400000
	v_fmaak_f32 v55, v24, v48, 0x4b400000
	v_fmaak_f32 v46, v25, v48, 0x4b400000
	v_perm_b32 v53, v54, v53, s33
	v_perm_b32 v55, v46, v55, s34
	v_or_b32_e32 v61, v53, v55
	v_fmaak_f32 v49, v26, v48, 0x4b400000
	v_fmaak_f32 v50, v27, v48, 0x4b400000
	v_fmaak_f32 v51, v28, v48, 0x4b400000
	v_fmaak_f32 v52, v29, v48, 0x4b400000
	v_perm_b32 v49, v50, v49, s33
	v_perm_b32 v51, v52, v51, s34
	v_or_b32_e32 v62, v49, v51
	v_fmaak_f32 v53, v30, v48, 0x4b400000
	v_fmaak_f32 v54, v31, v48, 0x4b400000
	v_fmaak_f32 v55, v32, v48, 0x4b400000
	v_fmaak_f32 v46, v33, v48, 0x4b400000
	v_perm_b32 v53, v54, v53, s33
	v_perm_b32 v55, v46, v55, s34
	v_or_b32_e32 v63, v53, v55
	s_waitcnt vmcnt(0)
	ds_read_b128 v[18:21], v38 offset:0
	ds_read_b128 v[22:25], v38 offset:1024
	ds_read_b128 v[26:29], v38 offset:2048
	ds_read_b128 v[30:33], v38 offset:3072
	s_waitcnt lgkmcnt(0)
	s_mov_b32 m0, s36
	s_nop 0
	global_load_lds_dwordx4 v34, s[16:17] nt
	global_load_lds_dwordx4 v34, s[16:17] offset:1024 nt
	global_load_lds_dwordx4 v34, s[16:17] offset:2048 nt
	global_load_lds_dwordx4 v35, s[16:17] offset:3072 nt
	s_add_u32 s16, s16, 0x7d00
	s_addc_u32 s17, s17, 0
	v_cndmask_b32_e64 v30, 0, v30, s[18:19]
	v_cndmask_b32_e64 v31, 0, v31, s[18:19]
	v_cndmask_b32_e64 v32, 0, v32, s[18:19]
	v_cndmask_b32_e64 v33, 0, v33, s[18:19]
	v_max3_f32 v41, |v18|, |v19|, |v20|
	v_max3_f32 v42, |v21|, |v22|, |v23|
	v_max3_f32 v43, |v24|, |v25|, |v26|
	v_max3_f32 v44, |v27|, |v28|, |v29|
	v_max3_f32 v45, |v30|, |v31|, |v32|
	v_max3_f32 v41, v41, v42, |v33|
	v_max3_f32 v43, v43, v44, v45
	v_max_f32_e32 v41, v41, v43
	v_pk_add_f32 v[2:3], v[2:3], v[18:19]
	v_pk_add_f32 v[4:5], v[4:5], v[20:21]
	v_max_f32_dpp v41, v41, v41 quad_perm:[1,0,3,2] row_mask:0xf bank_mask:0xf
	v_pk_add_f32 v[6:7], v[6:7], v[22:23]
	v_pk_add_f32 v[8:9], v[8:9], v[24:25]
	v_max_f32_dpp v41, v41, v41 quad_perm:[2,3,0,1] row_mask:0xf bank_mask:0xf
	v_pk_add_f32 v[10:11], v[10:11], v[26:27]
	v_pk_add_f32 v[12:13], v[12:13], v[28:29]
	v_max_f32_dpp v41, v41, v41 row_half_mirror row_mask:0xf bank_mask:0xf
	v_pk_add_f32 v[14:15], v[14:15], v[30:31]
	v_pk_add_f32 v[16:17], v[16:17], v[32:33]
	v_max_f32_dpp v41, v41, v41 row_mirror row_mask:0xf bank_mask:0xf
	s_nop 1
	v_max_f32_dpp v41, v41, v41 row_bcast:15 row_mask:0xa bank_mask:0xf
	s_nop 1
	v_max_f32_dpp v41, v41, v41 row_bcast:31 row_mask:0xc bank_mask:0xf
	s_nop 1
	v_readlane_b32 s28, v41, 63
	s_nop 1
	v_div_scale_f32 v48, s[30:31], s28, s28, v47
	v_rcp_f32_e32 v49, v48
	s_nop 0
	v_fma_f32 v50, -v48, v49, 1.0
	v_fmac_f32_e32 v49, v50, v49
	v_mov_b32_e32 v50, s28
	v_div_scale_f32 v50, vcc, s32, v50, s32
	v_mul_f32_e32 v51, v50, v49
	v_fma_f32 v52, -v48, v51, v50
	v_fmac_f32_e32 v51, v52, v49
	v_fma_f32 v48, -v48, v51, v50
	v_div_fmas_f32 v48, v48, v49, v51
	v_div_fixup_f32 v48, v48, s28, v47
	v_cmp_gt_f32_e64 vcc, s28, 0
	v_writelane_b32 v40, s28, 2
	s_nop 0
	v_cndmask_b32_e32 v48, 0, v48, vcc
	v_fmaak_f32 v49, v18, v48, 0x4b400000
	v_fmaak_f32 v50, v19, v48, 0x4b400000
	v_fmaak_f32 v51, v20, v48, 0x4b400000
	v_fmaak_f32 v52, v21, v48, 0x4b400000
	v_perm_b32 v49, v50, v49, s33
	v_perm_b32 v51, v52, v51, s34
	v_or_b32_e32 v64, v49, v51
	v_fmaak_f32 v53, v22, v48, 0x4b400000
	v_fmaak_f32 v54, v23, v48, 0x4b400000
	v_fmaak_f32 v55, v24, v48, 0x4b400000
	v_fmaak_f32 v46, v25, v48, 0x4b400000
	v_perm_b32 v53, v54, v53, s33
	v_perm_b32 v55, v46, v55, s34
	v_or_b32_e32 v65, v53, v55
	v_fmaak_f32 v49, v26, v48, 0x4b400000
	v_fmaak_f32 v50, v27, v48, 0x4b400000
	v_fmaak_f32 v51, v28, v48, 0x4b400000
	v_fmaak_f32 v52, v29, v48, 0x4b400000
	v_perm_b32 v49, v50, v49, s33
	v_perm_b32 v51, v52, v51, s34
	v_or_b32_e32 v66, v49, v51
	v_fmaak_f32 v53, v30, v48, 0x4b400000
	v_fmaak_f32 v54, v31, v48, 0x4b400000
	v_fmaak_f32 v55, v32, v48, 0x4b400000
	v_fmaak_f32 v46, v33, v48, 0x4b400000
	v_perm_b32 v53, v54, v53, s33
	v_perm_b32 v55, v46, v55, s34
	v_or_b32_e32 v67, v53, v55
	s_waitcnt vmcnt(0)
	ds_read_b128 v[18:21], v38 offset:4096
	ds_read_b128 v[22:25], v38 offset:5120
	ds_read_b128 v[26:29], v38 offset:6144
	ds_read_b128 v[30:33], v38 offset:7168
	s_waitcnt lgkmcnt(0)
	s_mov_b32 m0, s35
	s_nop 0
	global_load_lds_dwordx4 v34, s[16:17] nt
	global_load_lds_dwordx4 v34, s[16:17] offset:1024 nt
	global_load_lds_dwordx4 v34, s[16:17] offset:2048 nt
	global_load_lds_dwordx4 v35, s[16:17] offset:3072 nt
	s_add_u32 s16, s16, 0x7d00
	s_addc_u32 s17, s17, 0
	v_cndmask_b32_e64 v30, 0, v30, s[18:19]
	v_cndmask_b32_e64 v31, 0, v31, s[18:19]
	v_cndmask_b32_e64 v32, 0, v32, s[18:19]
	v_cndmask_b32_e64 v33, 0, v33, s[18:19]
	v_max3_f32 v41, |v18|, |v19|, |v20|
	v_max3_f32 v42, |v21|, |v22|, |v23|
	v_max3_f32 v43, |v24|, |v25|, |v26|
	v_max3_f32 v44, |v27|, |v28|, |v29|
	v_max3_f32 v45, |v30|, |v31|, |v32|
	v_max3_f32 v41, v41, v42, |v33|
	v_max3_f32 v43, v43, v44, v45
	v_max_f32_e32 v41, v41, v43
	v_pk_add_f32 v[2:3], v[2:3], v[18:19]
	v_pk_add_f32 v[4:5], v[4:5], v[20:21]
	v_max_f32_dpp v41, v41, v41 quad_perm:[1,0,3,2] row_mask:0xf bank_mask:0xf
	v_pk_add_f32 v[6:7], v[6:7], v[22:23]
	v_pk_add_f32 v[8:9], v[8:9], v[24:25]
	v_max_f32_dpp v41, v41, v41 quad_perm:[2,3,0,1] row_mask:0xf bank_mask:0xf
	v_pk_add_f32 v[10:11], v[10:11], v[26:27]
	v_pk_add_f32 v[12:13], v[12:13], v[28:29]
	v_max_f32_dpp v41, v41, v41 row_half_mirror row_mask:0xf bank_mask:0xf
	v_pk_add_f32 v[14:15], v[14:15], v[30:31]
	v_pk_add_f32 v[16:17], v[16:17], v[32:33]
	v_max_f32_dpp v41, v41, v41 row_mirror row_mask:0xf bank_mask:0xf
	s_nop 1
	v_max_f32_dpp v41, v41, v41 row_bcast:15 row_mask:0xa bank_mask:0xf
	s_nop 1
	v_max_f32_dpp v41, v41, v41 row_bcast:31 row_mask:0xc bank_mask:0xf
	s_nop 1
	v_readlane_b32 s28, v41, 63
	s_nop 1
	v_div_scale_f32 v48, s[30:31], s28, s28, v47
	v_rcp_f32_e32 v49, v48
	s_nop 0
	v_fma_f32 v50, -v48, v49, 1.0
	v_fmac_f32_e32 v49, v50, v49
	v_mov_b32_e32 v50, s28
	v_div_scale_f32 v50, vcc, s32, v50, s32
	v_mul_f32_e32 v51, v50, v49
	v_fma_f32 v52, -v48, v51, v50
	v_fmac_f32_e32 v51, v52, v49
	v_fma_f32 v48, -v48, v51, v50
	v_div_fmas_f32 v48, v48, v49, v51
	v_div_fixup_f32 v48, v48, s28, v47
	v_cmp_gt_f32_e64 vcc, s28, 0
	v_writelane_b32 v40, s28, 3
	s_nop 0
	v_cndmask_b32_e32 v48, 0, v48, vcc
	v_fmaak_f32 v49, v18, v48, 0x4b400000
	v_fmaak_f32 v50, v19, v48, 0x4b400000
	v_fmaak_f32 v51, v20, v48, 0x4b400000
	v_fmaak_f32 v52, v21, v48, 0x4b400000
	v_perm_b32 v49, v50, v49, s33
	v_perm_b32 v51, v52, v51, s34
	v_or_b32_e32 v68, v49, v51
	v_fmaak_f32 v53, v22, v48, 0x4b400000
	v_fmaak_f32 v54, v23, v48, 0x4b400000
	v_fmaak_f32 v55, v24, v48, 0x4b400000
	v_fmaak_f32 v46, v25, v48, 0x4b400000
	v_perm_b32 v53, v54, v53, s33
	v_perm_b32 v55, v46, v55, s34
	v_or_b32_e32 v69, v53, v55
	v_fmaak_f32 v49, v26, v48, 0x4b400000
	v_fmaak_f32 v50, v27, v48, 0x4b400000
	v_fmaak_f32 v51, v28, v48, 0x4b400000
	v_fmaak_f32 v52, v29, v48, 0x4b400000
	v_perm_b32 v49, v50, v49, s33
	v_perm_b32 v51, v52, v51, s34
	v_or_b32_e32 v70, v49, v51
	v_fmaak_f32 v53, v30, v48, 0x4b400000
	v_fmaak_f32 v54, v31, v48, 0x4b400000
	v_fmaak_f32 v55, v32, v48, 0x4b400000
	v_fmaak_f32 v46, v33, v48, 0x4b400000
	v_perm_b32 v53, v54, v53, s33
	v_perm_b32 v55, v46, v55, s34
	v_or_b32_e32 v71, v53, v55
	s_waitcnt vmcnt(0)
	ds_read_b128 v[18:21], v38 offset:0
	ds_read_b128 v[22:25], v38 offset:1024
	ds_read_b128 v[26:29], v38 offset:2048
	ds_read_b128 v[30:33], v38 offset:3072
	s_waitcnt lgkmcnt(0)
	s_mov_b32 m0, s36
	s_nop 0
	global_load_lds_dwordx4 v34, s[16:17] nt
	global_load_lds_dwordx4 v34, s[16:17] offset:1024 nt
	global_load_lds_dwordx4 v34, s[16:17] offset:2048 nt
	global_load_lds_dwordx4 v35, s[16:17] offset:3072 nt
	s_add_u32 s16, s16, 0x7d00
	s_addc_u32 s17, s17, 0
	v_cndmask_b32_e64 v30, 0, v30, s[18:19]
	v_cndmask_b32_e64 v31, 0, v31, s[18:19]
	v_cndmask_b32_e64 v32, 0, v32, s[18:19]
	v_cndmask_b32_e64 v33, 0, v33, s[18:19]
	v_max3_f32 v41, |v18|, |v19|, |v20|
	v_max3_f32 v42, |v21|, |v22|, |v23|
	v_max3_f32 v43, |v24|, |v25|, |v26|
	v_max3_f32 v44, |v27|, |v28|, |v29|
	v_max3_f32 v45, |v30|, |v31|, |v32|
	v_max3_f32 v41, v41, v42, |v33|
	v_max3_f32 v43, v43, v44, v45
	v_max_f32_e32 v41, v41, v43
	v_pk_add_f32 v[2:3], v[2:3], v[18:19]
	v_pk_add_f32 v[4:5], v[4:5], v[20:21]
	v_max_f32_dpp v41, v41, v41 quad_perm:[1,0,3,2] row_mask:0xf bank_mask:0xf
	v_pk_add_f32 v[6:7], v[6:7], v[22:23]
	v_pk_add_f32 v[8:9], v[8:9], v[24:25]
	v_max_f32_dpp v41, v41, v41 quad_perm:[2,3,0,1] row_mask:0xf bank_mask:0xf
	v_pk_add_f32 v[10:11], v[10:11], v[26:27]
	v_pk_add_f32 v[12:13], v[12:13], v[28:29]
	v_max_f32_dpp v41, v41, v41 row_half_mirror row_mask:0xf bank_mask:0xf
	v_pk_add_f32 v[14:15], v[14:15], v[30:31]
	v_pk_add_f32 v[16:17], v[16:17], v[32:33]
	v_max_f32_dpp v41, v41, v41 row_mirror row_mask:0xf bank_mask:0xf
	s_nop 1
	v_max_f32_dpp v41, v41, v41 row_bcast:15 row_mask:0xa bank_mask:0xf
	s_nop 1
	v_max_f32_dpp v41, v41, v41 row_bcast:31 row_mask:0xc bank_mask:0xf
	s_nop 1
	v_readlane_b32 s28, v41, 63
	s_nop 1
	v_div_scale_f32 v48, s[30:31], s28, s28, v47
	v_rcp_f32_e32 v49, v48
	s_nop 0
	v_fma_f32 v50, -v48, v49, 1.0
	v_fmac_f32_e32 v49, v50, v49
	v_mov_b32_e32 v50, s28
	v_div_scale_f32 v50, vcc, s32, v50, s32
	v_mul_f32_e32 v51, v50, v49
	v_fma_f32 v52, -v48, v51, v50
	v_fmac_f32_e32 v51, v52, v49
	v_fma_f32 v48, -v48, v51, v50
	v_div_fmas_f32 v48, v48, v49, v51
	v_div_fixup_f32 v48, v48, s28, v47
	v_cmp_gt_f32_e64 vcc, s28, 0
	v_writelane_b32 v40, s28, 4
	s_nop 0
	v_cndmask_b32_e32 v48, 0, v48, vcc
	v_fmaak_f32 v49, v18, v48, 0x4b400000
	v_fmaak_f32 v50, v19, v48, 0x4b400000
	v_fmaak_f32 v51, v20, v48, 0x4b400000
	v_fmaak_f32 v52, v21, v48, 0x4b400000
	v_perm_b32 v49, v50, v49, s33
	v_perm_b32 v51, v52, v51, s34
	v_or_b32_e32 v72, v49, v51
	v_fmaak_f32 v53, v22, v48, 0x4b400000
	v_fmaak_f32 v54, v23, v48, 0x4b400000
	v_fmaak_f32 v55, v24, v48, 0x4b400000
	v_fmaak_f32 v46, v25, v48, 0x4b400000
	v_perm_b32 v53, v54, v53, s33
	v_perm_b32 v55, v46, v55, s34
	v_or_b32_e32 v73, v53, v55
	v_fmaak_f32 v49, v26, v48, 0x4b400000
	v_fmaak_f32 v50, v27, v48, 0x4b400000
	v_fmaak_f32 v51, v28, v48, 0x4b400000
	v_fmaak_f32 v52, v29, v48, 0x4b400000
	v_perm_b32 v49, v50, v49, s33
	v_perm_b32 v51, v52, v51, s34
	v_or_b32_e32 v74, v49, v51
	v_fmaak_f32 v53, v30, v48, 0x4b400000
	v_fmaak_f32 v54, v31, v48, 0x4b400000
	v_fmaak_f32 v55, v32, v48, 0x4b400000
	v_fmaak_f32 v46, v33, v48, 0x4b400000
	v_perm_b32 v53, v54, v53, s33
	v_perm_b32 v55, v46, v55, s34
	v_or_b32_e32 v75, v53, v55
	s_waitcnt vmcnt(0)
	ds_read_b128 v[18:21], v38 offset:4096
	ds_read_b128 v[22:25], v38 offset:5120
	ds_read_b128 v[26:29], v38 offset:6144
	ds_read_b128 v[30:33], v38 offset:7168
	s_waitcnt lgkmcnt(0)
	s_mov_b32 m0, s35
	s_nop 0
	global_load_lds_dwordx4 v34, s[16:17] nt
	global_load_lds_dwordx4 v34, s[16:17] offset:1024 nt
	global_load_lds_dwordx4 v34, s[16:17] offset:2048 nt
	global_load_lds_dwordx4 v35, s[16:17] offset:3072 nt
	s_add_u32 s16, s16, 0x7d00
	s_addc_u32 s17, s17, 0
	v_cndmask_b32_e64 v30, 0, v30, s[18:19]
	v_cndmask_b32_e64 v31, 0, v31, s[18:19]
	v_cndmask_b32_e64 v32, 0, v32, s[18:19]
	v_cndmask_b32_e64 v33, 0, v33, s[18:19]
	v_max3_f32 v41, |v18|, |v19|, |v20|
	v_max3_f32 v42, |v21|, |v22|, |v23|
	v_max3_f32 v43, |v24|, |v25|, |v26|
	v_max3_f32 v44, |v27|, |v28|, |v29|
	v_max3_f32 v45, |v30|, |v31|, |v32|
	v_max3_f32 v41, v41, v42, |v33|
	v_max3_f32 v43, v43, v44, v45
	v_max_f32_e32 v41, v41, v43
	v_pk_add_f32 v[2:3], v[2:3], v[18:19]
	v_pk_add_f32 v[4:5], v[4:5], v[20:21]
	v_max_f32_dpp v41, v41, v41 quad_perm:[1,0,3,2] row_mask:0xf bank_mask:0xf
	v_pk_add_f32 v[6:7], v[6:7], v[22:23]
	v_pk_add_f32 v[8:9], v[8:9], v[24:25]
	v_max_f32_dpp v41, v41, v41 quad_perm:[2,3,0,1] row_mask:0xf bank_mask:0xf
	v_pk_add_f32 v[10:11], v[10:11], v[26:27]
	v_pk_add_f32 v[12:13], v[12:13], v[28:29]
	v_max_f32_dpp v41, v41, v41 row_half_mirror row_mask:0xf bank_mask:0xf
	v_pk_add_f32 v[14:15], v[14:15], v[30:31]
	v_pk_add_f32 v[16:17], v[16:17], v[32:33]
	v_max_f32_dpp v41, v41, v41 row_mirror row_mask:0xf bank_mask:0xf
	s_nop 1
	v_max_f32_dpp v41, v41, v41 row_bcast:15 row_mask:0xa bank_mask:0xf
	s_nop 1
	v_max_f32_dpp v41, v41, v41 row_bcast:31 row_mask:0xc bank_mask:0xf
	s_nop 1
	v_readlane_b32 s28, v41, 63
	s_nop 1
	v_div_scale_f32 v48, s[30:31], s28, s28, v47
	v_rcp_f32_e32 v49, v48
	s_nop 0
	v_fma_f32 v50, -v48, v49, 1.0
	v_fmac_f32_e32 v49, v50, v49
	v_mov_b32_e32 v50, s28
	v_div_scale_f32 v50, vcc, s32, v50, s32
	v_mul_f32_e32 v51, v50, v49
	v_fma_f32 v52, -v48, v51, v50
	v_fmac_f32_e32 v51, v52, v49
	v_fma_f32 v48, -v48, v51, v50
	v_div_fmas_f32 v48, v48, v49, v51
	v_div_fixup_f32 v48, v48, s28, v47
	v_cmp_gt_f32_e64 vcc, s28, 0
	v_writelane_b32 v40, s28, 5
	s_nop 0
	v_cndmask_b32_e32 v48, 0, v48, vcc
	v_fmaak_f32 v49, v18, v48, 0x4b400000
	v_fmaak_f32 v50, v19, v48, 0x4b400000
	v_fmaak_f32 v51, v20, v48, 0x4b400000
	v_fmaak_f32 v52, v21, v48, 0x4b400000
	v_perm_b32 v49, v50, v49, s33
	v_perm_b32 v51, v52, v51, s34
	v_or_b32_e32 v76, v49, v51
	v_fmaak_f32 v53, v22, v48, 0x4b400000
	v_fmaak_f32 v54, v23, v48, 0x4b400000
	v_fmaak_f32 v55, v24, v48, 0x4b400000
	v_fmaak_f32 v46, v25, v48, 0x4b400000
	v_perm_b32 v53, v54, v53, s33
	v_perm_b32 v55, v46, v55, s34
	v_or_b32_e32 v77, v53, v55
	v_fmaak_f32 v49, v26, v48, 0x4b400000
	v_fmaak_f32 v50, v27, v48, 0x4b400000
	v_fmaak_f32 v51, v28, v48, 0x4b400000
	v_fmaak_f32 v52, v29, v48, 0x4b400000
	v_perm_b32 v49, v50, v49, s33
	v_perm_b32 v51, v52, v51, s34
	v_or_b32_e32 v78, v49, v51
	v_fmaak_f32 v53, v30, v48, 0x4b400000
	v_fmaak_f32 v54, v31, v48, 0x4b400000
	v_fmaak_f32 v55, v32, v48, 0x4b400000
	v_fmaak_f32 v46, v33, v48, 0x4b400000
	v_perm_b32 v53, v54, v53, s33
	v_perm_b32 v55, v46, v55, s34
	v_or_b32_e32 v79, v53, v55
	s_waitcnt vmcnt(0)
	ds_read_b128 v[18:21], v38 offset:0
	ds_read_b128 v[22:25], v38 offset:1024
	ds_read_b128 v[26:29], v38 offset:2048
	ds_read_b128 v[30:33], v38 offset:3072
	s_waitcnt lgkmcnt(0)
	s_mov_b32 m0, s36
	s_nop 0
	global_load_lds_dwordx4 v34, s[16:17] nt
	global_load_lds_dwordx4 v34, s[16:17] offset:1024 nt
	global_load_lds_dwordx4 v34, s[16:17] offset:2048 nt
	global_load_lds_dwordx4 v35, s[16:17] offset:3072 nt
	s_add_u32 s16, s16, 0x7d00
	s_addc_u32 s17, s17, 0
	v_cndmask_b32_e64 v30, 0, v30, s[18:19]
	v_cndmask_b32_e64 v31, 0, v31, s[18:19]
	v_cndmask_b32_e64 v32, 0, v32, s[18:19]
	v_cndmask_b32_e64 v33, 0, v33, s[18:19]
	v_max3_f32 v41, |v18|, |v19|, |v20|
	v_max3_f32 v42, |v21|, |v22|, |v23|
	v_max3_f32 v43, |v24|, |v25|, |v26|
	v_max3_f32 v44, |v27|, |v28|, |v29|
	v_max3_f32 v45, |v30|, |v31|, |v32|
	v_max3_f32 v41, v41, v42, |v33|
	v_max3_f32 v43, v43, v44, v45
	v_max_f32_e32 v41, v41, v43
	v_pk_add_f32 v[2:3], v[2:3], v[18:19]
	v_pk_add_f32 v[4:5], v[4:5], v[20:21]
	v_max_f32_dpp v41, v41, v41 quad_perm:[1,0,3,2] row_mask:0xf bank_mask:0xf
	v_pk_add_f32 v[6:7], v[6:7], v[22:23]
	v_pk_add_f32 v[8:9], v[8:9], v[24:25]
	v_max_f32_dpp v41, v41, v41 quad_perm:[2,3,0,1] row_mask:0xf bank_mask:0xf
	v_pk_add_f32 v[10:11], v[10:11], v[26:27]
	v_pk_add_f32 v[12:13], v[12:13], v[28:29]
	v_max_f32_dpp v41, v41, v41 row_half_mirror row_mask:0xf bank_mask:0xf
	v_pk_add_f32 v[14:15], v[14:15], v[30:31]
	v_pk_add_f32 v[16:17], v[16:17], v[32:33]
	v_max_f32_dpp v41, v41, v41 row_mirror row_mask:0xf bank_mask:0xf
	s_nop 1
	v_max_f32_dpp v41, v41, v41 row_bcast:15 row_mask:0xa bank_mask:0xf
	s_nop 1
	v_max_f32_dpp v41, v41, v41 row_bcast:31 row_mask:0xc bank_mask:0xf
	s_nop 1
	v_readlane_b32 s28, v41, 63
	s_nop 1
	v_div_scale_f32 v48, s[30:31], s28, s28, v47
	v_rcp_f32_e32 v49, v48
	s_nop 0
	v_fma_f32 v50, -v48, v49, 1.0
	v_fmac_f32_e32 v49, v50, v49
	v_mov_b32_e32 v50, s28
	v_div_scale_f32 v50, vcc, s32, v50, s32
	v_mul_f32_e32 v51, v50, v49
	v_fma_f32 v52, -v48, v51, v50
	v_fmac_f32_e32 v51, v52, v49
	v_fma_f32 v48, -v48, v51, v50
	v_div_fmas_f32 v48, v48, v49, v51
	v_div_fixup_f32 v48, v48, s28, v47
	v_cmp_gt_f32_e64 vcc, s28, 0
	v_writelane_b32 v40, s28, 6
	s_nop 0
	v_cndmask_b32_e32 v48, 0, v48, vcc
	v_fmaak_f32 v49, v18, v48, 0x4b400000
	v_fmaak_f32 v50, v19, v48, 0x4b400000
	v_fmaak_f32 v51, v20, v48, 0x4b400000
	v_fmaak_f32 v52, v21, v48, 0x4b400000
	v_perm_b32 v49, v50, v49, s33
	v_perm_b32 v51, v52, v51, s34
	v_or_b32_e32 v80, v49, v51
	v_fmaak_f32 v53, v22, v48, 0x4b400000
	v_fmaak_f32 v54, v23, v48, 0x4b400000
	v_fmaak_f32 v55, v24, v48, 0x4b400000
	v_fmaak_f32 v46, v25, v48, 0x4b400000
	v_perm_b32 v53, v54, v53, s33
	v_perm_b32 v55, v46, v55, s34
	v_or_b32_e32 v81, v53, v55
	v_fmaak_f32 v49, v26, v48, 0x4b400000
	v_fmaak_f32 v50, v27, v48, 0x4b400000
	v_fmaak_f32 v51, v28, v48, 0x4b400000
	v_fmaak_f32 v52, v29, v48, 0x4b400000
	v_perm_b32 v49, v50, v49, s33
	v_perm_b32 v51, v52, v51, s34
	v_or_b32_e32 v82, v49, v51
	v_fmaak_f32 v53, v30, v48, 0x4b400000
	v_fmaak_f32 v54, v31, v48, 0x4b400000
	v_fmaak_f32 v55, v32, v48, 0x4b400000
	v_fmaak_f32 v46, v33, v48, 0x4b400000
	v_perm_b32 v53, v54, v53, s33
	v_perm_b32 v55, v46, v55, s34
	v_or_b32_e32 v83, v53, v55
	s_waitcnt vmcnt(0)
	ds_read_b128 v[18:21], v38 offset:4096
	ds_read_b128 v[22:25], v38 offset:5120
	ds_read_b128 v[26:29], v38 offset:6144
	ds_read_b128 v[30:33], v38 offset:7168
	s_waitcnt lgkmcnt(0)
	s_mov_b32 m0, s35
	s_nop 0
	global_load_lds_dwordx4 v34, s[16:17] nt
	global_load_lds_dwordx4 v34, s[16:17] offset:1024 nt
	global_load_lds_dwordx4 v34, s[16:17] offset:2048 nt
	global_load_lds_dwordx4 v35, s[16:17] offset:3072 nt
	s_add_u32 s16, s16, 0x7d00
	s_addc_u32 s17, s17, 0
	v_cndmask_b32_e64 v30, 0, v30, s[18:19]
	v_cndmask_b32_e64 v31, 0, v31, s[18:19]
	v_cndmask_b32_e64 v32, 0, v32, s[18:19]
	v_cndmask_b32_e64 v33, 0, v33, s[18:19]
	v_max3_f32 v41, |v18|, |v19|, |v20|
	v_max3_f32 v42, |v21|, |v22|, |v23|
	v_max3_f32 v43, |v24|, |v25|, |v26|
	v_max3_f32 v44, |v27|, |v28|, |v29|
	v_max3_f32 v45, |v30|, |v31|, |v32|
	v_max3_f32 v41, v41, v42, |v33|
	v_max3_f32 v43, v43, v44, v45
	v_max_f32_e32 v41, v41, v43
	v_pk_add_f32 v[2:3], v[2:3], v[18:19]
	v_pk_add_f32 v[4:5], v[4:5], v[20:21]
	v_max_f32_dpp v41, v41, v41 quad_perm:[1,0,3,2] row_mask:0xf bank_mask:0xf
	v_pk_add_f32 v[6:7], v[6:7], v[22:23]
	v_pk_add_f32 v[8:9], v[8:9], v[24:25]
	v_max_f32_dpp v41, v41, v41 quad_perm:[2,3,0,1] row_mask:0xf bank_mask:0xf
	v_pk_add_f32 v[10:11], v[10:11], v[26:27]
	v_pk_add_f32 v[12:13], v[12:13], v[28:29]
	v_max_f32_dpp v41, v41, v41 row_half_mirror row_mask:0xf bank_mask:0xf
	v_pk_add_f32 v[14:15], v[14:15], v[30:31]
	v_pk_add_f32 v[16:17], v[16:17], v[32:33]
	v_max_f32_dpp v41, v41, v41 row_mirror row_mask:0xf bank_mask:0xf
	s_nop 1
	v_max_f32_dpp v41, v41, v41 row_bcast:15 row_mask:0xa bank_mask:0xf
	s_nop 1
	v_max_f32_dpp v41, v41, v41 row_bcast:31 row_mask:0xc bank_mask:0xf
	s_nop 1
	v_readlane_b32 s28, v41, 63
	s_nop 1
	v_div_scale_f32 v48, s[30:31], s28, s28, v47
	v_rcp_f32_e32 v49, v48
	s_nop 0
	v_fma_f32 v50, -v48, v49, 1.0
	v_fmac_f32_e32 v49, v50, v49
	v_mov_b32_e32 v50, s28
	v_div_scale_f32 v50, vcc, s32, v50, s32
	v_mul_f32_e32 v51, v50, v49
	v_fma_f32 v52, -v48, v51, v50
	v_fmac_f32_e32 v51, v52, v49
	v_fma_f32 v48, -v48, v51, v50
	v_div_fmas_f32 v48, v48, v49, v51
	v_div_fixup_f32 v48, v48, s28, v47
	v_cmp_gt_f32_e64 vcc, s28, 0
	v_writelane_b32 v40, s28, 7
	s_nop 0
	v_cndmask_b32_e32 v48, 0, v48, vcc
	v_fmaak_f32 v49, v18, v48, 0x4b400000
	v_fmaak_f32 v50, v19, v48, 0x4b400000
	v_fmaak_f32 v51, v20, v48, 0x4b400000
	v_fmaak_f32 v52, v21, v48, 0x4b400000
	v_perm_b32 v49, v50, v49, s33
	v_perm_b32 v51, v52, v51, s34
	v_or_b32_e32 v84, v49, v51
	v_fmaak_f32 v53, v22, v48, 0x4b400000
	v_fmaak_f32 v54, v23, v48, 0x4b400000
	v_fmaak_f32 v55, v24, v48, 0x4b400000
	v_fmaak_f32 v46, v25, v48, 0x4b400000
	v_perm_b32 v53, v54, v53, s33
	v_perm_b32 v55, v46, v55, s34
	v_or_b32_e32 v85, v53, v55
	v_fmaak_f32 v49, v26, v48, 0x4b400000
	v_fmaak_f32 v50, v27, v48, 0x4b400000
	v_fmaak_f32 v51, v28, v48, 0x4b400000
	v_fmaak_f32 v52, v29, v48, 0x4b400000
	v_perm_b32 v49, v50, v49, s33
	v_perm_b32 v51, v52, v51, s34
	v_or_b32_e32 v86, v49, v51
	v_fmaak_f32 v53, v30, v48, 0x4b400000
	v_fmaak_f32 v54, v31, v48, 0x4b400000
	v_fmaak_f32 v55, v32, v48, 0x4b400000
	v_fmaak_f32 v46, v33, v48, 0x4b400000
	v_perm_b32 v53, v54, v53, s33
	v_perm_b32 v55, v46, v55, s34
	v_or_b32_e32 v87, v53, v55
	s_waitcnt vmcnt(0)
	ds_read_b128 v[18:21], v38 offset:0
	ds_read_b128 v[22:25], v38 offset:1024
	ds_read_b128 v[26:29], v38 offset:2048
	ds_read_b128 v[30:33], v38 offset:3072
	s_waitcnt lgkmcnt(0)
	s_mov_b32 m0, s36
	s_nop 0
	global_load_lds_dwordx4 v34, s[16:17] nt
	global_load_lds_dwordx4 v34, s[16:17] offset:1024 nt
	global_load_lds_dwordx4 v34, s[16:17] offset:2048 nt
	global_load_lds_dwordx4 v35, s[16:17] offset:3072 nt
	s_add_u32 s16, s16, 0x7d00
	s_addc_u32 s17, s17, 0
	v_cndmask_b32_e64 v30, 0, v30, s[18:19]
	v_cndmask_b32_e64 v31, 0, v31, s[18:19]
	v_cndmask_b32_e64 v32, 0, v32, s[18:19]
	v_cndmask_b32_e64 v33, 0, v33, s[18:19]
	v_max3_f32 v41, |v18|, |v19|, |v20|
	v_max3_f32 v42, |v21|, |v22|, |v23|
	v_max3_f32 v43, |v24|, |v25|, |v26|
	v_max3_f32 v44, |v27|, |v28|, |v29|
	v_max3_f32 v45, |v30|, |v31|, |v32|
	v_max3_f32 v41, v41, v42, |v33|
	v_max3_f32 v43, v43, v44, v45
	v_max_f32_e32 v41, v41, v43
	v_pk_add_f32 v[2:3], v[2:3], v[18:19]
	v_pk_add_f32 v[4:5], v[4:5], v[20:21]
	v_max_f32_dpp v41, v41, v41 quad_perm:[1,0,3,2] row_mask:0xf bank_mask:0xf
	v_pk_add_f32 v[6:7], v[6:7], v[22:23]
	v_pk_add_f32 v[8:9], v[8:9], v[24:25]
	v_max_f32_dpp v41, v41, v41 quad_perm:[2,3,0,1] row_mask:0xf bank_mask:0xf
	v_pk_add_f32 v[10:11], v[10:11], v[26:27]
	v_pk_add_f32 v[12:13], v[12:13], v[28:29]
	v_max_f32_dpp v41, v41, v41 row_half_mirror row_mask:0xf bank_mask:0xf
	v_pk_add_f32 v[14:15], v[14:15], v[30:31]
	v_pk_add_f32 v[16:17], v[16:17], v[32:33]
	v_max_f32_dpp v41, v41, v41 row_mirror row_mask:0xf bank_mask:0xf
	s_nop 1
	v_max_f32_dpp v41, v41, v41 row_bcast:15 row_mask:0xa bank_mask:0xf
	s_nop 1
	v_max_f32_dpp v41, v41, v41 row_bcast:31 row_mask:0xc bank_mask:0xf
	s_nop 1
	v_readlane_b32 s28, v41, 63
	s_nop 1
	v_div_scale_f32 v48, s[30:31], s28, s28, v47
	v_rcp_f32_e32 v49, v48
	s_nop 0
	v_fma_f32 v50, -v48, v49, 1.0
	v_fmac_f32_e32 v49, v50, v49
	v_mov_b32_e32 v50, s28
	v_div_scale_f32 v50, vcc, s32, v50, s32
	v_mul_f32_e32 v51, v50, v49
	v_fma_f32 v52, -v48, v51, v50
	v_fmac_f32_e32 v51, v52, v49
	v_fma_f32 v48, -v48, v51, v50
	v_div_fmas_f32 v48, v48, v49, v51
	v_div_fixup_f32 v48, v48, s28, v47
	v_cmp_gt_f32_e64 vcc, s28, 0
	v_writelane_b32 v40, s28, 8
	s_nop 0
	v_cndmask_b32_e32 v48, 0, v48, vcc
	v_fmaak_f32 v49, v18, v48, 0x4b400000
	v_fmaak_f32 v50, v19, v48, 0x4b400000
	v_fmaak_f32 v51, v20, v48, 0x4b400000
	v_fmaak_f32 v52, v21, v48, 0x4b400000
	v_perm_b32 v49, v50, v49, s33
	v_perm_b32 v51, v52, v51, s34
	v_or_b32_e32 v88, v49, v51
	v_fmaak_f32 v53, v22, v48, 0x4b400000
	v_fmaak_f32 v54, v23, v48, 0x4b400000
	v_fmaak_f32 v55, v24, v48, 0x4b400000
	v_fmaak_f32 v46, v25, v48, 0x4b400000
	v_perm_b32 v53, v54, v53, s33
	v_perm_b32 v55, v46, v55, s34
	v_or_b32_e32 v89, v53, v55
	v_fmaak_f32 v49, v26, v48, 0x4b400000
	v_fmaak_f32 v50, v27, v48, 0x4b400000
	v_fmaak_f32 v51, v28, v48, 0x4b400000
	v_fmaak_f32 v52, v29, v48, 0x4b400000
	v_perm_b32 v49, v50, v49, s33
	v_perm_b32 v51, v52, v51, s34
	v_or_b32_e32 v90, v49, v51
	v_fmaak_f32 v53, v30, v48, 0x4b400000
	v_fmaak_f32 v54, v31, v48, 0x4b400000
	v_fmaak_f32 v55, v32, v48, 0x4b400000
	v_fmaak_f32 v46, v33, v48, 0x4b400000
	v_perm_b32 v53, v54, v53, s33
	v_perm_b32 v55, v46, v55, s34
	v_or_b32_e32 v91, v53, v55
	s_waitcnt vmcnt(0)
	ds_read_b128 v[18:21], v38 offset:4096
	ds_read_b128 v[22:25], v38 offset:5120
	ds_read_b128 v[26:29], v38 offset:6144
	ds_read_b128 v[30:33], v38 offset:7168
	s_waitcnt lgkmcnt(0)
	s_mov_b32 m0, s35
	s_nop 0
	global_load_lds_dwordx4 v34, s[16:17] nt
	global_load_lds_dwordx4 v34, s[16:17] offset:1024 nt
	global_load_lds_dwordx4 v34, s[16:17] offset:2048 nt
	global_load_lds_dwordx4 v35, s[16:17] offset:3072 nt
	s_add_u32 s16, s16, 0x7d00
	s_addc_u32 s17, s17, 0
	v_cndmask_b32_e64 v30, 0, v30, s[18:19]
	v_cndmask_b32_e64 v31, 0, v31, s[18:19]
	v_cndmask_b32_e64 v32, 0, v32, s[18:19]
	v_cndmask_b32_e64 v33, 0, v33, s[18:19]
	v_max3_f32 v41, |v18|, |v19|, |v20|
	v_max3_f32 v42, |v21|, |v22|, |v23|
	v_max3_f32 v43, |v24|, |v25|, |v26|
	v_max3_f32 v44, |v27|, |v28|, |v29|
	v_max3_f32 v45, |v30|, |v31|, |v32|
	v_max3_f32 v41, v41, v42, |v33|
	v_max3_f32 v43, v43, v44, v45
	v_max_f32_e32 v41, v41, v43
	v_pk_add_f32 v[2:3], v[2:3], v[18:19]
	v_pk_add_f32 v[4:5], v[4:5], v[20:21]
	v_max_f32_dpp v41, v41, v41 quad_perm:[1,0,3,2] row_mask:0xf bank_mask:0xf
	v_pk_add_f32 v[6:7], v[6:7], v[22:23]
	v_pk_add_f32 v[8:9], v[8:9], v[24:25]
	v_max_f32_dpp v41, v41, v41 quad_perm:[2,3,0,1] row_mask:0xf bank_mask:0xf
	v_pk_add_f32 v[10:11], v[10:11], v[26:27]
	v_pk_add_f32 v[12:13], v[12:13], v[28:29]
	v_max_f32_dpp v41, v41, v41 row_half_mirror row_mask:0xf bank_mask:0xf
	v_pk_add_f32 v[14:15], v[14:15], v[30:31]
	v_pk_add_f32 v[16:17], v[16:17], v[32:33]
	v_max_f32_dpp v41, v41, v41 row_mirror row_mask:0xf bank_mask:0xf
	s_nop 1
	v_max_f32_dpp v41, v41, v41 row_bcast:15 row_mask:0xa bank_mask:0xf
	s_nop 1
	v_max_f32_dpp v41, v41, v41 row_bcast:31 row_mask:0xc bank_mask:0xf
	s_nop 1
	v_readlane_b32 s28, v41, 63
	s_nop 1
	v_div_scale_f32 v48, s[30:31], s28, s28, v47
	v_rcp_f32_e32 v49, v48
	s_nop 0
	v_fma_f32 v50, -v48, v49, 1.0
	v_fmac_f32_e32 v49, v50, v49
	v_mov_b32_e32 v50, s28
	v_div_scale_f32 v50, vcc, s32, v50, s32
	v_mul_f32_e32 v51, v50, v49
	v_fma_f32 v52, -v48, v51, v50
	v_fmac_f32_e32 v51, v52, v49
	v_fma_f32 v48, -v48, v51, v50
	v_div_fmas_f32 v48, v48, v49, v51
	v_div_fixup_f32 v48, v48, s28, v47
	v_cmp_gt_f32_e64 vcc, s28, 0
	v_writelane_b32 v40, s28, 9
	s_nop 0
	v_cndmask_b32_e32 v48, 0, v48, vcc
	v_fmaak_f32 v49, v18, v48, 0x4b400000
	v_fmaak_f32 v50, v19, v48, 0x4b400000
	v_fmaak_f32 v51, v20, v48, 0x4b400000
	v_fmaak_f32 v52, v21, v48, 0x4b400000
	v_perm_b32 v49, v50, v49, s33
	v_perm_b32 v51, v52, v51, s34
	v_or_b32_e32 v92, v49, v51
	v_fmaak_f32 v53, v22, v48, 0x4b400000
	v_fmaak_f32 v54, v23, v48, 0x4b400000
	v_fmaak_f32 v55, v24, v48, 0x4b400000
	v_fmaak_f32 v46, v25, v48, 0x4b400000
	v_perm_b32 v53, v54, v53, s33
	v_perm_b32 v55, v46, v55, s34
	v_or_b32_e32 v93, v53, v55
	v_fmaak_f32 v49, v26, v48, 0x4b400000
	v_fmaak_f32 v50, v27, v48, 0x4b400000
	v_fmaak_f32 v51, v28, v48, 0x4b400000
	v_fmaak_f32 v52, v29, v48, 0x4b400000
	v_perm_b32 v49, v50, v49, s33
	v_perm_b32 v51, v52, v51, s34
	v_or_b32_e32 v94, v49, v51
	v_fmaak_f32 v53, v30, v48, 0x4b400000
	v_fmaak_f32 v54, v31, v48, 0x4b400000
	v_fmaak_f32 v55, v32, v48, 0x4b400000
	v_fmaak_f32 v46, v33, v48, 0x4b400000
	v_perm_b32 v53, v54, v53, s33
	v_perm_b32 v55, v46, v55, s34
	v_or_b32_e32 v95, v53, v55
	s_waitcnt vmcnt(0)
	ds_read_b128 v[18:21], v38 offset:0
	ds_read_b128 v[22:25], v38 offset:1024
	ds_read_b128 v[26:29], v38 offset:2048
	ds_read_b128 v[30:33], v38 offset:3072
	s_waitcnt lgkmcnt(0)
	s_mov_b32 m0, s36
	s_nop 0
	global_load_lds_dwordx4 v34, s[16:17] nt
	global_load_lds_dwordx4 v34, s[16:17] offset:1024 nt
	global_load_lds_dwordx4 v34, s[16:17] offset:2048 nt
	global_load_lds_dwordx4 v35, s[16:17] offset:3072 nt
	s_add_u32 s16, s16, 0x7d00
	s_addc_u32 s17, s17, 0
	v_cndmask_b32_e64 v30, 0, v30, s[18:19]
	v_cndmask_b32_e64 v31, 0, v31, s[18:19]
	v_cndmask_b32_e64 v32, 0, v32, s[18:19]
	v_cndmask_b32_e64 v33, 0, v33, s[18:19]
	v_max3_f32 v41, |v18|, |v19|, |v20|
	v_max3_f32 v42, |v21|, |v22|, |v23|
	v_max3_f32 v43, |v24|, |v25|, |v26|
	v_max3_f32 v44, |v27|, |v28|, |v29|
	v_max3_f32 v45, |v30|, |v31|, |v32|
	v_max3_f32 v41, v41, v42, |v33|
	v_max3_f32 v43, v43, v44, v45
	v_max_f32_e32 v41, v41, v43
	v_pk_add_f32 v[2:3], v[2:3], v[18:19]
	v_pk_add_f32 v[4:5], v[4:5], v[20:21]
	v_max_f32_dpp v41, v41, v41 quad_perm:[1,0,3,2] row_mask:0xf bank_mask:0xf
	v_pk_add_f32 v[6:7], v[6:7], v[22:23]
	v_pk_add_f32 v[8:9], v[8:9], v[24:25]
	v_max_f32_dpp v41, v41, v41 quad_perm:[2,3,0,1] row_mask:0xf bank_mask:0xf
	v_pk_add_f32 v[10:11], v[10:11], v[26:27]
	v_pk_add_f32 v[12:13], v[12:13], v[28:29]
	v_max_f32_dpp v41, v41, v41 row_half_mirror row_mask:0xf bank_mask:0xf
	v_pk_add_f32 v[14:15], v[14:15], v[30:31]
	v_pk_add_f32 v[16:17], v[16:17], v[32:33]
	v_max_f32_dpp v41, v41, v41 row_mirror row_mask:0xf bank_mask:0xf
	s_nop 1
	v_max_f32_dpp v41, v41, v41 row_bcast:15 row_mask:0xa bank_mask:0xf
	s_nop 1
	v_max_f32_dpp v41, v41, v41 row_bcast:31 row_mask:0xc bank_mask:0xf
	s_nop 1
	v_readlane_b32 s28, v41, 63
	s_nop 1
	v_div_scale_f32 v48, s[30:31], s28, s28, v47
	v_rcp_f32_e32 v49, v48
	s_nop 0
	v_fma_f32 v50, -v48, v49, 1.0
	v_fmac_f32_e32 v49, v50, v49
	v_mov_b32_e32 v50, s28
	v_div_scale_f32 v50, vcc, s32, v50, s32
	v_mul_f32_e32 v51, v50, v49
	v_fma_f32 v52, -v48, v51, v50
	v_fmac_f32_e32 v51, v52, v49
	v_fma_f32 v48, -v48, v51, v50
	v_div_fmas_f32 v48, v48, v49, v51
	v_div_fixup_f32 v48, v48, s28, v47
	v_cmp_gt_f32_e64 vcc, s28, 0
	v_writelane_b32 v40, s28, 10
	s_nop 0
	v_cndmask_b32_e32 v48, 0, v48, vcc
	v_fmaak_f32 v49, v18, v48, 0x4b400000
	v_fmaak_f32 v50, v19, v48, 0x4b400000
	v_fmaak_f32 v51, v20, v48, 0x4b400000
	v_fmaak_f32 v52, v21, v48, 0x4b400000
	v_perm_b32 v49, v50, v49, s33
	v_perm_b32 v51, v52, v51, s34
	v_or_b32_e32 v96, v49, v51
	v_fmaak_f32 v53, v22, v48, 0x4b400000
	v_fmaak_f32 v54, v23, v48, 0x4b400000
	v_fmaak_f32 v55, v24, v48, 0x4b400000
	v_fmaak_f32 v46, v25, v48, 0x4b400000
	v_perm_b32 v53, v54, v53, s33
	v_perm_b32 v55, v46, v55, s34
	v_or_b32_e32 v97, v53, v55
	v_fmaak_f32 v49, v26, v48, 0x4b400000
	v_fmaak_f32 v50, v27, v48, 0x4b400000
	v_fmaak_f32 v51, v28, v48, 0x4b400000
	v_fmaak_f32 v52, v29, v48, 0x4b400000
	v_perm_b32 v49, v50, v49, s33
	v_perm_b32 v51, v52, v51, s34
	v_or_b32_e32 v98, v49, v51
	v_fmaak_f32 v53, v30, v48, 0x4b400000
	v_fmaak_f32 v54, v31, v48, 0x4b400000
	v_fmaak_f32 v55, v32, v48, 0x4b400000
	v_fmaak_f32 v46, v33, v48, 0x4b400000
	v_perm_b32 v53, v54, v53, s33
	v_perm_b32 v55, v46, v55, s34
	v_or_b32_e32 v99, v53, v55
	s_waitcnt vmcnt(0)
	ds_read_b128 v[18:21], v38 offset:4096
	ds_read_b128 v[22:25], v38 offset:5120
	ds_read_b128 v[26:29], v38 offset:6144
	ds_read_b128 v[30:33], v38 offset:7168
	s_waitcnt lgkmcnt(0)
	s_mov_b32 m0, s35
	s_nop 0
	global_load_lds_dwordx4 v34, s[16:17] nt
	global_load_lds_dwordx4 v34, s[16:17] offset:1024 nt
	global_load_lds_dwordx4 v34, s[16:17] offset:2048 nt
	global_load_lds_dwordx4 v35, s[16:17] offset:3072 nt
	s_add_u32 s16, s16, 0x7d00
	s_addc_u32 s17, s17, 0
	v_cndmask_b32_e64 v30, 0, v30, s[18:19]
	v_cndmask_b32_e64 v31, 0, v31, s[18:19]
	v_cndmask_b32_e64 v32, 0, v32, s[18:19]
	v_cndmask_b32_e64 v33, 0, v33, s[18:19]
	v_max3_f32 v41, |v18|, |v19|, |v20|
	v_max3_f32 v42, |v21|, |v22|, |v23|
	v_max3_f32 v43, |v24|, |v25|, |v26|
	v_max3_f32 v44, |v27|, |v28|, |v29|
	v_max3_f32 v45, |v30|, |v31|, |v32|
	v_max3_f32 v41, v41, v42, |v33|
	v_max3_f32 v43, v43, v44, v45
	v_max_f32_e32 v41, v41, v43
	v_pk_add_f32 v[2:3], v[2:3], v[18:19]
	v_pk_add_f32 v[4:5], v[4:5], v[20:21]
	v_max_f32_dpp v41, v41, v41 quad_perm:[1,0,3,2] row_mask:0xf bank_mask:0xf
	v_pk_add_f32 v[6:7], v[6:7], v[22:23]
	v_pk_add_f32 v[8:9], v[8:9], v[24:25]
	v_max_f32_dpp v41, v41, v41 quad_perm:[2,3,0,1] row_mask:0xf bank_mask:0xf
	v_pk_add_f32 v[10:11], v[10:11], v[26:27]
	v_pk_add_f32 v[12:13], v[12:13], v[28:29]
	v_max_f32_dpp v41, v41, v41 row_half_mirror row_mask:0xf bank_mask:0xf
	v_pk_add_f32 v[14:15], v[14:15], v[30:31]
	v_pk_add_f32 v[16:17], v[16:17], v[32:33]
	v_max_f32_dpp v41, v41, v41 row_mirror row_mask:0xf bank_mask:0xf
	s_nop 1
	v_max_f32_dpp v41, v41, v41 row_bcast:15 row_mask:0xa bank_mask:0xf
	s_nop 1
	v_max_f32_dpp v41, v41, v41 row_bcast:31 row_mask:0xc bank_mask:0xf
	s_nop 1
	v_readlane_b32 s28, v41, 63
	s_nop 1
	v_div_scale_f32 v48, s[30:31], s28, s28, v47
	v_rcp_f32_e32 v49, v48
	s_nop 0
	v_fma_f32 v50, -v48, v49, 1.0
	v_fmac_f32_e32 v49, v50, v49
	v_mov_b32_e32 v50, s28
	v_div_scale_f32 v50, vcc, s32, v50, s32
	v_mul_f32_e32 v51, v50, v49
	v_fma_f32 v52, -v48, v51, v50
	v_fmac_f32_e32 v51, v52, v49
	v_fma_f32 v48, -v48, v51, v50
	v_div_fmas_f32 v48, v48, v49, v51
	v_div_fixup_f32 v48, v48, s28, v47
	v_cmp_gt_f32_e64 vcc, s28, 0
	v_writelane_b32 v40, s28, 11
	s_nop 0
	v_cndmask_b32_e32 v48, 0, v48, vcc
	v_fmaak_f32 v49, v18, v48, 0x4b400000
	v_fmaak_f32 v50, v19, v48, 0x4b400000
	v_fmaak_f32 v51, v20, v48, 0x4b400000
	v_fmaak_f32 v52, v21, v48, 0x4b400000
	v_perm_b32 v49, v50, v49, s33
	v_perm_b32 v51, v52, v51, s34
	v_or_b32_e32 v100, v49, v51
	v_fmaak_f32 v53, v22, v48, 0x4b400000
	v_fmaak_f32 v54, v23, v48, 0x4b400000
	v_fmaak_f32 v55, v24, v48, 0x4b400000
	v_fmaak_f32 v46, v25, v48, 0x4b400000
	v_perm_b32 v53, v54, v53, s33
	v_perm_b32 v55, v46, v55, s34
	v_or_b32_e32 v101, v53, v55
	v_fmaak_f32 v49, v26, v48, 0x4b400000
	v_fmaak_f32 v50, v27, v48, 0x4b400000
	v_fmaak_f32 v51, v28, v48, 0x4b400000
	v_fmaak_f32 v52, v29, v48, 0x4b400000
	v_perm_b32 v49, v50, v49, s33
	v_perm_b32 v51, v52, v51, s34
	v_or_b32_e32 v102, v49, v51
	v_fmaak_f32 v53, v30, v48, 0x4b400000
	v_fmaak_f32 v54, v31, v48, 0x4b400000
	v_fmaak_f32 v55, v32, v48, 0x4b400000
	v_fmaak_f32 v46, v33, v48, 0x4b400000
	v_perm_b32 v53, v54, v53, s33
	v_perm_b32 v55, v46, v55, s34
	v_or_b32_e32 v103, v53, v55
	s_waitcnt vmcnt(0)
	ds_read_b128 v[18:21], v38 offset:0
	ds_read_b128 v[22:25], v38 offset:1024
	ds_read_b128 v[26:29], v38 offset:2048
	ds_read_b128 v[30:33], v38 offset:3072
	s_waitcnt lgkmcnt(0)
	s_mov_b32 m0, s36
	s_nop 0
	global_load_lds_dwordx4 v34, s[16:17] nt
	global_load_lds_dwordx4 v34, s[16:17] offset:1024 nt
	global_load_lds_dwordx4 v34, s[16:17] offset:2048 nt
	global_load_lds_dwordx4 v35, s[16:17] offset:3072 nt
	s_add_u32 s16, s16, 0x7d00
	s_addc_u32 s17, s17, 0
	v_cndmask_b32_e64 v30, 0, v30, s[18:19]
	v_cndmask_b32_e64 v31, 0, v31, s[18:19]
	v_cndmask_b32_e64 v32, 0, v32, s[18:19]
	v_cndmask_b32_e64 v33, 0, v33, s[18:19]
	v_max3_f32 v41, |v18|, |v19|, |v20|
	v_max3_f32 v42, |v21|, |v22|, |v23|
	v_max3_f32 v43, |v24|, |v25|, |v26|
	v_max3_f32 v44, |v27|, |v28|, |v29|
	v_max3_f32 v45, |v30|, |v31|, |v32|
	v_max3_f32 v41, v41, v42, |v33|
	v_max3_f32 v43, v43, v44, v45
	v_max_f32_e32 v41, v41, v43
	v_pk_add_f32 v[2:3], v[2:3], v[18:19]
	v_pk_add_f32 v[4:5], v[4:5], v[20:21]
	v_max_f32_dpp v41, v41, v41 quad_perm:[1,0,3,2] row_mask:0xf bank_mask:0xf
	v_pk_add_f32 v[6:7], v[6:7], v[22:23]
	v_pk_add_f32 v[8:9], v[8:9], v[24:25]
	v_max_f32_dpp v41, v41, v41 quad_perm:[2,3,0,1] row_mask:0xf bank_mask:0xf
	v_pk_add_f32 v[10:11], v[10:11], v[26:27]
	v_pk_add_f32 v[12:13], v[12:13], v[28:29]
	v_max_f32_dpp v41, v41, v41 row_half_mirror row_mask:0xf bank_mask:0xf
	v_pk_add_f32 v[14:15], v[14:15], v[30:31]
	v_pk_add_f32 v[16:17], v[16:17], v[32:33]
	v_max_f32_dpp v41, v41, v41 row_mirror row_mask:0xf bank_mask:0xf
	s_nop 1
	v_max_f32_dpp v41, v41, v41 row_bcast:15 row_mask:0xa bank_mask:0xf
	s_nop 1
	v_max_f32_dpp v41, v41, v41 row_bcast:31 row_mask:0xc bank_mask:0xf
	s_nop 1
	v_readlane_b32 s28, v41, 63
	s_nop 1
	v_div_scale_f32 v48, s[30:31], s28, s28, v47
	v_rcp_f32_e32 v49, v48
	s_nop 0
	v_fma_f32 v50, -v48, v49, 1.0
	v_fmac_f32_e32 v49, v50, v49
	v_mov_b32_e32 v50, s28
	v_div_scale_f32 v50, vcc, s32, v50, s32
	v_mul_f32_e32 v51, v50, v49
	v_fma_f32 v52, -v48, v51, v50
	v_fmac_f32_e32 v51, v52, v49
	v_fma_f32 v48, -v48, v51, v50
	v_div_fmas_f32 v48, v48, v49, v51
	v_div_fixup_f32 v48, v48, s28, v47
	v_cmp_gt_f32_e64 vcc, s28, 0
	v_writelane_b32 v40, s28, 12
	s_nop 0
	v_cndmask_b32_e32 v48, 0, v48, vcc
	v_fmaak_f32 v49, v18, v48, 0x4b400000
	v_fmaak_f32 v50, v19, v48, 0x4b400000
	v_fmaak_f32 v51, v20, v48, 0x4b400000
	v_fmaak_f32 v52, v21, v48, 0x4b400000
	v_perm_b32 v49, v50, v49, s33
	v_perm_b32 v51, v52, v51, s34
	v_or_b32_e32 v104, v49, v51
	v_fmaak_f32 v53, v22, v48, 0x4b400000
	v_fmaak_f32 v54, v23, v48, 0x4b400000
	v_fmaak_f32 v55, v24, v48, 0x4b400000
	v_fmaak_f32 v46, v25, v48, 0x4b400000
	v_perm_b32 v53, v54, v53, s33
	v_perm_b32 v55, v46, v55, s34
	v_or_b32_e32 v105, v53, v55
	v_fmaak_f32 v49, v26, v48, 0x4b400000
	v_fmaak_f32 v50, v27, v48, 0x4b400000
	v_fmaak_f32 v51, v28, v48, 0x4b400000
	v_fmaak_f32 v52, v29, v48, 0x4b400000
	v_perm_b32 v49, v50, v49, s33
	v_perm_b32 v51, v52, v51, s34
	v_or_b32_e32 v106, v49, v51
	v_fmaak_f32 v53, v30, v48, 0x4b400000
	v_fmaak_f32 v54, v31, v48, 0x4b400000
	v_fmaak_f32 v55, v32, v48, 0x4b400000
	v_fmaak_f32 v46, v33, v48, 0x4b400000
	v_perm_b32 v53, v54, v53, s33
	v_perm_b32 v55, v46, v55, s34
	v_or_b32_e32 v107, v53, v55
	s_waitcnt vmcnt(0)
	ds_read_b128 v[18:21], v38 offset:4096
	ds_read_b128 v[22:25], v38 offset:5120
	ds_read_b128 v[26:29], v38 offset:6144
	ds_read_b128 v[30:33], v38 offset:7168
	s_waitcnt lgkmcnt(0)
	s_mov_b32 m0, s35
	s_nop 0
	global_load_lds_dwordx4 v34, s[16:17] nt
	global_load_lds_dwordx4 v34, s[16:17] offset:1024 nt
	global_load_lds_dwordx4 v34, s[16:17] offset:2048 nt
	global_load_lds_dwordx4 v35, s[16:17] offset:3072 nt
	s_add_u32 s16, s16, 0x7d00
	s_addc_u32 s17, s17, 0
	v_cndmask_b32_e64 v30, 0, v30, s[18:19]
	v_cndmask_b32_e64 v31, 0, v31, s[18:19]
	v_cndmask_b32_e64 v32, 0, v32, s[18:19]
	v_cndmask_b32_e64 v33, 0, v33, s[18:19]
	v_max3_f32 v41, |v18|, |v19|, |v20|
	v_max3_f32 v42, |v21|, |v22|, |v23|
	v_max3_f32 v43, |v24|, |v25|, |v26|
	v_max3_f32 v44, |v27|, |v28|, |v29|
	v_max3_f32 v45, |v30|, |v31|, |v32|
	v_max3_f32 v41, v41, v42, |v33|
	v_max3_f32 v43, v43, v44, v45
	v_max_f32_e32 v41, v41, v43
	v_pk_add_f32 v[2:3], v[2:3], v[18:19]
	v_pk_add_f32 v[4:5], v[4:5], v[20:21]
	v_max_f32_dpp v41, v41, v41 quad_perm:[1,0,3,2] row_mask:0xf bank_mask:0xf
	v_pk_add_f32 v[6:7], v[6:7], v[22:23]
	v_pk_add_f32 v[8:9], v[8:9], v[24:25]
	v_max_f32_dpp v41, v41, v41 quad_perm:[2,3,0,1] row_mask:0xf bank_mask:0xf
	v_pk_add_f32 v[10:11], v[10:11], v[26:27]
	v_pk_add_f32 v[12:13], v[12:13], v[28:29]
	v_max_f32_dpp v41, v41, v41 row_half_mirror row_mask:0xf bank_mask:0xf
	v_pk_add_f32 v[14:15], v[14:15], v[30:31]
	v_pk_add_f32 v[16:17], v[16:17], v[32:33]
	v_max_f32_dpp v41, v41, v41 row_mirror row_mask:0xf bank_mask:0xf
	s_nop 1
	v_max_f32_dpp v41, v41, v41 row_bcast:15 row_mask:0xa bank_mask:0xf
	s_nop 1
	v_max_f32_dpp v41, v41, v41 row_bcast:31 row_mask:0xc bank_mask:0xf
	s_nop 1
	v_readlane_b32 s28, v41, 63
	s_nop 1
	v_div_scale_f32 v48, s[30:31], s28, s28, v47
	v_rcp_f32_e32 v49, v48
	s_nop 0
	v_fma_f32 v50, -v48, v49, 1.0
	v_fmac_f32_e32 v49, v50, v49
	v_mov_b32_e32 v50, s28
	v_div_scale_f32 v50, vcc, s32, v50, s32
	v_mul_f32_e32 v51, v50, v49
	v_fma_f32 v52, -v48, v51, v50
	v_fmac_f32_e32 v51, v52, v49
	v_fma_f32 v48, -v48, v51, v50
	v_div_fmas_f32 v48, v48, v49, v51
	v_div_fixup_f32 v48, v48, s28, v47
	v_cmp_gt_f32_e64 vcc, s28, 0
	v_writelane_b32 v40, s28, 13
	s_nop 0
	v_cndmask_b32_e32 v48, 0, v48, vcc
	v_fmaak_f32 v49, v18, v48, 0x4b400000
	v_fmaak_f32 v50, v19, v48, 0x4b400000
	v_fmaak_f32 v51, v20, v48, 0x4b400000
	v_fmaak_f32 v52, v21, v48, 0x4b400000
	v_perm_b32 v49, v50, v49, s33
	v_perm_b32 v51, v52, v51, s34
	v_or_b32_e32 v108, v49, v51
	v_fmaak_f32 v53, v22, v48, 0x4b400000
	v_fmaak_f32 v54, v23, v48, 0x4b400000
	v_fmaak_f32 v55, v24, v48, 0x4b400000
	v_fmaak_f32 v46, v25, v48, 0x4b400000
	v_perm_b32 v53, v54, v53, s33
	v_perm_b32 v55, v46, v55, s34
	v_or_b32_e32 v109, v53, v55
	v_fmaak_f32 v49, v26, v48, 0x4b400000
	v_fmaak_f32 v50, v27, v48, 0x4b400000
	v_fmaak_f32 v51, v28, v48, 0x4b400000
	v_fmaak_f32 v52, v29, v48, 0x4b400000
	v_perm_b32 v49, v50, v49, s33
	v_perm_b32 v51, v52, v51, s34
	v_or_b32_e32 v110, v49, v51
	v_fmaak_f32 v53, v30, v48, 0x4b400000
	v_fmaak_f32 v54, v31, v48, 0x4b400000
	v_fmaak_f32 v55, v32, v48, 0x4b400000
	v_fmaak_f32 v46, v33, v48, 0x4b400000
	v_perm_b32 v53, v54, v53, s33
	v_perm_b32 v55, v46, v55, s34
	v_or_b32_e32 v111, v53, v55
	s_waitcnt vmcnt(0)
	ds_read_b128 v[18:21], v38 offset:0
	ds_read_b128 v[22:25], v38 offset:1024
	ds_read_b128 v[26:29], v38 offset:2048
	ds_read_b128 v[30:33], v38 offset:3072
	s_waitcnt lgkmcnt(0)
	s_mov_b32 m0, s36
	s_nop 0
	global_load_lds_dwordx4 v34, s[16:17] nt
	global_load_lds_dwordx4 v34, s[16:17] offset:1024 nt
	global_load_lds_dwordx4 v34, s[16:17] offset:2048 nt
	global_load_lds_dwordx4 v35, s[16:17] offset:3072 nt
	s_add_u32 s16, s16, 0x7d00
	s_addc_u32 s17, s17, 0
	v_cndmask_b32_e64 v30, 0, v30, s[18:19]
	v_cndmask_b32_e64 v31, 0, v31, s[18:19]
	v_cndmask_b32_e64 v32, 0, v32, s[18:19]
	v_cndmask_b32_e64 v33, 0, v33, s[18:19]
	v_max3_f32 v41, |v18|, |v19|, |v20|
	v_max3_f32 v42, |v21|, |v22|, |v23|
	v_max3_f32 v43, |v24|, |v25|, |v26|
	v_max3_f32 v44, |v27|, |v28|, |v29|
	v_max3_f32 v45, |v30|, |v31|, |v32|
	v_max3_f32 v41, v41, v42, |v33|
	v_max3_f32 v43, v43, v44, v45
	v_max_f32_e32 v41, v41, v43
	v_pk_add_f32 v[2:3], v[2:3], v[18:19]
	v_pk_add_f32 v[4:5], v[4:5], v[20:21]
	v_max_f32_dpp v41, v41, v41 quad_perm:[1,0,3,2] row_mask:0xf bank_mask:0xf
	v_pk_add_f32 v[6:7], v[6:7], v[22:23]
	v_pk_add_f32 v[8:9], v[8:9], v[24:25]
	v_max_f32_dpp v41, v41, v41 quad_perm:[2,3,0,1] row_mask:0xf bank_mask:0xf
	v_pk_add_f32 v[10:11], v[10:11], v[26:27]
	v_pk_add_f32 v[12:13], v[12:13], v[28:29]
	v_max_f32_dpp v41, v41, v41 row_half_mirror row_mask:0xf bank_mask:0xf
	v_pk_add_f32 v[14:15], v[14:15], v[30:31]
	v_pk_add_f32 v[16:17], v[16:17], v[32:33]
	v_max_f32_dpp v41, v41, v41 row_mirror row_mask:0xf bank_mask:0xf
	s_nop 1
	v_max_f32_dpp v41, v41, v41 row_bcast:15 row_mask:0xa bank_mask:0xf
	s_nop 1
	v_max_f32_dpp v41, v41, v41 row_bcast:31 row_mask:0xc bank_mask:0xf
	s_nop 1
	v_readlane_b32 s28, v41, 63
	s_nop 1
	v_div_scale_f32 v48, s[30:31], s28, s28, v47
	v_rcp_f32_e32 v49, v48
	s_nop 0
	v_fma_f32 v50, -v48, v49, 1.0
	v_fmac_f32_e32 v49, v50, v49
	v_mov_b32_e32 v50, s28
	v_div_scale_f32 v50, vcc, s32, v50, s32
	v_mul_f32_e32 v51, v50, v49
	v_fma_f32 v52, -v48, v51, v50
	v_fmac_f32_e32 v51, v52, v49
	v_fma_f32 v48, -v48, v51, v50
	v_div_fmas_f32 v48, v48, v49, v51
	v_div_fixup_f32 v48, v48, s28, v47
	v_cmp_gt_f32_e64 vcc, s28, 0
	v_writelane_b32 v40, s28, 14
	s_nop 0
	v_cndmask_b32_e32 v48, 0, v48, vcc
	v_fmaak_f32 v49, v18, v48, 0x4b400000
	v_fmaak_f32 v50, v19, v48, 0x4b400000
	v_fmaak_f32 v51, v20, v48, 0x4b400000
	v_fmaak_f32 v52, v21, v48, 0x4b400000
	v_perm_b32 v49, v50, v49, s33
	v_perm_b32 v51, v52, v51, s34
	v_or_b32_e32 v112, v49, v51
	v_fmaak_f32 v53, v22, v48, 0x4b400000
	v_fmaak_f32 v54, v23, v48, 0x4b400000
	v_fmaak_f32 v55, v24, v48, 0x4b400000
	v_fmaak_f32 v46, v25, v48, 0x4b400000
	v_perm_b32 v53, v54, v53, s33
	v_perm_b32 v55, v46, v55, s34
	v_or_b32_e32 v113, v53, v55
	v_fmaak_f32 v49, v26, v48, 0x4b400000
	v_fmaak_f32 v50, v27, v48, 0x4b400000
	v_fmaak_f32 v51, v28, v48, 0x4b400000
	v_fmaak_f32 v52, v29, v48, 0x4b400000
	v_perm_b32 v49, v50, v49, s33
	v_perm_b32 v51, v52, v51, s34
	v_or_b32_e32 v114, v49, v51
	v_fmaak_f32 v53, v30, v48, 0x4b400000
	v_fmaak_f32 v54, v31, v48, 0x4b400000
	v_fmaak_f32 v55, v32, v48, 0x4b400000
	v_fmaak_f32 v46, v33, v48, 0x4b400000
	v_perm_b32 v53, v54, v53, s33
	v_perm_b32 v55, v46, v55, s34
	v_or_b32_e32 v115, v53, v55
	s_waitcnt vmcnt(0)
	ds_read_b128 v[18:21], v38 offset:4096
	ds_read_b128 v[22:25], v38 offset:5120
	ds_read_b128 v[26:29], v38 offset:6144
	ds_read_b128 v[30:33], v38 offset:7168
	s_waitcnt lgkmcnt(0)
	s_mov_b32 m0, s35
	s_nop 0
	global_load_lds_dwordx4 v34, s[16:17] nt
	global_load_lds_dwordx4 v34, s[16:17] offset:1024 nt
	global_load_lds_dwordx4 v34, s[16:17] offset:2048 nt
	global_load_lds_dwordx4 v35, s[16:17] offset:3072 nt
	s_add_u32 s16, s16, 0x7d00
	s_addc_u32 s17, s17, 0
	v_cndmask_b32_e64 v30, 0, v30, s[18:19]
	v_cndmask_b32_e64 v31, 0, v31, s[18:19]
	v_cndmask_b32_e64 v32, 0, v32, s[18:19]
	v_cndmask_b32_e64 v33, 0, v33, s[18:19]
	v_max3_f32 v41, |v18|, |v19|, |v20|
	v_max3_f32 v42, |v21|, |v22|, |v23|
	v_max3_f32 v43, |v24|, |v25|, |v26|
	v_max3_f32 v44, |v27|, |v28|, |v29|
	v_max3_f32 v45, |v30|, |v31|, |v32|
	v_max3_f32 v41, v41, v42, |v33|
	v_max3_f32 v43, v43, v44, v45
	v_max_f32_e32 v41, v41, v43
	v_pk_add_f32 v[2:3], v[2:3], v[18:19]
	v_pk_add_f32 v[4:5], v[4:5], v[20:21]
	v_max_f32_dpp v41, v41, v41 quad_perm:[1,0,3,2] row_mask:0xf bank_mask:0xf
	v_pk_add_f32 v[6:7], v[6:7], v[22:23]
	v_pk_add_f32 v[8:9], v[8:9], v[24:25]
	v_max_f32_dpp v41, v41, v41 quad_perm:[2,3,0,1] row_mask:0xf bank_mask:0xf
	v_pk_add_f32 v[10:11], v[10:11], v[26:27]
	v_pk_add_f32 v[12:13], v[12:13], v[28:29]
	v_max_f32_dpp v41, v41, v41 row_half_mirror row_mask:0xf bank_mask:0xf
	v_pk_add_f32 v[14:15], v[14:15], v[30:31]
	v_pk_add_f32 v[16:17], v[16:17], v[32:33]
	v_max_f32_dpp v41, v41, v41 row_mirror row_mask:0xf bank_mask:0xf
	s_nop 1
	v_max_f32_dpp v41, v41, v41 row_bcast:15 row_mask:0xa bank_mask:0xf
	s_nop 1
	v_max_f32_dpp v41, v41, v41 row_bcast:31 row_mask:0xc bank_mask:0xf
	s_nop 1
	v_readlane_b32 s28, v41, 63
	s_nop 1
	v_div_scale_f32 v48, s[30:31], s28, s28, v47
	v_rcp_f32_e32 v49, v48
	s_nop 0
	v_fma_f32 v50, -v48, v49, 1.0
	v_fmac_f32_e32 v49, v50, v49
	v_mov_b32_e32 v50, s28
	v_div_scale_f32 v50, vcc, s32, v50, s32
	v_mul_f32_e32 v51, v50, v49
	v_fma_f32 v52, -v48, v51, v50
	v_fmac_f32_e32 v51, v52, v49
	v_fma_f32 v48, -v48, v51, v50
	v_div_fmas_f32 v48, v48, v49, v51
	v_div_fixup_f32 v48, v48, s28, v47
	v_cmp_gt_f32_e64 vcc, s28, 0
	v_writelane_b32 v40, s28, 15
	s_nop 0
	v_cndmask_b32_e32 v48, 0, v48, vcc
	v_fmaak_f32 v49, v18, v48, 0x4b400000
	v_fmaak_f32 v50, v19, v48, 0x4b400000
	v_fmaak_f32 v51, v20, v48, 0x4b400000
	v_fmaak_f32 v52, v21, v48, 0x4b400000
	v_perm_b32 v49, v50, v49, s33
	v_perm_b32 v51, v52, v51, s34
	v_or_b32_e32 v116, v49, v51
	v_fmaak_f32 v53, v22, v48, 0x4b400000
	v_fmaak_f32 v54, v23, v48, 0x4b400000
	v_fmaak_f32 v55, v24, v48, 0x4b400000
	v_fmaak_f32 v46, v25, v48, 0x4b400000
	v_perm_b32 v53, v54, v53, s33
	v_perm_b32 v55, v46, v55, s34
	v_or_b32_e32 v117, v53, v55
	v_fmaak_f32 v49, v26, v48, 0x4b400000
	v_fmaak_f32 v50, v27, v48, 0x4b400000
	v_fmaak_f32 v51, v28, v48, 0x4b400000
	v_fmaak_f32 v52, v29, v48, 0x4b400000
	v_perm_b32 v49, v50, v49, s33
	v_perm_b32 v51, v52, v51, s34
	v_or_b32_e32 v118, v49, v51
	v_fmaak_f32 v53, v30, v48, 0x4b400000
	v_fmaak_f32 v54, v31, v48, 0x4b400000
	v_fmaak_f32 v55, v32, v48, 0x4b400000
	v_fmaak_f32 v46, v33, v48, 0x4b400000
	v_perm_b32 v53, v54, v53, s33
	v_perm_b32 v55, v46, v55, s34
	v_or_b32_e32 v119, v53, v55
	s_waitcnt vmcnt(0)
	ds_read_b128 v[18:21], v38 offset:0
	ds_read_b128 v[22:25], v38 offset:1024
	ds_read_b128 v[26:29], v38 offset:2048
	ds_read_b128 v[30:33], v38 offset:3072
	s_waitcnt lgkmcnt(0)
	s_mov_b32 m0, s36
	s_nop 0
	global_load_lds_dwordx4 v34, s[16:17] nt
	global_load_lds_dwordx4 v34, s[16:17] offset:1024 nt
	global_load_lds_dwordx4 v34, s[16:17] offset:2048 nt
	global_load_lds_dwordx4 v35, s[16:17] offset:3072 nt
	s_add_u32 s16, s16, 0x7d00
	s_addc_u32 s17, s17, 0
	v_cndmask_b32_e64 v30, 0, v30, s[18:19]
	v_cndmask_b32_e64 v31, 0, v31, s[18:19]
	v_cndmask_b32_e64 v32, 0, v32, s[18:19]
	v_cndmask_b32_e64 v33, 0, v33, s[18:19]
	v_max3_f32 v41, |v18|, |v19|, |v20|
	v_max3_f32 v42, |v21|, |v22|, |v23|
	v_max3_f32 v43, |v24|, |v25|, |v26|
	v_max3_f32 v44, |v27|, |v28|, |v29|
	v_max3_f32 v45, |v30|, |v31|, |v32|
	v_max3_f32 v41, v41, v42, |v33|
	v_max3_f32 v43, v43, v44, v45
	v_max_f32_e32 v41, v41, v43
	v_pk_add_f32 v[2:3], v[2:3], v[18:19]
	v_pk_add_f32 v[4:5], v[4:5], v[20:21]
	v_max_f32_dpp v41, v41, v41 quad_perm:[1,0,3,2] row_mask:0xf bank_mask:0xf
	v_pk_add_f32 v[6:7], v[6:7], v[22:23]
	v_pk_add_f32 v[8:9], v[8:9], v[24:25]
	v_max_f32_dpp v41, v41, v41 quad_perm:[2,3,0,1] row_mask:0xf bank_mask:0xf
	v_pk_add_f32 v[10:11], v[10:11], v[26:27]
	v_pk_add_f32 v[12:13], v[12:13], v[28:29]
	v_max_f32_dpp v41, v41, v41 row_half_mirror row_mask:0xf bank_mask:0xf
	v_pk_add_f32 v[14:15], v[14:15], v[30:31]
	v_pk_add_f32 v[16:17], v[16:17], v[32:33]
	v_max_f32_dpp v41, v41, v41 row_mirror row_mask:0xf bank_mask:0xf
	s_nop 1
	v_max_f32_dpp v41, v41, v41 row_bcast:15 row_mask:0xa bank_mask:0xf
	s_nop 1
	v_max_f32_dpp v41, v41, v41 row_bcast:31 row_mask:0xc bank_mask:0xf
	s_nop 1
	v_readlane_b32 s28, v41, 63
	s_nop 1
	v_div_scale_f32 v48, s[30:31], s28, s28, v47
	v_rcp_f32_e32 v49, v48
	s_nop 0
	v_fma_f32 v50, -v48, v49, 1.0
	v_fmac_f32_e32 v49, v50, v49
	v_mov_b32_e32 v50, s28
	v_div_scale_f32 v50, vcc, s32, v50, s32
	v_mul_f32_e32 v51, v50, v49
	v_fma_f32 v52, -v48, v51, v50
	v_fmac_f32_e32 v51, v52, v49
	v_fma_f32 v48, -v48, v51, v50
	v_div_fmas_f32 v48, v48, v49, v51
	v_div_fixup_f32 v48, v48, s28, v47
	v_cmp_gt_f32_e64 vcc, s28, 0
	v_writelane_b32 v40, s28, 16
	s_nop 0
	v_cndmask_b32_e32 v48, 0, v48, vcc
	v_fmaak_f32 v49, v18, v48, 0x4b400000
	v_fmaak_f32 v50, v19, v48, 0x4b400000
	v_fmaak_f32 v51, v20, v48, 0x4b400000
	v_fmaak_f32 v52, v21, v48, 0x4b400000
	v_perm_b32 v49, v50, v49, s33
	v_perm_b32 v51, v52, v51, s34
	v_or_b32_e32 v120, v49, v51
	v_fmaak_f32 v53, v22, v48, 0x4b400000
	v_fmaak_f32 v54, v23, v48, 0x4b400000
	v_fmaak_f32 v55, v24, v48, 0x4b400000
	v_fmaak_f32 v46, v25, v48, 0x4b400000
	v_perm_b32 v53, v54, v53, s33
	v_perm_b32 v55, v46, v55, s34
	v_or_b32_e32 v121, v53, v55
	v_fmaak_f32 v49, v26, v48, 0x4b400000
	v_fmaak_f32 v50, v27, v48, 0x4b400000
	v_fmaak_f32 v51, v28, v48, 0x4b400000
	v_fmaak_f32 v52, v29, v48, 0x4b400000
	v_perm_b32 v49, v50, v49, s33
	v_perm_b32 v51, v52, v51, s34
	v_or_b32_e32 v122, v49, v51
	v_fmaak_f32 v53, v30, v48, 0x4b400000
	v_fmaak_f32 v54, v31, v48, 0x4b400000
	v_fmaak_f32 v55, v32, v48, 0x4b400000
	v_fmaak_f32 v46, v33, v48, 0x4b400000
	v_perm_b32 v53, v54, v53, s33
	v_perm_b32 v55, v46, v55, s34
	v_or_b32_e32 v123, v53, v55
	s_waitcnt vmcnt(0)
	ds_read_b128 v[18:21], v38 offset:4096
	ds_read_b128 v[22:25], v38 offset:5120
	ds_read_b128 v[26:29], v38 offset:6144
	ds_read_b128 v[30:33], v38 offset:7168
	s_waitcnt lgkmcnt(0)
	s_mov_b32 m0, s35
	s_nop 0
	global_load_lds_dwordx4 v34, s[16:17] nt
	global_load_lds_dwordx4 v34, s[16:17] offset:1024 nt
	global_load_lds_dwordx4 v34, s[16:17] offset:2048 nt
	global_load_lds_dwordx4 v35, s[16:17] offset:3072 nt
	s_add_u32 s16, s16, 0x7d00
	s_addc_u32 s17, s17, 0
	v_cndmask_b32_e64 v30, 0, v30, s[18:19]
	v_cndmask_b32_e64 v31, 0, v31, s[18:19]
	v_cndmask_b32_e64 v32, 0, v32, s[18:19]
	v_cndmask_b32_e64 v33, 0, v33, s[18:19]
	v_max3_f32 v41, |v18|, |v19|, |v20|
	v_max3_f32 v42, |v21|, |v22|, |v23|
	v_max3_f32 v43, |v24|, |v25|, |v26|
	v_max3_f32 v44, |v27|, |v28|, |v29|
	v_max3_f32 v45, |v30|, |v31|, |v32|
	v_max3_f32 v41, v41, v42, |v33|
	v_max3_f32 v43, v43, v44, v45
	v_max_f32_e32 v41, v41, v43
	v_pk_add_f32 v[2:3], v[2:3], v[18:19]
	v_pk_add_f32 v[4:5], v[4:5], v[20:21]
	v_max_f32_dpp v41, v41, v41 quad_perm:[1,0,3,2] row_mask:0xf bank_mask:0xf
	v_pk_add_f32 v[6:7], v[6:7], v[22:23]
	v_pk_add_f32 v[8:9], v[8:9], v[24:25]
	v_max_f32_dpp v41, v41, v41 quad_perm:[2,3,0,1] row_mask:0xf bank_mask:0xf
	v_pk_add_f32 v[10:11], v[10:11], v[26:27]
	v_pk_add_f32 v[12:13], v[12:13], v[28:29]
	v_max_f32_dpp v41, v41, v41 row_half_mirror row_mask:0xf bank_mask:0xf
	v_pk_add_f32 v[14:15], v[14:15], v[30:31]
	v_pk_add_f32 v[16:17], v[16:17], v[32:33]
	v_max_f32_dpp v41, v41, v41 row_mirror row_mask:0xf bank_mask:0xf
	s_nop 1
	v_max_f32_dpp v41, v41, v41 row_bcast:15 row_mask:0xa bank_mask:0xf
	s_nop 1
	v_max_f32_dpp v41, v41, v41 row_bcast:31 row_mask:0xc bank_mask:0xf
	s_nop 1
	v_readlane_b32 s28, v41, 63
	s_nop 1
	v_div_scale_f32 v48, s[30:31], s28, s28, v47
	v_rcp_f32_e32 v49, v48
	s_nop 0
	v_fma_f32 v50, -v48, v49, 1.0
	v_fmac_f32_e32 v49, v50, v49
	v_mov_b32_e32 v50, s28
	v_div_scale_f32 v50, vcc, s32, v50, s32
	v_mul_f32_e32 v51, v50, v49
	v_fma_f32 v52, -v48, v51, v50
	v_fmac_f32_e32 v51, v52, v49
	v_fma_f32 v48, -v48, v51, v50
	v_div_fmas_f32 v48, v48, v49, v51
	v_div_fixup_f32 v48, v48, s28, v47
	v_cmp_gt_f32_e64 vcc, s28, 0
	v_writelane_b32 v40, s28, 17
	s_nop 0
	v_cndmask_b32_e32 v48, 0, v48, vcc
	v_fmaak_f32 v49, v18, v48, 0x4b400000
	v_fmaak_f32 v50, v19, v48, 0x4b400000
	v_fmaak_f32 v51, v20, v48, 0x4b400000
	v_fmaak_f32 v52, v21, v48, 0x4b400000
	v_perm_b32 v49, v50, v49, s33
	v_perm_b32 v51, v52, v51, s34
	v_or_b32_e32 v124, v49, v51
	v_fmaak_f32 v53, v22, v48, 0x4b400000
	v_fmaak_f32 v54, v23, v48, 0x4b400000
	v_fmaak_f32 v55, v24, v48, 0x4b400000
	v_fmaak_f32 v46, v25, v48, 0x4b400000
	v_perm_b32 v53, v54, v53, s33
	v_perm_b32 v55, v46, v55, s34
	v_or_b32_e32 v125, v53, v55
	v_fmaak_f32 v49, v26, v48, 0x4b400000
	v_fmaak_f32 v50, v27, v48, 0x4b400000
	v_fmaak_f32 v51, v28, v48, 0x4b400000
	v_fmaak_f32 v52, v29, v48, 0x4b400000
	v_perm_b32 v49, v50, v49, s33
	v_perm_b32 v51, v52, v51, s34
	v_or_b32_e32 v126, v49, v51
	v_fmaak_f32 v53, v30, v48, 0x4b400000
	v_fmaak_f32 v54, v31, v48, 0x4b400000
	v_fmaak_f32 v55, v32, v48, 0x4b400000
	v_fmaak_f32 v46, v33, v48, 0x4b400000
	v_perm_b32 v53, v54, v53, s33
	v_perm_b32 v55, v46, v55, s34
	v_or_b32_e32 v127, v53, v55
	s_waitcnt vmcnt(0)
	ds_read_b128 v[18:21], v38 offset:0
	ds_read_b128 v[22:25], v38 offset:1024
	ds_read_b128 v[26:29], v38 offset:2048
	ds_read_b128 v[30:33], v38 offset:3072
	s_waitcnt lgkmcnt(0)
	s_mov_b32 m0, s36
	s_nop 0
	global_load_lds_dwordx4 v34, s[16:17] nt
	global_load_lds_dwordx4 v34, s[16:17] offset:1024 nt
	global_load_lds_dwordx4 v34, s[16:17] offset:2048 nt
	global_load_lds_dwordx4 v35, s[16:17] offset:3072 nt
	s_add_u32 s16, s16, 0x7d00
	s_addc_u32 s17, s17, 0
	v_cndmask_b32_e64 v30, 0, v30, s[18:19]
	v_cndmask_b32_e64 v31, 0, v31, s[18:19]
	v_cndmask_b32_e64 v32, 0, v32, s[18:19]
	v_cndmask_b32_e64 v33, 0, v33, s[18:19]
	v_max3_f32 v41, |v18|, |v19|, |v20|
	v_max3_f32 v42, |v21|, |v22|, |v23|
	v_max3_f32 v43, |v24|, |v25|, |v26|
	v_max3_f32 v44, |v27|, |v28|, |v29|
	v_max3_f32 v45, |v30|, |v31|, |v32|
	v_max3_f32 v41, v41, v42, |v33|
	v_max3_f32 v43, v43, v44, v45
	v_max_f32_e32 v41, v41, v43
	v_pk_add_f32 v[2:3], v[2:3], v[18:19]
	v_pk_add_f32 v[4:5], v[4:5], v[20:21]
	v_max_f32_dpp v41, v41, v41 quad_perm:[1,0,3,2] row_mask:0xf bank_mask:0xf
	v_pk_add_f32 v[6:7], v[6:7], v[22:23]
	v_pk_add_f32 v[8:9], v[8:9], v[24:25]
	v_max_f32_dpp v41, v41, v41 quad_perm:[2,3,0,1] row_mask:0xf bank_mask:0xf
	v_pk_add_f32 v[10:11], v[10:11], v[26:27]
	v_pk_add_f32 v[12:13], v[12:13], v[28:29]
	v_max_f32_dpp v41, v41, v41 row_half_mirror row_mask:0xf bank_mask:0xf
	v_pk_add_f32 v[14:15], v[14:15], v[30:31]
	v_pk_add_f32 v[16:17], v[16:17], v[32:33]
	v_max_f32_dpp v41, v41, v41 row_mirror row_mask:0xf bank_mask:0xf
	s_nop 1
	v_max_f32_dpp v41, v41, v41 row_bcast:15 row_mask:0xa bank_mask:0xf
	s_nop 1
	v_max_f32_dpp v41, v41, v41 row_bcast:31 row_mask:0xc bank_mask:0xf
	s_nop 1
	v_readlane_b32 s28, v41, 63
	s_nop 1
	v_div_scale_f32 v48, s[30:31], s28, s28, v47
	v_rcp_f32_e32 v49, v48
	s_nop 0
	v_fma_f32 v50, -v48, v49, 1.0
	v_fmac_f32_e32 v49, v50, v49
	v_mov_b32_e32 v50, s28
	v_div_scale_f32 v50, vcc, s32, v50, s32
	v_mul_f32_e32 v51, v50, v49
	v_fma_f32 v52, -v48, v51, v50
	v_fmac_f32_e32 v51, v52, v49
	v_fma_f32 v48, -v48, v51, v50
	v_div_fmas_f32 v48, v48, v49, v51
	v_div_fixup_f32 v48, v48, s28, v47
	v_cmp_gt_f32_e64 vcc, s28, 0
	v_writelane_b32 v40, s28, 18
	s_nop 0
	v_cndmask_b32_e32 v48, 0, v48, vcc
	v_fmaak_f32 v49, v18, v48, 0x4b400000
	v_fmaak_f32 v50, v19, v48, 0x4b400000
	v_fmaak_f32 v51, v20, v48, 0x4b400000
	v_fmaak_f32 v52, v21, v48, 0x4b400000
	v_perm_b32 v49, v50, v49, s33
	v_perm_b32 v51, v52, v51, s34
	v_or_b32_e32 v49, v49, v51
	global_store_dword v39, v49, s[20:21]
	v_fmaak_f32 v53, v22, v48, 0x4b400000
	v_fmaak_f32 v54, v23, v48, 0x4b400000
	v_fmaak_f32 v55, v24, v48, 0x4b400000
	v_fmaak_f32 v46, v25, v48, 0x4b400000
	v_perm_b32 v53, v54, v53, s33
	v_perm_b32 v55, v46, v55, s34
	v_or_b32_e32 v53, v53, v55
	global_store_dword v39, v53, s[22:23]
	v_fmaak_f32 v49, v26, v48, 0x4b400000
	v_fmaak_f32 v50, v27, v48, 0x4b400000
	v_fmaak_f32 v51, v28, v48, 0x4b400000
	v_fmaak_f32 v52, v29, v48, 0x4b400000
	v_perm_b32 v49, v50, v49, s33
	v_perm_b32 v51, v52, v51, s34
	v_or_b32_e32 v49, v49, v51
	global_store_dword v39, v49, s[24:25]
	v_fmaak_f32 v53, v30, v48, 0x4b400000
	v_fmaak_f32 v54, v31, v48, 0x4b400000
	v_fmaak_f32 v55, v32, v48, 0x4b400000
	v_fmaak_f32 v46, v33, v48, 0x4b400000
	v_perm_b32 v53, v54, v53, s33
	v_perm_b32 v55, v46, v55, s34
	v_or_b32_e32 v53, v53, v55
	global_store_dword v39, v53, s[26:27]
	s_add_u32 s20, s20, 0x400
	s_addc_u32 s21, s21, 0
	s_add_u32 s22, s22, 0x400
	s_addc_u32 s23, s23, 0
	s_add_u32 s24, s24, 0x400
	s_addc_u32 s25, s25, 0
	s_add_u32 s26, s26, 0x400
	s_addc_u32 s27, s27, 0
	s_waitcnt vmcnt(4)
	ds_read_b128 v[18:21], v38 offset:4096
	ds_read_b128 v[22:25], v38 offset:5120
	ds_read_b128 v[26:29], v38 offset:6144
	ds_read_b128 v[30:33], v38 offset:7168
	s_waitcnt lgkmcnt(0)
	s_mov_b32 m0, s35
	s_nop 0
	global_load_lds_dwordx4 v34, s[16:17] nt
	global_load_lds_dwordx4 v34, s[16:17] offset:1024 nt
	global_load_lds_dwordx4 v34, s[16:17] offset:2048 nt
	global_load_lds_dwordx4 v35, s[16:17] offset:3072 nt
	s_add_u32 s16, s16, 0x7d00
	s_addc_u32 s17, s17, 0
	v_cndmask_b32_e64 v30, 0, v30, s[18:19]
	v_cndmask_b32_e64 v31, 0, v31, s[18:19]
	v_cndmask_b32_e64 v32, 0, v32, s[18:19]
	v_cndmask_b32_e64 v33, 0, v33, s[18:19]
	v_max3_f32 v41, |v18|, |v19|, |v20|
	v_max3_f32 v42, |v21|, |v22|, |v23|
	v_max3_f32 v43, |v24|, |v25|, |v26|
	v_max3_f32 v44, |v27|, |v28|, |v29|
	v_max3_f32 v45, |v30|, |v31|, |v32|
	v_max3_f32 v41, v41, v42, |v33|
	v_max3_f32 v43, v43, v44, v45
	v_max_f32_e32 v41, v41, v43
	v_pk_add_f32 v[2:3], v[2:3], v[18:19]
	v_pk_add_f32 v[4:5], v[4:5], v[20:21]
	v_max_f32_dpp v41, v41, v41 quad_perm:[1,0,3,2] row_mask:0xf bank_mask:0xf
	v_pk_add_f32 v[6:7], v[6:7], v[22:23]
	v_pk_add_f32 v[8:9], v[8:9], v[24:25]
	v_max_f32_dpp v41, v41, v41 quad_perm:[2,3,0,1] row_mask:0xf bank_mask:0xf
	v_pk_add_f32 v[10:11], v[10:11], v[26:27]
	v_pk_add_f32 v[12:13], v[12:13], v[28:29]
	v_max_f32_dpp v41, v41, v41 row_half_mirror row_mask:0xf bank_mask:0xf
	v_pk_add_f32 v[14:15], v[14:15], v[30:31]
	v_pk_add_f32 v[16:17], v[16:17], v[32:33]
	v_max_f32_dpp v41, v41, v41 row_mirror row_mask:0xf bank_mask:0xf
	s_nop 1
	v_max_f32_dpp v41, v41, v41 row_bcast:15 row_mask:0xa bank_mask:0xf
	s_nop 1
	v_max_f32_dpp v41, v41, v41 row_bcast:31 row_mask:0xc bank_mask:0xf
	s_nop 1
	v_readlane_b32 s28, v41, 63
	s_nop 1
	v_div_scale_f32 v48, s[30:31], s28, s28, v47
	v_rcp_f32_e32 v49, v48
	s_nop 0
	v_fma_f32 v50, -v48, v49, 1.0
	v_fmac_f32_e32 v49, v50, v49
	v_mov_b32_e32 v50, s28
	v_div_scale_f32 v50, vcc, s32, v50, s32
	v_mul_f32_e32 v51, v50, v49
	v_fma_f32 v52, -v48, v51, v50
	v_fmac_f32_e32 v51, v52, v49
	v_fma_f32 v48, -v48, v51, v50
	v_div_fmas_f32 v48, v48, v49, v51
	v_div_fixup_f32 v48, v48, s28, v47
	v_cmp_gt_f32_e64 vcc, s28, 0
	v_writelane_b32 v40, s28, 19
	s_nop 0
	v_cndmask_b32_e32 v48, 0, v48, vcc
	v_fmaak_f32 v49, v18, v48, 0x4b400000
	v_fmaak_f32 v50, v19, v48, 0x4b400000
	v_fmaak_f32 v51, v20, v48, 0x4b400000
	v_fmaak_f32 v52, v21, v48, 0x4b400000
	v_perm_b32 v49, v50, v49, s33
	v_perm_b32 v51, v52, v51, s34
	v_or_b32_e32 v49, v49, v51
	global_store_dword v39, v49, s[20:21]
	v_fmaak_f32 v53, v22, v48, 0x4b400000
	v_fmaak_f32 v54, v23, v48, 0x4b400000
	v_fmaak_f32 v55, v24, v48, 0x4b400000
	v_fmaak_f32 v46, v25, v48, 0x4b400000
	v_perm_b32 v53, v54, v53, s33
	v_perm_b32 v55, v46, v55, s34
	v_or_b32_e32 v53, v53, v55
	global_store_dword v39, v53, s[22:23]
	v_fmaak_f32 v49, v26, v48, 0x4b400000
	v_fmaak_f32 v50, v27, v48, 0x4b400000
	v_fmaak_f32 v51, v28, v48, 0x4b400000
	v_fmaak_f32 v52, v29, v48, 0x4b400000
	v_perm_b32 v49, v50, v49, s33
	v_perm_b32 v51, v52, v51, s34
	v_or_b32_e32 v49, v49, v51
	global_store_dword v39, v49, s[24:25]
	v_fmaak_f32 v53, v30, v48, 0x4b400000
	v_fmaak_f32 v54, v31, v48, 0x4b400000
	v_fmaak_f32 v55, v32, v48, 0x4b400000
	v_fmaak_f32 v46, v33, v48, 0x4b400000
	v_perm_b32 v53, v54, v53, s33
	v_perm_b32 v55, v46, v55, s34
	v_or_b32_e32 v53, v53, v55
	global_store_dword v39, v53, s[26:27]
	s_add_u32 s20, s20, 0x400
	s_addc_u32 s21, s21, 0
	s_add_u32 s22, s22, 0x400
	s_addc_u32 s23, s23, 0
	s_add_u32 s24, s24, 0x400
	s_addc_u32 s25, s25, 0
	s_add_u32 s26, s26, 0x400
	s_addc_u32 s27, s27, 0
	s_waitcnt vmcnt(4)
	ds_read_b128 v[18:21], v38 offset:0
	ds_read_b128 v[22:25], v38 offset:1024
	ds_read_b128 v[26:29], v38 offset:2048
	ds_read_b128 v[30:33], v38 offset:3072
	s_waitcnt lgkmcnt(0)
	s_mov_b32 m0, s36
	s_nop 0
	global_load_lds_dwordx4 v34, s[16:17] nt
	global_load_lds_dwordx4 v34, s[16:17] offset:1024 nt
	global_load_lds_dwordx4 v34, s[16:17] offset:2048 nt
	global_load_lds_dwordx4 v35, s[16:17] offset:3072 nt
	s_add_u32 s16, s16, 0x7d00
	s_addc_u32 s17, s17, 0
	v_cndmask_b32_e64 v30, 0, v30, s[18:19]
	v_cndmask_b32_e64 v31, 0, v31, s[18:19]
	v_cndmask_b32_e64 v32, 0, v32, s[18:19]
	v_cndmask_b32_e64 v33, 0, v33, s[18:19]
	v_max3_f32 v41, |v18|, |v19|, |v20|
	v_max3_f32 v42, |v21|, |v22|, |v23|
	v_max3_f32 v43, |v24|, |v25|, |v26|
	v_max3_f32 v44, |v27|, |v28|, |v29|
	v_max3_f32 v45, |v30|, |v31|, |v32|
	v_max3_f32 v41, v41, v42, |v33|
	v_max3_f32 v43, v43, v44, v45
	v_max_f32_e32 v41, v41, v43
	v_pk_add_f32 v[2:3], v[2:3], v[18:19]
	v_pk_add_f32 v[4:5], v[4:5], v[20:21]
	v_max_f32_dpp v41, v41, v41 quad_perm:[1,0,3,2] row_mask:0xf bank_mask:0xf
	v_pk_add_f32 v[6:7], v[6:7], v[22:23]
	v_pk_add_f32 v[8:9], v[8:9], v[24:25]
	v_max_f32_dpp v41, v41, v41 quad_perm:[2,3,0,1] row_mask:0xf bank_mask:0xf
	v_pk_add_f32 v[10:11], v[10:11], v[26:27]
	v_pk_add_f32 v[12:13], v[12:13], v[28:29]
	v_max_f32_dpp v41, v41, v41 row_half_mirror row_mask:0xf bank_mask:0xf
	v_pk_add_f32 v[14:15], v[14:15], v[30:31]
	v_pk_add_f32 v[16:17], v[16:17], v[32:33]
	v_max_f32_dpp v41, v41, v41 row_mirror row_mask:0xf bank_mask:0xf
	s_nop 1
	v_max_f32_dpp v41, v41, v41 row_bcast:15 row_mask:0xa bank_mask:0xf
	s_nop 1
	v_max_f32_dpp v41, v41, v41 row_bcast:31 row_mask:0xc bank_mask:0xf
	s_nop 1
	v_readlane_b32 s28, v41, 63
	s_nop 1
	v_div_scale_f32 v48, s[30:31], s28, s28, v47
	v_rcp_f32_e32 v49, v48
	s_nop 0
	v_fma_f32 v50, -v48, v49, 1.0
	v_fmac_f32_e32 v49, v50, v49
	v_mov_b32_e32 v50, s28
	v_div_scale_f32 v50, vcc, s32, v50, s32
	v_mul_f32_e32 v51, v50, v49
	v_fma_f32 v52, -v48, v51, v50
	v_fmac_f32_e32 v51, v52, v49
	v_fma_f32 v48, -v48, v51, v50
	v_div_fmas_f32 v48, v48, v49, v51
	v_div_fixup_f32 v48, v48, s28, v47
	v_cmp_gt_f32_e64 vcc, s28, 0
	v_writelane_b32 v40, s28, 20
	s_nop 0
	v_cndmask_b32_e32 v48, 0, v48, vcc
	v_fmaak_f32 v49, v18, v48, 0x4b400000
	v_fmaak_f32 v50, v19, v48, 0x4b400000
	v_fmaak_f32 v51, v20, v48, 0x4b400000
	v_fmaak_f32 v52, v21, v48, 0x4b400000
	v_perm_b32 v49, v50, v49, s33
	v_perm_b32 v51, v52, v51, s34
	v_or_b32_e32 v49, v49, v51
	global_store_dword v39, v49, s[20:21]
	v_fmaak_f32 v53, v22, v48, 0x4b400000
	v_fmaak_f32 v54, v23, v48, 0x4b400000
	v_fmaak_f32 v55, v24, v48, 0x4b400000
	v_fmaak_f32 v46, v25, v48, 0x4b400000
	v_perm_b32 v53, v54, v53, s33
	v_perm_b32 v55, v46, v55, s34
	v_or_b32_e32 v53, v53, v55
	global_store_dword v39, v53, s[22:23]
	v_fmaak_f32 v49, v26, v48, 0x4b400000
	v_fmaak_f32 v50, v27, v48, 0x4b400000
	v_fmaak_f32 v51, v28, v48, 0x4b400000
	v_fmaak_f32 v52, v29, v48, 0x4b400000
	v_perm_b32 v49, v50, v49, s33
	v_perm_b32 v51, v52, v51, s34
	v_or_b32_e32 v49, v49, v51
	global_store_dword v39, v49, s[24:25]
	v_fmaak_f32 v53, v30, v48, 0x4b400000
	v_fmaak_f32 v54, v31, v48, 0x4b400000
	v_fmaak_f32 v55, v32, v48, 0x4b400000
	v_fmaak_f32 v46, v33, v48, 0x4b400000
	v_perm_b32 v53, v54, v53, s33
	v_perm_b32 v55, v46, v55, s34
	v_or_b32_e32 v53, v53, v55
	global_store_dword v39, v53, s[26:27]
	s_add_u32 s20, s20, 0x400
	s_addc_u32 s21, s21, 0
	s_add_u32 s22, s22, 0x400
	s_addc_u32 s23, s23, 0
	s_add_u32 s24, s24, 0x400
	s_addc_u32 s25, s25, 0
	s_add_u32 s26, s26, 0x400
	s_addc_u32 s27, s27, 0
	s_waitcnt vmcnt(4)
	ds_read_b128 v[18:21], v38 offset:4096
	ds_read_b128 v[22:25], v38 offset:5120
	ds_read_b128 v[26:29], v38 offset:6144
	ds_read_b128 v[30:33], v38 offset:7168
	s_waitcnt lgkmcnt(0)
	s_mov_b32 m0, s35
	s_nop 0
	global_load_lds_dwordx4 v34, s[16:17] nt
	global_load_lds_dwordx4 v34, s[16:17] offset:1024 nt
	global_load_lds_dwordx4 v34, s[16:17] offset:2048 nt
	global_load_lds_dwordx4 v35, s[16:17] offset:3072 nt
	s_add_u32 s16, s16, 0x7d00
	s_addc_u32 s17, s17, 0
	v_cndmask_b32_e64 v30, 0, v30, s[18:19]
	v_cndmask_b32_e64 v31, 0, v31, s[18:19]
	v_cndmask_b32_e64 v32, 0, v32, s[18:19]
	v_cndmask_b32_e64 v33, 0, v33, s[18:19]
	v_max3_f32 v41, |v18|, |v19|, |v20|
	v_max3_f32 v42, |v21|, |v22|, |v23|
	v_max3_f32 v43, |v24|, |v25|, |v26|
	v_max3_f32 v44, |v27|, |v28|, |v29|
	v_max3_f32 v45, |v30|, |v31|, |v32|
	v_max3_f32 v41, v41, v42, |v33|
	v_max3_f32 v43, v43, v44, v45
	v_max_f32_e32 v41, v41, v43
	v_pk_add_f32 v[2:3], v[2:3], v[18:19]
	v_pk_add_f32 v[4:5], v[4:5], v[20:21]
	v_max_f32_dpp v41, v41, v41 quad_perm:[1,0,3,2] row_mask:0xf bank_mask:0xf
	v_pk_add_f32 v[6:7], v[6:7], v[22:23]
	v_pk_add_f32 v[8:9], v[8:9], v[24:25]
	v_max_f32_dpp v41, v41, v41 quad_perm:[2,3,0,1] row_mask:0xf bank_mask:0xf
	v_pk_add_f32 v[10:11], v[10:11], v[26:27]
	v_pk_add_f32 v[12:13], v[12:13], v[28:29]
	v_max_f32_dpp v41, v41, v41 row_half_mirror row_mask:0xf bank_mask:0xf
	v_pk_add_f32 v[14:15], v[14:15], v[30:31]
	v_pk_add_f32 v[16:17], v[16:17], v[32:33]
	v_max_f32_dpp v41, v41, v41 row_mirror row_mask:0xf bank_mask:0xf
	s_nop 1
	v_max_f32_dpp v41, v41, v41 row_bcast:15 row_mask:0xa bank_mask:0xf
	s_nop 1
	v_max_f32_dpp v41, v41, v41 row_bcast:31 row_mask:0xc bank_mask:0xf
	s_nop 1
	v_readlane_b32 s28, v41, 63
	s_nop 1
	v_div_scale_f32 v48, s[30:31], s28, s28, v47
	v_rcp_f32_e32 v49, v48
	s_nop 0
	v_fma_f32 v50, -v48, v49, 1.0
	v_fmac_f32_e32 v49, v50, v49
	v_mov_b32_e32 v50, s28
	v_div_scale_f32 v50, vcc, s32, v50, s32
	v_mul_f32_e32 v51, v50, v49
	v_fma_f32 v52, -v48, v51, v50
	v_fmac_f32_e32 v51, v52, v49
	v_fma_f32 v48, -v48, v51, v50
	v_div_fmas_f32 v48, v48, v49, v51
	v_div_fixup_f32 v48, v48, s28, v47
	v_cmp_gt_f32_e64 vcc, s28, 0
	v_writelane_b32 v40, s28, 21
	s_nop 0
	v_cndmask_b32_e32 v48, 0, v48, vcc
	v_fmaak_f32 v49, v18, v48, 0x4b400000
	v_fmaak_f32 v50, v19, v48, 0x4b400000
	v_fmaak_f32 v51, v20, v48, 0x4b400000
	v_fmaak_f32 v52, v21, v48, 0x4b400000
	v_perm_b32 v49, v50, v49, s33
	v_perm_b32 v51, v52, v51, s34
	v_or_b32_e32 v49, v49, v51
	global_store_dword v39, v49, s[20:21]
	v_fmaak_f32 v53, v22, v48, 0x4b400000
	v_fmaak_f32 v54, v23, v48, 0x4b400000
	v_fmaak_f32 v55, v24, v48, 0x4b400000
	v_fmaak_f32 v46, v25, v48, 0x4b400000
	v_perm_b32 v53, v54, v53, s33
	v_perm_b32 v55, v46, v55, s34
	v_or_b32_e32 v53, v53, v55
	global_store_dword v39, v53, s[22:23]
	v_fmaak_f32 v49, v26, v48, 0x4b400000
	v_fmaak_f32 v50, v27, v48, 0x4b400000
	v_fmaak_f32 v51, v28, v48, 0x4b400000
	v_fmaak_f32 v52, v29, v48, 0x4b400000
	v_perm_b32 v49, v50, v49, s33
	v_perm_b32 v51, v52, v51, s34
	v_or_b32_e32 v49, v49, v51
	global_store_dword v39, v49, s[24:25]
	v_fmaak_f32 v53, v30, v48, 0x4b400000
	v_fmaak_f32 v54, v31, v48, 0x4b400000
	v_fmaak_f32 v55, v32, v48, 0x4b400000
	v_fmaak_f32 v46, v33, v48, 0x4b400000
	v_perm_b32 v53, v54, v53, s33
	v_perm_b32 v55, v46, v55, s34
	v_or_b32_e32 v53, v53, v55
	global_store_dword v39, v53, s[26:27]
	s_add_u32 s20, s20, 0x400
	s_addc_u32 s21, s21, 0
	s_add_u32 s22, s22, 0x400
	s_addc_u32 s23, s23, 0
	s_add_u32 s24, s24, 0x400
	s_addc_u32 s25, s25, 0
	s_add_u32 s26, s26, 0x400
	s_addc_u32 s27, s27, 0
	s_waitcnt vmcnt(4)
	ds_read_b128 v[18:21], v38 offset:0
	ds_read_b128 v[22:25], v38 offset:1024
	ds_read_b128 v[26:29], v38 offset:2048
	ds_read_b128 v[30:33], v38 offset:3072
	s_waitcnt lgkmcnt(0)
	s_mov_b32 m0, s36
	s_nop 0
	global_load_lds_dwordx4 v34, s[16:17] nt
	global_load_lds_dwordx4 v34, s[16:17] offset:1024 nt
	global_load_lds_dwordx4 v34, s[16:17] offset:2048 nt
	global_load_lds_dwordx4 v35, s[16:17] offset:3072 nt
	s_add_u32 s16, s16, 0x7d00
	s_addc_u32 s17, s17, 0
	v_cndmask_b32_e64 v30, 0, v30, s[18:19]
	v_cndmask_b32_e64 v31, 0, v31, s[18:19]
	v_cndmask_b32_e64 v32, 0, v32, s[18:19]
	v_cndmask_b32_e64 v33, 0, v33, s[18:19]
	v_max3_f32 v41, |v18|, |v19|, |v20|
	v_max3_f32 v42, |v21|, |v22|, |v23|
	v_max3_f32 v43, |v24|, |v25|, |v26|
	v_max3_f32 v44, |v27|, |v28|, |v29|
	v_max3_f32 v45, |v30|, |v31|, |v32|
	v_max3_f32 v41, v41, v42, |v33|
	v_max3_f32 v43, v43, v44, v45
	v_max_f32_e32 v41, v41, v43
	v_pk_add_f32 v[2:3], v[2:3], v[18:19]
	v_pk_add_f32 v[4:5], v[4:5], v[20:21]
	v_max_f32_dpp v41, v41, v41 quad_perm:[1,0,3,2] row_mask:0xf bank_mask:0xf
	v_pk_add_f32 v[6:7], v[6:7], v[22:23]
	v_pk_add_f32 v[8:9], v[8:9], v[24:25]
	v_max_f32_dpp v41, v41, v41 quad_perm:[2,3,0,1] row_mask:0xf bank_mask:0xf
	v_pk_add_f32 v[10:11], v[10:11], v[26:27]
	v_pk_add_f32 v[12:13], v[12:13], v[28:29]
	v_max_f32_dpp v41, v41, v41 row_half_mirror row_mask:0xf bank_mask:0xf
	v_pk_add_f32 v[14:15], v[14:15], v[30:31]
	v_pk_add_f32 v[16:17], v[16:17], v[32:33]
	v_max_f32_dpp v41, v41, v41 row_mirror row_mask:0xf bank_mask:0xf
	s_nop 1
	v_max_f32_dpp v41, v41, v41 row_bcast:15 row_mask:0xa bank_mask:0xf
	s_nop 1
	v_max_f32_dpp v41, v41, v41 row_bcast:31 row_mask:0xc bank_mask:0xf
	s_nop 1
	v_readlane_b32 s28, v41, 63
	s_nop 1
	v_div_scale_f32 v48, s[30:31], s28, s28, v47
	v_rcp_f32_e32 v49, v48
	s_nop 0
	v_fma_f32 v50, -v48, v49, 1.0
	v_fmac_f32_e32 v49, v50, v49
	v_mov_b32_e32 v50, s28
	v_div_scale_f32 v50, vcc, s32, v50, s32
	v_mul_f32_e32 v51, v50, v49
	v_fma_f32 v52, -v48, v51, v50
	v_fmac_f32_e32 v51, v52, v49
	v_fma_f32 v48, -v48, v51, v50
	v_div_fmas_f32 v48, v48, v49, v51
	v_div_fixup_f32 v48, v48, s28, v47
	v_cmp_gt_f32_e64 vcc, s28, 0
	v_writelane_b32 v40, s28, 22
	s_nop 0
	v_cndmask_b32_e32 v48, 0, v48, vcc
	v_fmaak_f32 v49, v18, v48, 0x4b400000
	v_fmaak_f32 v50, v19, v48, 0x4b400000
	v_fmaak_f32 v51, v20, v48, 0x4b400000
	v_fmaak_f32 v52, v21, v48, 0x4b400000
	v_perm_b32 v49, v50, v49, s33
	v_perm_b32 v51, v52, v51, s34
	v_or_b32_e32 v49, v49, v51
	global_store_dword v39, v49, s[20:21]
	v_fmaak_f32 v53, v22, v48, 0x4b400000
	v_fmaak_f32 v54, v23, v48, 0x4b400000
	v_fmaak_f32 v55, v24, v48, 0x4b400000
	v_fmaak_f32 v46, v25, v48, 0x4b400000
	v_perm_b32 v53, v54, v53, s33
	v_perm_b32 v55, v46, v55, s34
	v_or_b32_e32 v53, v53, v55
	global_store_dword v39, v53, s[22:23]
	v_fmaak_f32 v49, v26, v48, 0x4b400000
	v_fmaak_f32 v50, v27, v48, 0x4b400000
	v_fmaak_f32 v51, v28, v48, 0x4b400000
	v_fmaak_f32 v52, v29, v48, 0x4b400000
	v_perm_b32 v49, v50, v49, s33
	v_perm_b32 v51, v52, v51, s34
	v_or_b32_e32 v49, v49, v51
	global_store_dword v39, v49, s[24:25]
	v_fmaak_f32 v53, v30, v48, 0x4b400000
	v_fmaak_f32 v54, v31, v48, 0x4b400000
	v_fmaak_f32 v55, v32, v48, 0x4b400000
	v_fmaak_f32 v46, v33, v48, 0x4b400000
	v_perm_b32 v53, v54, v53, s33
	v_perm_b32 v55, v46, v55, s34
	v_or_b32_e32 v53, v53, v55
	global_store_dword v39, v53, s[26:27]
	s_add_u32 s20, s20, 0x400
	s_addc_u32 s21, s21, 0
	s_add_u32 s22, s22, 0x400
	s_addc_u32 s23, s23, 0
	s_add_u32 s24, s24, 0x400
	s_addc_u32 s25, s25, 0
	s_add_u32 s26, s26, 0x400
	s_addc_u32 s27, s27, 0
	s_waitcnt vmcnt(4)
	ds_read_b128 v[18:21], v38 offset:4096
	ds_read_b128 v[22:25], v38 offset:5120
	ds_read_b128 v[26:29], v38 offset:6144
	ds_read_b128 v[30:33], v38 offset:7168
	s_waitcnt lgkmcnt(0)
	s_cmp_eq_u32 s29, 1
	s_cbranch_scc0 .Lk1_nodma24
	s_mov_b32 m0, s35
	s_nop 0
	global_load_lds_dwordx4 v34, s[16:17] nt
	global_load_lds_dwordx4 v34, s[16:17] offset:1024 nt
	global_load_lds_dwordx4 v34, s[16:17] offset:2048 nt
	global_load_lds_dwordx4 v35, s[16:17] offset:3072 nt
	s_add_u32 s16, s16, 0x7d00
	s_addc_u32 s17, s17, 0
.Lk1_nodma24:
	v_cndmask_b32_e64 v30, 0, v30, s[18:19]
	v_cndmask_b32_e64 v31, 0, v31, s[18:19]
	v_cndmask_b32_e64 v32, 0, v32, s[18:19]
	v_cndmask_b32_e64 v33, 0, v33, s[18:19]
	v_max3_f32 v41, |v18|, |v19|, |v20|
	v_max3_f32 v42, |v21|, |v22|, |v23|
	v_max3_f32 v43, |v24|, |v25|, |v26|
	v_max3_f32 v44, |v27|, |v28|, |v29|
	v_max3_f32 v45, |v30|, |v31|, |v32|
	v_max3_f32 v41, v41, v42, |v33|
	v_max3_f32 v43, v43, v44, v45
	v_max_f32_e32 v41, v41, v43
	v_pk_add_f32 v[2:3], v[2:3], v[18:19]
	v_pk_add_f32 v[4:5], v[4:5], v[20:21]
	v_max_f32_dpp v41, v41, v41 quad_perm:[1,0,3,2] row_mask:0xf bank_mask:0xf
	v_pk_add_f32 v[6:7], v[6:7], v[22:23]
	v_pk_add_f32 v[8:9], v[8:9], v[24:25]
	v_max_f32_dpp v41, v41, v41 quad_perm:[2,3,0,1] row_mask:0xf bank_mask:0xf
	v_pk_add_f32 v[10:11], v[10:11], v[26:27]
	v_pk_add_f32 v[12:13], v[12:13], v[28:29]
	v_max_f32_dpp v41, v41, v41 row_half_mirror row_mask:0xf bank_mask:0xf
	v_pk_add_f32 v[14:15], v[14:15], v[30:31]
	v_pk_add_f32 v[16:17], v[16:17], v[32:33]
	v_max_f32_dpp v41, v41, v41 row_mirror row_mask:0xf bank_mask:0xf
	s_nop 1
	v_max_f32_dpp v41, v41, v41 row_bcast:15 row_mask:0xa bank_mask:0xf
	s_nop 1
	v_max_f32_dpp v41, v41, v41 row_bcast:31 row_mask:0xc bank_mask:0xf
	s_nop 1
	v_readlane_b32 s28, v41, 63
	s_nop 1
	v_div_scale_f32 v48, s[30:31], s28, s28, v47
	v_rcp_f32_e32 v49, v48
	s_nop 0
	v_fma_f32 v50, -v48, v49, 1.0
	v_fmac_f32_e32 v49, v50, v49
	v_mov_b32_e32 v50, s28
	v_div_scale_f32 v50, vcc, s32, v50, s32
	v_mul_f32_e32 v51, v50, v49
	v_fma_f32 v52, -v48, v51, v50
	v_fmac_f32_e32 v51, v52, v49
	v_fma_f32 v48, -v48, v51, v50
	v_div_fmas_f32 v48, v48, v49, v51
	v_div_fixup_f32 v48, v48, s28, v47
	v_cmp_gt_f32_e64 vcc, s28, 0
	v_writelane_b32 v40, s28, 23
	s_nop 0
	v_cndmask_b32_e32 v48, 0, v48, vcc
	v_fmaak_f32 v49, v18, v48, 0x4b400000
	v_fmaak_f32 v50, v19, v48, 0x4b400000
	v_fmaak_f32 v51, v20, v48, 0x4b400000
	v_fmaak_f32 v52, v21, v48, 0x4b400000
	v_perm_b32 v49, v50, v49, s33
	v_perm_b32 v51, v52, v51, s34
	v_or_b32_e32 v49, v49, v51
	global_store_dword v39, v49, s[20:21]
	v_fmaak_f32 v53, v22, v48, 0x4b400000
	v_fmaak_f32 v54, v23, v48, 0x4b400000
	v_fmaak_f32 v55, v24, v48, 0x4b400000
	v_fmaak_f32 v46, v25, v48, 0x4b400000
	v_perm_b32 v53, v54, v53, s33
	v_perm_b32 v55, v46, v55, s34
	v_or_b32_e32 v53, v53, v55
	global_store_dword v39, v53, s[22:23]
	v_fmaak_f32 v49, v26, v48, 0x4b400000
	v_fmaak_f32 v50, v27, v48, 0x4b400000
	v_fmaak_f32 v51, v28, v48, 0x4b400000
	v_fmaak_f32 v52, v29, v48, 0x4b400000
	v_perm_b32 v49, v50, v49, s33
	v_perm_b32 v51, v52, v51, s34
	v_or_b32_e32 v49, v49, v51
	global_store_dword v39, v49, s[24:25]
	v_fmaak_f32 v53, v30, v48, 0x4b400000
	v_fmaak_f32 v54, v31, v48, 0x4b400000
	v_fmaak_f32 v55, v32, v48, 0x4b400000
	v_fmaak_f32 v46, v33, v48, 0x4b400000
	v_perm_b32 v53, v54, v53, s33
	v_perm_b32 v55, v46, v55, s34
	v_or_b32_e32 v53, v53, v55
	global_store_dword v39, v53, s[26:27]
	s_add_u32 s20, s20, 0x400
	s_addc_u32 s21, s21, 0
	s_add_u32 s22, s22, 0x400
	s_addc_u32 s23, s23, 0
	s_add_u32 s24, s24, 0x400
	s_addc_u32 s25, s25, 0
	s_add_u32 s26, s26, 0x400
	s_addc_u32 s27, s27, 0
	s_cmp_eq_u32 s29, 1
	s_cbranch_scc0 .Lk1_flush
	s_waitcnt vmcnt(4)
	ds_read_b128 v[18:21], v38 offset:0
	ds_read_b128 v[22:25], v38 offset:1024
	ds_read_b128 v[26:29], v38 offset:2048
	ds_read_b128 v[30:33], v38 offset:3072
	s_waitcnt lgkmcnt(0)
	v_cndmask_b32_e64 v30, 0, v30, s[18:19]
	v_cndmask_b32_e64 v31, 0, v31, s[18:19]
	v_cndmask_b32_e64 v32, 0, v32, s[18:19]
	v_cndmask_b32_e64 v33, 0, v33, s[18:19]
	v_max3_f32 v41, |v18|, |v19|, |v20|
	v_max3_f32 v42, |v21|, |v22|, |v23|
	v_max3_f32 v43, |v24|, |v25|, |v26|
	v_max3_f32 v44, |v27|, |v28|, |v29|
	v_max3_f32 v45, |v30|, |v31|, |v32|
	v_max3_f32 v41, v41, v42, |v33|
	v_max3_f32 v43, v43, v44, v45
	v_max_f32_e32 v41, v41, v43
	v_pk_add_f32 v[2:3], v[2:3], v[18:19]
	v_pk_add_f32 v[4:5], v[4:5], v[20:21]
	v_max_f32_dpp v41, v41, v41 quad_perm:[1,0,3,2] row_mask:0xf bank_mask:0xf
	v_pk_add_f32 v[6:7], v[6:7], v[22:23]
	v_pk_add_f32 v[8:9], v[8:9], v[24:25]
	v_max_f32_dpp v41, v41, v41 quad_perm:[2,3,0,1] row_mask:0xf bank_mask:0xf
	v_pk_add_f32 v[10:11], v[10:11], v[26:27]
	v_pk_add_f32 v[12:13], v[12:13], v[28:29]
	v_max_f32_dpp v41, v41, v41 row_half_mirror row_mask:0xf bank_mask:0xf
	v_pk_add_f32 v[14:15], v[14:15], v[30:31]
	v_pk_add_f32 v[16:17], v[16:17], v[32:33]
	v_max_f32_dpp v41, v41, v41 row_mirror row_mask:0xf bank_mask:0xf
	s_nop 1
	v_max_f32_dpp v41, v41, v41 row_bcast:15 row_mask:0xa bank_mask:0xf
	s_nop 1
	v_max_f32_dpp v41, v41, v41 row_bcast:31 row_mask:0xc bank_mask:0xf
	s_nop 1
	v_readlane_b32 s28, v41, 63
	s_nop 1
	v_div_scale_f32 v48, s[30:31], s28, s28, v47
	v_rcp_f32_e32 v49, v48
	s_nop 0
	v_fma_f32 v50, -v48, v49, 1.0
	v_fmac_f32_e32 v49, v50, v49
	v_mov_b32_e32 v50, s28
	v_div_scale_f32 v50, vcc, s32, v50, s32
	v_mul_f32_e32 v51, v50, v49
	v_fma_f32 v52, -v48, v51, v50
	v_fmac_f32_e32 v51, v52, v49
	v_fma_f32 v48, -v48, v51, v50
	v_div_fmas_f32 v48, v48, v49, v51
	v_div_fixup_f32 v48, v48, s28, v47
	v_cmp_gt_f32_e64 vcc, s28, 0
	v_writelane_b32 v40, s28, 24
	s_nop 0
	v_cndmask_b32_e32 v48, 0, v48, vcc
	v_fmaak_f32 v49, v18, v48, 0x4b400000
	v_fmaak_f32 v50, v19, v48, 0x4b400000
	v_fmaak_f32 v51, v20, v48, 0x4b400000
	v_fmaak_f32 v52, v21, v48, 0x4b400000
	v_perm_b32 v49, v50, v49, s33
	v_perm_b32 v51, v52, v51, s34
	v_or_b32_e32 v49, v49, v51
	global_store_dword v39, v49, s[20:21]
	v_fmaak_f32 v53, v22, v48, 0x4b400000
	v_fmaak_f32 v54, v23, v48, 0x4b400000
	v_fmaak_f32 v55, v24, v48, 0x4b400000
	v_fmaak_f32 v46, v25, v48, 0x4b400000
	v_perm_b32 v53, v54, v53, s33
	v_perm_b32 v55, v46, v55, s34
	v_or_b32_e32 v53, v53, v55
	global_store_dword v39, v53, s[22:23]
	v_fmaak_f32 v49, v26, v48, 0x4b400000
	v_fmaak_f32 v50, v27, v48, 0x4b400000
	v_fmaak_f32 v51, v28, v48, 0x4b400000
	v_fmaak_f32 v52, v29, v48, 0x4b400000
	v_perm_b32 v49, v50, v49, s33
	v_perm_b32 v51, v52, v51, s34
	v_or_b32_e32 v49, v49, v51
	global_store_dword v39, v49, s[24:25]
	v_fmaak_f32 v53, v30, v48, 0x4b400000
	v_fmaak_f32 v54, v31, v48, 0x4b400000
	v_fmaak_f32 v55, v32, v48, 0x4b400000
	v_fmaak_f32 v46, v33, v48, 0x4b400000
	v_perm_b32 v53, v54, v53, s33
	v_perm_b32 v55, v46, v55, s34
	v_or_b32_e32 v53, v53, v55
	global_store_dword v39, v53, s[26:27]
	s_add_u32 s20, s20, 0x400
	s_addc_u32 s21, s21, 0
	s_add_u32 s22, s22, 0x400
	s_addc_u32 s23, s23, 0
	s_add_u32 s24, s24, 0x400
	s_addc_u32 s25, s25, 0
	s_add_u32 s26, s26, 0x400
	s_addc_u32 s27, s27, 0

_Z15k3_pairs_slicedPKDv4_jPKfPKiS5_PiPf:
	s_load_dwordx8 s[4:11], s[0:1], 0x0
	s_load_dwordx2 s[12:13], s[0:1], 0x20
	v_and_b32_e32 v1, 63, v0
	v_lshrrev_b32_e32 v2, 6, v0
	s_and_b32 s14, s2, 7
	s_lshr_b32 s15, s2, 3
	v_readfirstlane_b32 s16, v2
	s_lshl_b32 s17, s15, 10
	s_lshl_b32 s24, s16, 8
	s_add_u32 s17, s17, s24
	v_and_b32_e32 v2, 7, v1
	v_lshrrev_b32_e32 v3, 3, v1
	v_cmp_eq_u32_e64 s[40:41], 0, v2
	v_cmp_eq_u32_e64 s[42:43], 1, v2
	v_cmp_eq_u32_e64 s[44:45], 2, v2
	v_cmp_eq_u32_e64 s[46:47], 3, v2
	v_cmp_eq_u32_e64 s[48:49], 4, v2
	v_cmp_eq_u32_e64 s[50:51], 5, v2
	v_cmp_eq_u32_e64 s[52:53], 6, v2
	v_cmp_eq_u32_e64 s[54:55], 7, v2
	v_lshl_add_u32 v28, v2, 3, v3
	v_lshlrev_b32_e32 v28, 2, v28
	v_lshlrev_b32_e32 v3, 2, v3
	v_lshlrev_b32_e32 v2, 4, v2
	v_lshlrev_b32_e32 v29, 2, v1
	v_lshlrev_b32_e32 v30, 2, v2
	s_lshl_b32 s26, s17, 2
	s_lshl_b32 s27, s14, 9
	s_mul_i32 s34, s14, 0xc35000
	s_waitcnt lgkmcnt(0)
	s_add_u32 s24, s8, s26
	s_addc_u32 s25, s9, 0
	s_add_u32 s28, s10, s26
	s_addc_u32 s29, s11, 0
	global_load_dword v20, v29, s[24:25]
	global_load_dword v24, v29, s[28:29]
	global_load_dword v21, v29, s[24:25] offset:256
	global_load_dword v25, v29, s[28:29] offset:256
	global_load_dword v22, v29, s[24:25] offset:512
	global_load_dword v26, v29, s[28:29] offset:512
	global_load_dword v23, v29, s[24:25] offset:768
	global_load_dword v27, v29, s[28:29] offset:768
	s_add_u32 s30, s6, s27
	s_addc_u32 s31, s7, 0
	global_load_dwordx4 v[4:7], v30, s[30:31]
	global_load_dwordx4 v[8:11], v30, s[30:31] offset:16
	global_load_dwordx4 v[12:15], v30, s[30:31] offset:32
	global_load_dwordx4 v[16:19], v30, s[30:31] offset:48
	s_add_u32 s18, s4, s34
	s_addc_u32 s19, s5, 0
	s_add_u32 s21, s14, 2
	s_cmp_lt_u32 s14, 2
	s_cselect_b32 s21, s14, s21
	s_lshl_b32 s21, s21, 19
	s_add_u32 s22, s14, 10
	s_lshl_b32 s22, s22, 19
	s_sub_u32 s23, s14, 6
	s_lshl_b32 s23, s23, 19
	s_sub_u32 s23, s23, 0x262a80
	s_cmp_lt_u32 s14, 6
	s_cselect_b32 s33, s22, s23
	s_ashr_i32 s35, s33, 31
	s_add_u32 s20, s12, s21
	s_addc_u32 s21, s13, 0
	s_add_u32 s22, s12, s33
	s_addc_u32 s23, s13, s35
	s_add_u32 s20, s20, s26
	s_addc_u32 s21, s21, 0
	s_add_u32 s22, s22, s26
	s_addc_u32 s23, s23, 0
	s_waitcnt vmcnt(4)
	ds_bpermute_b32 v104, v3, v20
	ds_bpermute_b32 v105, v3, v24
	s_waitcnt lgkmcnt(0)
	v_lshl_add_u32 v106, v104, 7, v2
	v_lshl_add_u32 v107, v105, 7, v2
	global_load_dwordx4 v[32:35], v106, s[18:19]
	global_load_dwordx4 v[36:39], v107, s[18:19]
	ds_bpermute_b32 v104, v3, v20 offset:32
	ds_bpermute_b32 v105, v3, v24 offset:32
	s_waitcnt lgkmcnt(0)
	v_lshl_add_u32 v106, v104, 7, v2
	v_lshl_add_u32 v107, v105, 7, v2
	global_load_dwordx4 v[40:43], v106, s[18:19]
	global_load_dwordx4 v[44:47], v107, s[18:19]
	ds_bpermute_b32 v104, v3, v20 offset:64
	ds_bpermute_b32 v105, v3, v24 offset:64
	s_waitcnt lgkmcnt(0)
	v_lshl_add_u32 v106, v104, 7, v2
	v_lshl_add_u32 v107, v105, 7, v2
	global_load_dwordx4 v[48:51], v106, s[18:19]
	global_load_dwordx4 v[52:55], v107, s[18:19]
	ds_bpermute_b32 v104, v3, v20 offset:96
	ds_bpermute_b32 v105, v3, v24 offset:96
	s_waitcnt lgkmcnt(0)
	v_lshl_add_u32 v106, v104, 7, v2
	v_lshl_add_u32 v107, v105, 7, v2
	global_load_dwordx4 v[56:59], v106, s[18:19]
	global_load_dwordx4 v[60:63], v107, s[18:19]
	ds_bpermute_b32 v104, v3, v20 offset:128
	ds_bpermute_b32 v105, v3, v24 offset:128
	s_waitcnt lgkmcnt(0)
	v_lshl_add_u32 v106, v104, 7, v2
	v_lshl_add_u32 v107, v105, 7, v2
	global_load_dwordx4 v[64:67], v106, s[18:19]
	global_load_dwordx4 v[68:71], v107, s[18:19]
	ds_bpermute_b32 v104, v3, v20 offset:160
	ds_bpermute_b32 v105, v3, v24 offset:160
	s_waitcnt lgkmcnt(0)
	v_lshl_add_u32 v106, v104, 7, v2
	v_lshl_add_u32 v107, v105, 7, v2
	global_load_dwordx4 v[72:75], v106, s[18:19]
	global_load_dwordx4 v[76:79], v107, s[18:19]
	ds_bpermute_b32 v104, v3, v20 offset:192
	ds_bpermute_b32 v105, v3, v24 offset:192
	s_waitcnt lgkmcnt(0)
	v_lshl_add_u32 v106, v104, 7, v2
	v_lshl_add_u32 v107, v105, 7, v2
	global_load_dwordx4 v[80:83], v106, s[18:19]
	global_load_dwordx4 v[84:87], v107, s[18:19]
	ds_bpermute_b32 v104, v3, v20 offset:224
	ds_bpermute_b32 v105, v3, v24 offset:224
	s_waitcnt lgkmcnt(0)
	v_lshl_add_u32 v106, v104, 7, v2
	v_lshl_add_u32 v107, v105, 7, v2
	global_load_dwordx4 v[88:91], v106, s[18:19]
	global_load_dwordx4 v[92:95], v107, s[18:19]
	ds_bpermute_b32 v104, v3, v21
	ds_bpermute_b32 v105, v3, v25
	s_waitcnt vmcnt(14)
	v_mov_b32_e32 v96, 0
	v_dot4c_i32_i8_e32 v96, v32, v36
	v_cvt_f32_i32_sdwa v98, sext(v32) dst_sel:DWORD dst_unused:UNUSED_PAD src0_sel:BYTE_0
	v_cvt_f32_i32_sdwa v99, sext(v33) dst_sel:DWORD dst_unused:UNUSED_PAD src0_sel:BYTE_0
	v_dot4c_i32_i8_e32 v96, v33, v37
	v_cvt_f32_i32_sdwa v100, sext(v34) dst_sel:DWORD dst_unused:UNUSED_PAD src0_sel:BYTE_0
	v_dot4c_i32_i8_e32 v96, v34, v38
	v_cvt_f32_i32_sdwa v101, sext(v35) dst_sel:DWORD dst_unused:UNUSED_PAD src0_sel:BYTE_0
	v_dot4c_i32_i8_e32 v96, v35, v39
	v_fma_f32 v97, v98, v4, 0
	v_cvt_f32_i32_sdwa v98, sext(v32) dst_sel:DWORD dst_unused:UNUSED_PAD src0_sel:BYTE_1
	v_fmac_f32_e32 v97, v99, v8
	v_cvt_f32_i32_sdwa v99, sext(v33) dst_sel:DWORD dst_unused:UNUSED_PAD src0_sel:BYTE_1
	v_fmac_f32_e32 v97, v100, v12
	v_cvt_f32_i32_sdwa v100, sext(v34) dst_sel:DWORD dst_unused:UNUSED_PAD src0_sel:BYTE_1
	v_fmac_f32_e32 v97, v101, v16
	v_cvt_f32_i32_sdwa v101, sext(v35) dst_sel:DWORD dst_unused:UNUSED_PAD src0_sel:BYTE_1
	v_add_u32_dpp v96, v96, v96 quad_perm:[1,0,3,2] row_mask:0xf bank_mask:0xf bound_ctrl:1
	v_fmac_f32_e32 v97, v98, v5
	v_cvt_f32_i32_sdwa v98, sext(v32) dst_sel:DWORD dst_unused:UNUSED_PAD src0_sel:BYTE_2
	v_fmac_f32_e32 v97, v99, v9
	v_cvt_f32_i32_sdwa v99, sext(v33) dst_sel:DWORD dst_unused:UNUSED_PAD src0_sel:BYTE_2
	v_fmac_f32_e32 v97, v100, v13
	v_cvt_f32_i32_sdwa v100, sext(v34) dst_sel:DWORD dst_unused:UNUSED_PAD src0_sel:BYTE_2
	v_add_u32_dpp v96, v96, v96 quad_perm:[2,3,0,1] row_mask:0xf bank_mask:0xf bound_ctrl:1
	v_fmac_f32_e32 v97, v101, v17
	v_cvt_f32_i32_sdwa v101, sext(v35) dst_sel:DWORD dst_unused:UNUSED_PAD src0_sel:BYTE_2
	v_fmac_f32_e32 v97, v98, v6
	v_cvt_f32_i32_sdwa v98, sext(v32) dst_sel:DWORD dst_unused:UNUSED_PAD src0_sel:BYTE_3
	v_fmac_f32_e32 v97, v99, v10
	v_cvt_f32_i32_sdwa v99, sext(v33) dst_sel:DWORD dst_unused:UNUSED_PAD src0_sel:BYTE_3
	v_add_u32_dpp v96, v96, v96 row_half_mirror row_mask:0xf bank_mask:0xf bound_ctrl:1
	v_fmac_f32_e32 v97, v100, v14
	v_cvt_f32_i32_sdwa v100, sext(v34) dst_sel:DWORD dst_unused:UNUSED_PAD src0_sel:BYTE_3
	v_fmac_f32_e32 v97, v101, v18
	v_cvt_f32_i32_sdwa v101, sext(v35) dst_sel:DWORD dst_unused:UNUSED_PAD src0_sel:BYTE_3
	v_fmac_f32_e32 v97, v98, v7
	v_fmac_f32_e32 v97, v99, v11
	v_fmac_f32_e32 v97, v100, v15
	v_fmac_f32_e32 v97, v101, v19
	v_cndmask_b32_e64 v102, 0, v96, s[40:41]
	s_waitcnt lgkmcnt(0)
	v_add_f32_dpp v97, v97, v97 quad_perm:[1,0,3,2] row_mask:0xf bank_mask:0xf bound_ctrl:1
	v_lshl_add_u32 v106, v104, 7, v2
	v_lshl_add_u32 v107, v105, 7, v2
	v_add_f32_dpp v97, v97, v97 quad_perm:[2,3,0,1] row_mask:0xf bank_mask:0xf bound_ctrl:1
	global_load_dwordx4 v[32:35], v106, s[18:19]
	global_load_dwordx4 v[36:39], v107, s[18:19]
	v_add_f32_dpp v97, v97, v97 row_half_mirror row_mask:0xf bank_mask:0xf bound_ctrl:1
	v_cndmask_b32_e64 v103, 0, v97, s[40:41]
	ds_bpermute_b32 v104, v3, v21 offset:32
	ds_bpermute_b32 v105, v3, v25 offset:32
	s_waitcnt vmcnt(14)
	v_mov_b32_e32 v96, 0
	v_dot4c_i32_i8_e32 v96, v40, v44
	v_cvt_f32_i32_sdwa v98, sext(v40) dst_sel:DWORD dst_unused:UNUSED_PAD src0_sel:BYTE_0
	v_cvt_f32_i32_sdwa v99, sext(v41) dst_sel:DWORD dst_unused:UNUSED_PAD src0_sel:BYTE_0
	v_dot4c_i32_i8_e32 v96, v41, v45
	v_cvt_f32_i32_sdwa v100, sext(v42) dst_sel:DWORD dst_unused:UNUSED_PAD src0_sel:BYTE_0
	v_dot4c_i32_i8_e32 v96, v42, v46
	v_cvt_f32_i32_sdwa v101, sext(v43) dst_sel:DWORD dst_unused:UNUSED_PAD src0_sel:BYTE_0
	v_dot4c_i32_i8_e32 v96, v43, v47
	v_fma_f32 v97, v98, v4, 0
	v_cvt_f32_i32_sdwa v98, sext(v40) dst_sel:DWORD dst_unused:UNUSED_PAD src0_sel:BYTE_1
	v_fmac_f32_e32 v97, v99, v8
	v_cvt_f32_i32_sdwa v99, sext(v41) dst_sel:DWORD dst_unused:UNUSED_PAD src0_sel:BYTE_1
	v_fmac_f32_e32 v97, v100, v12
	v_cvt_f32_i32_sdwa v100, sext(v42) dst_sel:DWORD dst_unused:UNUSED_PAD src0_sel:BYTE_1
	v_fmac_f32_e32 v97, v101, v16
	v_cvt_f32_i32_sdwa v101, sext(v43) dst_sel:DWORD dst_unused:UNUSED_PAD src0_sel:BYTE_1
	v_add_u32_dpp v96, v96, v96 quad_perm:[1,0,3,2] row_mask:0xf bank_mask:0xf bound_ctrl:1
	v_fmac_f32_e32 v97, v98, v5
	v_cvt_f32_i32_sdwa v98, sext(v40) dst_sel:DWORD dst_unused:UNUSED_PAD src0_sel:BYTE_2
	v_fmac_f32_e32 v97, v99, v9
	v_cvt_f32_i32_sdwa v99, sext(v41) dst_sel:DWORD dst_unused:UNUSED_PAD src0_sel:BYTE_2
	v_fmac_f32_e32 v97, v100, v13
	v_cvt_f32_i32_sdwa v100, sext(v42) dst_sel:DWORD dst_unused:UNUSED_PAD src0_sel:BYTE_2
	v_add_u32_dpp v96, v96, v96 quad_perm:[2,3,0,1] row_mask:0xf bank_mask:0xf bound_ctrl:1
	v_fmac_f32_e32 v97, v101, v17
	v_cvt_f32_i32_sdwa v101, sext(v43) dst_sel:DWORD dst_unused:UNUSED_PAD src0_sel:BYTE_2
	v_fmac_f32_e32 v97, v98, v6
	v_cvt_f32_i32_sdwa v98, sext(v40) dst_sel:DWORD dst_unused:UNUSED_PAD src0_sel:BYTE_3
	v_fmac_f32_e32 v97, v99, v10
	v_cvt_f32_i32_sdwa v99, sext(v41) dst_sel:DWORD dst_unused:UNUSED_PAD src0_sel:BYTE_3
	v_add_u32_dpp v96, v96, v96 row_half_mirror row_mask:0xf bank_mask:0xf bound_ctrl:1
	v_fmac_f32_e32 v97, v100, v14
	v_cvt_f32_i32_sdwa v100, sext(v42) dst_sel:DWORD dst_unused:UNUSED_PAD src0_sel:BYTE_3
	v_fmac_f32_e32 v97, v101, v18
	v_cvt_f32_i32_sdwa v101, sext(v43) dst_sel:DWORD dst_unused:UNUSED_PAD src0_sel:BYTE_3
	v_fmac_f32_e32 v97, v98, v7
	v_fmac_f32_e32 v97, v99, v11
	v_fmac_f32_e32 v97, v100, v15
	v_fmac_f32_e32 v97, v101, v19
	v_cndmask_b32_e64 v102, v102, v96, s[42:43]
	s_waitcnt lgkmcnt(0)
	v_add_f32_dpp v97, v97, v97 quad_perm:[1,0,3,2] row_mask:0xf bank_mask:0xf bound_ctrl:1
	v_lshl_add_u32 v106, v104, 7, v2
	v_lshl_add_u32 v107, v105, 7, v2
	v_add_f32_dpp v97, v97, v97 quad_perm:[2,3,0,1] row_mask:0xf bank_mask:0xf bound_ctrl:1
	global_load_dwordx4 v[40:43], v106, s[18:19]
	global_load_dwordx4 v[44:47], v107, s[18:19]
	v_add_f32_dpp v97, v97, v97 row_half_mirror row_mask:0xf bank_mask:0xf bound_ctrl:1
	v_cndmask_b32_e64 v103, v103, v97, s[42:43]
	ds_bpermute_b32 v104, v3, v21 offset:64
	ds_bpermute_b32 v105, v3, v25 offset:64
	s_waitcnt vmcnt(14)
	v_mov_b32_e32 v96, 0
	v_dot4c_i32_i8_e32 v96, v48, v52
	v_cvt_f32_i32_sdwa v98, sext(v48) dst_sel:DWORD dst_unused:UNUSED_PAD src0_sel:BYTE_0
	v_cvt_f32_i32_sdwa v99, sext(v49) dst_sel:DWORD dst_unused:UNUSED_PAD src0_sel:BYTE_0
	v_dot4c_i32_i8_e32 v96, v49, v53
	v_cvt_f32_i32_sdwa v100, sext(v50) dst_sel:DWORD dst_unused:UNUSED_PAD src0_sel:BYTE_0
	v_dot4c_i32_i8_e32 v96, v50, v54
	v_cvt_f32_i32_sdwa v101, sext(v51) dst_sel:DWORD dst_unused:UNUSED_PAD src0_sel:BYTE_0
	v_dot4c_i32_i8_e32 v96, v51, v55
	v_fma_f32 v97, v98, v4, 0
	v_cvt_f32_i32_sdwa v98, sext(v48) dst_sel:DWORD dst_unused:UNUSED_PAD src0_sel:BYTE_1
	v_fmac_f32_e32 v97, v99, v8
	v_cvt_f32_i32_sdwa v99, sext(v49) dst_sel:DWORD dst_unused:UNUSED_PAD src0_sel:BYTE_1
	v_fmac_f32_e32 v97, v100, v12
	v_cvt_f32_i32_sdwa v100, sext(v50) dst_sel:DWORD dst_unused:UNUSED_PAD src0_sel:BYTE_1
	v_fmac_f32_e32 v97, v101, v16
	v_cvt_f32_i32_sdwa v101, sext(v51) dst_sel:DWORD dst_unused:UNUSED_PAD src0_sel:BYTE_1
	v_add_u32_dpp v96, v96, v96 quad_perm:[1,0,3,2] row_mask:0xf bank_mask:0xf bound_ctrl:1
	v_fmac_f32_e32 v97, v98, v5
	v_cvt_f32_i32_sdwa v98, sext(v48) dst_sel:DWORD dst_unused:UNUSED_PAD src0_sel:BYTE_2
	v_fmac_f32_e32 v97, v99, v9
	v_cvt_f32_i32_sdwa v99, sext(v49) dst_sel:DWORD dst_unused:UNUSED_PAD src0_sel:BYTE_2
	v_fmac_f32_e32 v97, v100, v13
	v_cvt_f32_i32_sdwa v100, sext(v50) dst_sel:DWORD dst_unused:UNUSED_PAD src0_sel:BYTE_2
	v_add_u32_dpp v96, v96, v96 quad_perm:[2,3,0,1] row_mask:0xf bank_mask:0xf bound_ctrl:1
	v_fmac_f32_e32 v97, v101, v17
	v_cvt_f32_i32_sdwa v101, sext(v51) dst_sel:DWORD dst_unused:UNUSED_PAD src0_sel:BYTE_2
	v_fmac_f32_e32 v97, v98, v6
	v_cvt_f32_i32_sdwa v98, sext(v48) dst_sel:DWORD dst_unused:UNUSED_PAD src0_sel:BYTE_3
	v_fmac_f32_e32 v97, v99, v10
	v_cvt_f32_i32_sdwa v99, sext(v49) dst_sel:DWORD dst_unused:UNUSED_PAD src0_sel:BYTE_3
	v_add_u32_dpp v96, v96, v96 row_half_mirror row_mask:0xf bank_mask:0xf bound_ctrl:1
	v_fmac_f32_e32 v97, v100, v14
	v_cvt_f32_i32_sdwa v100, sext(v50) dst_sel:DWORD dst_unused:UNUSED_PAD src0_sel:BYTE_3
	v_fmac_f32_e32 v97, v101, v18
	v_cvt_f32_i32_sdwa v101, sext(v51) dst_sel:DWORD dst_unused:UNUSED_PAD src0_sel:BYTE_3
	v_fmac_f32_e32 v97, v98, v7
	v_fmac_f32_e32 v97, v99, v11
	v_fmac_f32_e32 v97, v100, v15
	v_fmac_f32_e32 v97, v101, v19
	v_cndmask_b32_e64 v102, v102, v96, s[44:45]
	s_waitcnt lgkmcnt(0)
	v_add_f32_dpp v97, v97, v97 quad_perm:[1,0,3,2] row_mask:0xf bank_mask:0xf bound_ctrl:1
	v_lshl_add_u32 v106, v104, 7, v2
	v_lshl_add_u32 v107, v105, 7, v2
	v_add_f32_dpp v97, v97, v97 quad_perm:[2,3,0,1] row_mask:0xf bank_mask:0xf bound_ctrl:1
	global_load_dwordx4 v[48:51], v106, s[18:19]
	global_load_dwordx4 v[52:55], v107, s[18:19]
	v_add_f32_dpp v97, v97, v97 row_half_mirror row_mask:0xf bank_mask:0xf bound_ctrl:1
	v_cndmask_b32_e64 v103, v103, v97, s[44:45]
	ds_bpermute_b32 v104, v3, v21 offset:96
	ds_bpermute_b32 v105, v3, v25 offset:96
	s_waitcnt vmcnt(14)
	v_mov_b32_e32 v96, 0
	v_dot4c_i32_i8_e32 v96, v56, v60
	v_cvt_f32_i32_sdwa v98, sext(v56) dst_sel:DWORD dst_unused:UNUSED_PAD src0_sel:BYTE_0
	v_cvt_f32_i32_sdwa v99, sext(v57) dst_sel:DWORD dst_unused:UNUSED_PAD src0_sel:BYTE_0
	v_dot4c_i32_i8_e32 v96, v57, v61
	v_cvt_f32_i32_sdwa v100, sext(v58) dst_sel:DWORD dst_unused:UNUSED_PAD src0_sel:BYTE_0
	v_dot4c_i32_i8_e32 v96, v58, v62
	v_cvt_f32_i32_sdwa v101, sext(v59) dst_sel:DWORD dst_unused:UNUSED_PAD src0_sel:BYTE_0
	v_dot4c_i32_i8_e32 v96, v59, v63
	v_fma_f32 v97, v98, v4, 0
	v_cvt_f32_i32_sdwa v98, sext(v56) dst_sel:DWORD dst_unused:UNUSED_PAD src0_sel:BYTE_1
	v_fmac_f32_e32 v97, v99, v8
	v_cvt_f32_i32_sdwa v99, sext(v57) dst_sel:DWORD dst_unused:UNUSED_PAD src0_sel:BYTE_1
	v_fmac_f32_e32 v97, v100, v12
	v_cvt_f32_i32_sdwa v100, sext(v58) dst_sel:DWORD dst_unused:UNUSED_PAD src0_sel:BYTE_1
	v_fmac_f32_e32 v97, v101, v16
	v_cvt_f32_i32_sdwa v101, sext(v59) dst_sel:DWORD dst_unused:UNUSED_PAD src0_sel:BYTE_1
	v_add_u32_dpp v96, v96, v96 quad_perm:[1,0,3,2] row_mask:0xf bank_mask:0xf bound_ctrl:1
	v_fmac_f32_e32 v97, v98, v5
	v_cvt_f32_i32_sdwa v98, sext(v56) dst_sel:DWORD dst_unused:UNUSED_PAD src0_sel:BYTE_2
	v_fmac_f32_e32 v97, v99, v9
	v_cvt_f32_i32_sdwa v99, sext(v57) dst_sel:DWORD dst_unused:UNUSED_PAD src0_sel:BYTE_2
	v_fmac_f32_e32 v97, v100, v13
	v_cvt_f32_i32_sdwa v100, sext(v58) dst_sel:DWORD dst_unused:UNUSED_PAD src0_sel:BYTE_2
	v_add_u32_dpp v96, v96, v96 quad_perm:[2,3,0,1] row_mask:0xf bank_mask:0xf bound_ctrl:1
	v_fmac_f32_e32 v97, v101, v17
	v_cvt_f32_i32_sdwa v101, sext(v59) dst_sel:DWORD dst_unused:UNUSED_PAD src0_sel:BYTE_2
	v_fmac_f32_e32 v97, v98, v6
	v_cvt_f32_i32_sdwa v98, sext(v56) dst_sel:DWORD dst_unused:UNUSED_PAD src0_sel:BYTE_3
	v_fmac_f32_e32 v97, v99, v10
	v_cvt_f32_i32_sdwa v99, sext(v57) dst_sel:DWORD dst_unused:UNUSED_PAD src0_sel:BYTE_3
	v_add_u32_dpp v96, v96, v96 row_half_mirror row_mask:0xf bank_mask:0xf bound_ctrl:1
	v_fmac_f32_e32 v97, v100, v14
	v_cvt_f32_i32_sdwa v100, sext(v58) dst_sel:DWORD dst_unused:UNUSED_PAD src0_sel:BYTE_3
	v_fmac_f32_e32 v97, v101, v18
	v_cvt_f32_i32_sdwa v101, sext(v59) dst_sel:DWORD dst_unused:UNUSED_PAD src0_sel:BYTE_3
	v_fmac_f32_e32 v97, v98, v7
	v_fmac_f32_e32 v97, v99, v11
	v_fmac_f32_e32 v97, v100, v15
	v_fmac_f32_e32 v97, v101, v19
	v_cndmask_b32_e64 v102, v102, v96, s[46:47]
	s_waitcnt lgkmcnt(0)
	v_add_f32_dpp v97, v97, v97 quad_perm:[1,0,3,2] row_mask:0xf bank_mask:0xf bound_ctrl:1
	v_lshl_add_u32 v106, v104, 7, v2
	v_lshl_add_u32 v107, v105, 7, v2
	v_add_f32_dpp v97, v97, v97 quad_perm:[2,3,0,1] row_mask:0xf bank_mask:0xf bound_ctrl:1
	global_load_dwordx4 v[56:59], v106, s[18:19]
	global_load_dwordx4 v[60:63], v107, s[18:19]
	v_add_f32_dpp v97, v97, v97 row_half_mirror row_mask:0xf bank_mask:0xf bound_ctrl:1
	v_cndmask_b32_e64 v103, v103, v97, s[46:47]
	ds_bpermute_b32 v104, v3, v21 offset:128
	ds_bpermute_b32 v105, v3, v25 offset:128
	s_waitcnt vmcnt(14)
	v_mov_b32_e32 v96, 0
	v_dot4c_i32_i8_e32 v96, v64, v68
	v_cvt_f32_i32_sdwa v98, sext(v64) dst_sel:DWORD dst_unused:UNUSED_PAD src0_sel:BYTE_0
	v_cvt_f32_i32_sdwa v99, sext(v65) dst_sel:DWORD dst_unused:UNUSED_PAD src0_sel:BYTE_0
	v_dot4c_i32_i8_e32 v96, v65, v69
	v_cvt_f32_i32_sdwa v100, sext(v66) dst_sel:DWORD dst_unused:UNUSED_PAD src0_sel:BYTE_0
	v_dot4c_i32_i8_e32 v96, v66, v70
	v_cvt_f32_i32_sdwa v101, sext(v67) dst_sel:DWORD dst_unused:UNUSED_PAD src0_sel:BYTE_0
	v_dot4c_i32_i8_e32 v96, v67, v71
	v_fma_f32 v97, v98, v4, 0
	v_cvt_f32_i32_sdwa v98, sext(v64) dst_sel:DWORD dst_unused:UNUSED_PAD src0_sel:BYTE_1
	v_fmac_f32_e32 v97, v99, v8
	v_cvt_f32_i32_sdwa v99, sext(v65) dst_sel:DWORD dst_unused:UNUSED_PAD src0_sel:BYTE_1
	v_fmac_f32_e32 v97, v100, v12
	v_cvt_f32_i32_sdwa v100, sext(v66) dst_sel:DWORD dst_unused:UNUSED_PAD src0_sel:BYTE_1
	v_fmac_f32_e32 v97, v101, v16
	v_cvt_f32_i32_sdwa v101, sext(v67) dst_sel:DWORD dst_unused:UNUSED_PAD src0_sel:BYTE_1
	v_add_u32_dpp v96, v96, v96 quad_perm:[1,0,3,2] row_mask:0xf bank_mask:0xf bound_ctrl:1
	v_fmac_f32_e32 v97, v98, v5
	v_cvt_f32_i32_sdwa v98, sext(v64) dst_sel:DWORD dst_unused:UNUSED_PAD src0_sel:BYTE_2
	v_fmac_f32_e32 v97, v99, v9
	v_cvt_f32_i32_sdwa v99, sext(v65) dst_sel:DWORD dst_unused:UNUSED_PAD src0_sel:BYTE_2
	v_fmac_f32_e32 v97, v100, v13
	v_cvt_f32_i32_sdwa v100, sext(v66) dst_sel:DWORD dst_unused:UNUSED_PAD src0_sel:BYTE_2
	v_add_u32_dpp v96, v96, v96 quad_perm:[2,3,0,1] row_mask:0xf bank_mask:0xf bound_ctrl:1
	v_fmac_f32_e32 v97, v101, v17
	v_cvt_f32_i32_sdwa v101, sext(v67) dst_sel:DWORD dst_unused:UNUSED_PAD src0_sel:BYTE_2
	v_fmac_f32_e32 v97, v98, v6
	v_cvt_f32_i32_sdwa v98, sext(v64) dst_sel:DWORD dst_unused:UNUSED_PAD src0_sel:BYTE_3
	v_fmac_f32_e32 v97, v99, v10
	v_cvt_f32_i32_sdwa v99, sext(v65) dst_sel:DWORD dst_unused:UNUSED_PAD src0_sel:BYTE_3
	v_add_u32_dpp v96, v96, v96 row_half_mirror row_mask:0xf bank_mask:0xf bound_ctrl:1
	v_fmac_f32_e32 v97, v100, v14
	v_cvt_f32_i32_sdwa v100, sext(v66) dst_sel:DWORD dst_unused:UNUSED_PAD src0_sel:BYTE_3
	v_fmac_f32_e32 v97, v101, v18
	v_cvt_f32_i32_sdwa v101, sext(v67) dst_sel:DWORD dst_unused:UNUSED_PAD src0_sel:BYTE_3
	v_fmac_f32_e32 v97, v98, v7
	v_fmac_f32_e32 v97, v99, v11
	v_fmac_f32_e32 v97, v100, v15
	v_fmac_f32_e32 v97, v101, v19
	v_cndmask_b32_e64 v102, v102, v96, s[48:49]
	s_waitcnt lgkmcnt(0)
	v_add_f32_dpp v97, v97, v97 quad_perm:[1,0,3,2] row_mask:0xf bank_mask:0xf bound_ctrl:1
	v_lshl_add_u32 v106, v104, 7, v2
	v_lshl_add_u32 v107, v105, 7, v2
	v_add_f32_dpp v97, v97, v97 quad_perm:[2,3,0,1] row_mask:0xf bank_mask:0xf bound_ctrl:1
	global_load_dwordx4 v[64:67], v106, s[18:19]
	global_load_dwordx4 v[68:71], v107, s[18:19]
	v_add_f32_dpp v97, v97, v97 row_half_mirror row_mask:0xf bank_mask:0xf bound_ctrl:1
	v_cndmask_b32_e64 v103, v103, v97, s[48:49]
	ds_bpermute_b32 v104, v3, v21 offset:160
	ds_bpermute_b32 v105, v3, v25 offset:160
	s_waitcnt vmcnt(14)
	v_mov_b32_e32 v96, 0
	v_dot4c_i32_i8_e32 v96, v72, v76
	v_cvt_f32_i32_sdwa v98, sext(v72) dst_sel:DWORD dst_unused:UNUSED_PAD src0_sel:BYTE_0
	v_cvt_f32_i32_sdwa v99, sext(v73) dst_sel:DWORD dst_unused:UNUSED_PAD src0_sel:BYTE_0
	v_dot4c_i32_i8_e32 v96, v73, v77
	v_cvt_f32_i32_sdwa v100, sext(v74) dst_sel:DWORD dst_unused:UNUSED_PAD src0_sel:BYTE_0
	v_dot4c_i32_i8_e32 v96, v74, v78
	v_cvt_f32_i32_sdwa v101, sext(v75) dst_sel:DWORD dst_unused:UNUSED_PAD src0_sel:BYTE_0
	v_dot4c_i32_i8_e32 v96, v75, v79
	v_fma_f32 v97, v98, v4, 0
	v_cvt_f32_i32_sdwa v98, sext(v72) dst_sel:DWORD dst_unused:UNUSED_PAD src0_sel:BYTE_1
	v_fmac_f32_e32 v97, v99, v8
	v_cvt_f32_i32_sdwa v99, sext(v73) dst_sel:DWORD dst_unused:UNUSED_PAD src0_sel:BYTE_1
	v_fmac_f32_e32 v97, v100, v12
	v_cvt_f32_i32_sdwa v100, sext(v74) dst_sel:DWORD dst_unused:UNUSED_PAD src0_sel:BYTE_1
	v_fmac_f32_e32 v97, v101, v16
	v_cvt_f32_i32_sdwa v101, sext(v75) dst_sel:DWORD dst_unused:UNUSED_PAD src0_sel:BYTE_1
	v_add_u32_dpp v96, v96, v96 quad_perm:[1,0,3,2] row_mask:0xf bank_mask:0xf bound_ctrl:1
	v_fmac_f32_e32 v97, v98, v5
	v_cvt_f32_i32_sdwa v98, sext(v72) dst_sel:DWORD dst_unused:UNUSED_PAD src0_sel:BYTE_2
	v_fmac_f32_e32 v97, v99, v9
	v_cvt_f32_i32_sdwa v99, sext(v73) dst_sel:DWORD dst_unused:UNUSED_PAD src0_sel:BYTE_2
	v_fmac_f32_e32 v97, v100, v13
	v_cvt_f32_i32_sdwa v100, sext(v74) dst_sel:DWORD dst_unused:UNUSED_PAD src0_sel:BYTE_2
	v_add_u32_dpp v96, v96, v96 quad_perm:[2,3,0,1] row_mask:0xf bank_mask:0xf bound_ctrl:1
	v_fmac_f32_e32 v97, v101, v17
	v_cvt_f32_i32_sdwa v101, sext(v75) dst_sel:DWORD dst_unused:UNUSED_PAD src0_sel:BYTE_2
	v_fmac_f32_e32 v97, v98, v6
	v_cvt_f32_i32_sdwa v98, sext(v72) dst_sel:DWORD dst_unused:UNUSED_PAD src0_sel:BYTE_3
	v_fmac_f32_e32 v97, v99, v10
	v_cvt_f32_i32_sdwa v99, sext(v73) dst_sel:DWORD dst_unused:UNUSED_PAD src0_sel:BYTE_3
	v_add_u32_dpp v96, v96, v96 row_half_mirror row_mask:0xf bank_mask:0xf bound_ctrl:1
	v_fmac_f32_e32 v97, v100, v14
	v_cvt_f32_i32_sdwa v100, sext(v74) dst_sel:DWORD dst_unused:UNUSED_PAD src0_sel:BYTE_3
	v_fmac_f32_e32 v97, v101, v18
	v_cvt_f32_i32_sdwa v101, sext(v75) dst_sel:DWORD dst_unused:UNUSED_PAD src0_sel:BYTE_3
	v_fmac_f32_e32 v97, v98, v7
	v_fmac_f32_e32 v97, v99, v11
	v_fmac_f32_e32 v97, v100, v15
	v_fmac_f32_e32 v97, v101, v19
	v_cndmask_b32_e64 v102, v102, v96, s[50:51]
	s_waitcnt lgkmcnt(0)
	v_add_f32_dpp v97, v97, v97 quad_perm:[1,0,3,2] row_mask:0xf bank_mask:0xf bound_ctrl:1
	v_lshl_add_u32 v106, v104, 7, v2
	v_lshl_add_u32 v107, v105, 7, v2
	v_add_f32_dpp v97, v97, v97 quad_perm:[2,3,0,1] row_mask:0xf bank_mask:0xf bound_ctrl:1
	global_load_dwordx4 v[72:75], v106, s[18:19]
	global_load_dwordx4 v[76:79], v107, s[18:19]
	v_add_f32_dpp v97, v97, v97 row_half_mirror row_mask:0xf bank_mask:0xf bound_ctrl:1
	v_cndmask_b32_e64 v103, v103, v97, s[50:51]
	ds_bpermute_b32 v104, v3, v21 offset:192
	ds_bpermute_b32 v105, v3, v25 offset:192
	s_waitcnt vmcnt(14)
	v_mov_b32_e32 v96, 0
	v_dot4c_i32_i8_e32 v96, v80, v84
	v_cvt_f32_i32_sdwa v98, sext(v80) dst_sel:DWORD dst_unused:UNUSED_PAD src0_sel:BYTE_0
	v_cvt_f32_i32_sdwa v99, sext(v81) dst_sel:DWORD dst_unused:UNUSED_PAD src0_sel:BYTE_0
	v_dot4c_i32_i8_e32 v96, v81, v85
	v_cvt_f32_i32_sdwa v100, sext(v82) dst_sel:DWORD dst_unused:UNUSED_PAD src0_sel:BYTE_0
	v_dot4c_i32_i8_e32 v96, v82, v86
	v_cvt_f32_i32_sdwa v101, sext(v83) dst_sel:DWORD dst_unused:UNUSED_PAD src0_sel:BYTE_0
	v_dot4c_i32_i8_e32 v96, v83, v87
	v_fma_f32 v97, v98, v4, 0
	v_cvt_f32_i32_sdwa v98, sext(v80) dst_sel:DWORD dst_unused:UNUSED_PAD src0_sel:BYTE_1
	v_fmac_f32_e32 v97, v99, v8
	v_cvt_f32_i32_sdwa v99, sext(v81) dst_sel:DWORD dst_unused:UNUSED_PAD src0_sel:BYTE_1
	v_fmac_f32_e32 v97, v100, v12
	v_cvt_f32_i32_sdwa v100, sext(v82) dst_sel:DWORD dst_unused:UNUSED_PAD src0_sel:BYTE_1
	v_fmac_f32_e32 v97, v101, v16
	v_cvt_f32_i32_sdwa v101, sext(v83) dst_sel:DWORD dst_unused:UNUSED_PAD src0_sel:BYTE_1
	v_add_u32_dpp v96, v96, v96 quad_perm:[1,0,3,2] row_mask:0xf bank_mask:0xf bound_ctrl:1
	v_fmac_f32_e32 v97, v98, v5
	v_cvt_f32_i32_sdwa v98, sext(v80) dst_sel:DWORD dst_unused:UNUSED_PAD src0_sel:BYTE_2
	v_fmac_f32_e32 v97, v99, v9
	v_cvt_f32_i32_sdwa v99, sext(v81) dst_sel:DWORD dst_unused:UNUSED_PAD src0_sel:BYTE_2
	v_fmac_f32_e32 v97, v100, v13
	v_cvt_f32_i32_sdwa v100, sext(v82) dst_sel:DWORD dst_unused:UNUSED_PAD src0_sel:BYTE_2
	v_add_u32_dpp v96, v96, v96 quad_perm:[2,3,0,1] row_mask:0xf bank_mask:0xf bound_ctrl:1
	v_fmac_f32_e32 v97, v101, v17
	v_cvt_f32_i32_sdwa v101, sext(v83) dst_sel:DWORD dst_unused:UNUSED_PAD src0_sel:BYTE_2
	v_fmac_f32_e32 v97, v98, v6
	v_cvt_f32_i32_sdwa v98, sext(v80) dst_sel:DWORD dst_unused:UNUSED_PAD src0_sel:BYTE_3
	v_fmac_f32_e32 v97, v99, v10
	v_cvt_f32_i32_sdwa v99, sext(v81) dst_sel:DWORD dst_unused:UNUSED_PAD src0_sel:BYTE_3
	v_add_u32_dpp v96, v96, v96 row_half_mirror row_mask:0xf bank_mask:0xf bound_ctrl:1
	v_fmac_f32_e32 v97, v100, v14
	v_cvt_f32_i32_sdwa v100, sext(v82) dst_sel:DWORD dst_unused:UNUSED_PAD src0_sel:BYTE_3
	v_fmac_f32_e32 v97, v101, v18
	v_cvt_f32_i32_sdwa v101, sext(v83) dst_sel:DWORD dst_unused:UNUSED_PAD src0_sel:BYTE_3
	v_fmac_f32_e32 v97, v98, v7
	v_fmac_f32_e32 v97, v99, v11
	v_fmac_f32_e32 v97, v100, v15
	v_fmac_f32_e32 v97, v101, v19
	v_cndmask_b32_e64 v102, v102, v96, s[52:53]
	s_waitcnt lgkmcnt(0)
	v_add_f32_dpp v97, v97, v97 quad_perm:[1,0,3,2] row_mask:0xf bank_mask:0xf bound_ctrl:1
	v_lshl_add_u32 v106, v104, 7, v2
	v_lshl_add_u32 v107, v105, 7, v2
	v_add_f32_dpp v97, v97, v97 quad_perm:[2,3,0,1] row_mask:0xf bank_mask:0xf bound_ctrl:1
	global_load_dwordx4 v[80:83], v106, s[18:19]
	global_load_dwordx4 v[84:87], v107, s[18:19]
	v_add_f32_dpp v97, v97, v97 row_half_mirror row_mask:0xf bank_mask:0xf bound_ctrl:1
	v_cndmask_b32_e64 v103, v103, v97, s[52:53]
	ds_bpermute_b32 v104, v3, v21 offset:224
	ds_bpermute_b32 v105, v3, v25 offset:224
	s_waitcnt vmcnt(14)
	v_mov_b32_e32 v96, 0
	v_dot4c_i32_i8_e32 v96, v88, v92
	v_cvt_f32_i32_sdwa v98, sext(v88) dst_sel:DWORD dst_unused:UNUSED_PAD src0_sel:BYTE_0
	v_cvt_f32_i32_sdwa v99, sext(v89) dst_sel:DWORD dst_unused:UNUSED_PAD src0_sel:BYTE_0
	v_dot4c_i32_i8_e32 v96, v89, v93
	v_cvt_f32_i32_sdwa v100, sext(v90) dst_sel:DWORD dst_unused:UNUSED_PAD src0_sel:BYTE_0
	v_dot4c_i32_i8_e32 v96, v90, v94
	v_cvt_f32_i32_sdwa v101, sext(v91) dst_sel:DWORD dst_unused:UNUSED_PAD src0_sel:BYTE_0
	v_dot4c_i32_i8_e32 v96, v91, v95
	v_fma_f32 v97, v98, v4, 0
	v_cvt_f32_i32_sdwa v98, sext(v88) dst_sel:DWORD dst_unused:UNUSED_PAD src0_sel:BYTE_1
	v_fmac_f32_e32 v97, v99, v8
	v_cvt_f32_i32_sdwa v99, sext(v89) dst_sel:DWORD dst_unused:UNUSED_PAD src0_sel:BYTE_1
	v_fmac_f32_e32 v97, v100, v12
	v_cvt_f32_i32_sdwa v100, sext(v90) dst_sel:DWORD dst_unused:UNUSED_PAD src0_sel:BYTE_1
	v_fmac_f32_e32 v97, v101, v16
	v_cvt_f32_i32_sdwa v101, sext(v91) dst_sel:DWORD dst_unused:UNUSED_PAD src0_sel:BYTE_1
	v_add_u32_dpp v96, v96, v96 quad_perm:[1,0,3,2] row_mask:0xf bank_mask:0xf bound_ctrl:1
	v_fmac_f32_e32 v97, v98, v5
	v_cvt_f32_i32_sdwa v98, sext(v88) dst_sel:DWORD dst_unused:UNUSED_PAD src0_sel:BYTE_2
	v_fmac_f32_e32 v97, v99, v9
	v_cvt_f32_i32_sdwa v99, sext(v89) dst_sel:DWORD dst_unused:UNUSED_PAD src0_sel:BYTE_2
	v_fmac_f32_e32 v97, v100, v13
	v_cvt_f32_i32_sdwa v100, sext(v90) dst_sel:DWORD dst_unused:UNUSED_PAD src0_sel:BYTE_2
	v_add_u32_dpp v96, v96, v96 quad_perm:[2,3,0,1] row_mask:0xf bank_mask:0xf bound_ctrl:1
	v_fmac_f32_e32 v97, v101, v17
	v_cvt_f32_i32_sdwa v101, sext(v91) dst_sel:DWORD dst_unused:UNUSED_PAD src0_sel:BYTE_2
	v_fmac_f32_e32 v97, v98, v6
	v_cvt_f32_i32_sdwa v98, sext(v88) dst_sel:DWORD dst_unused:UNUSED_PAD src0_sel:BYTE_3
	v_fmac_f32_e32 v97, v99, v10
	v_cvt_f32_i32_sdwa v99, sext(v89) dst_sel:DWORD dst_unused:UNUSED_PAD src0_sel:BYTE_3
	v_add_u32_dpp v96, v96, v96 row_half_mirror row_mask:0xf bank_mask:0xf bound_ctrl:1
	v_fmac_f32_e32 v97, v100, v14
	v_cvt_f32_i32_sdwa v100, sext(v90) dst_sel:DWORD dst_unused:UNUSED_PAD src0_sel:BYTE_3
	v_fmac_f32_e32 v97, v101, v18
	v_cvt_f32_i32_sdwa v101, sext(v91) dst_sel:DWORD dst_unused:UNUSED_PAD src0_sel:BYTE_3
	v_fmac_f32_e32 v97, v98, v7
	v_fmac_f32_e32 v97, v99, v11
	v_fmac_f32_e32 v97, v100, v15
	v_fmac_f32_e32 v97, v101, v19
	v_cndmask_b32_e64 v102, v102, v96, s[54:55]
	s_waitcnt lgkmcnt(0)
	v_add_f32_dpp v97, v97, v97 quad_perm:[1,0,3,2] row_mask:0xf bank_mask:0xf bound_ctrl:1
	v_lshl_add_u32 v106, v104, 7, v2
	v_lshl_add_u32 v107, v105, 7, v2
	v_add_f32_dpp v97, v97, v97 quad_perm:[2,3,0,1] row_mask:0xf bank_mask:0xf bound_ctrl:1
	global_load_dwordx4 v[88:91], v106, s[18:19]
	global_load_dwordx4 v[92:95], v107, s[18:19]
	v_add_f32_dpp v97, v97, v97 row_half_mirror row_mask:0xf bank_mask:0xf bound_ctrl:1
	v_cndmask_b32_e64 v103, v103, v97, s[54:55]
	global_store_dword v28, v102, s[20:21]
	global_store_dword v28, v103, s[22:23]
	ds_bpermute_b32 v104, v3, v22
	ds_bpermute_b32 v105, v3, v26
	s_waitcnt vmcnt(16)
	v_mov_b32_e32 v96, 0
	v_dot4c_i32_i8_e32 v96, v32, v36
	v_cvt_f32_i32_sdwa v98, sext(v32) dst_sel:DWORD dst_unused:UNUSED_PAD src0_sel:BYTE_0
	v_cvt_f32_i32_sdwa v99, sext(v33) dst_sel:DWORD dst_unused:UNUSED_PAD src0_sel:BYTE_0
	v_dot4c_i32_i8_e32 v96, v33, v37
	v_cvt_f32_i32_sdwa v100, sext(v34) dst_sel:DWORD dst_unused:UNUSED_PAD src0_sel:BYTE_0
	v_dot4c_i32_i8_e32 v96, v34, v38
	v_cvt_f32_i32_sdwa v101, sext(v35) dst_sel:DWORD dst_unused:UNUSED_PAD src0_sel:BYTE_0
	v_dot4c_i32_i8_e32 v96, v35, v39
	v_fma_f32 v97, v98, v4, 0
	v_cvt_f32_i32_sdwa v98, sext(v32) dst_sel:DWORD dst_unused:UNUSED_PAD src0_sel:BYTE_1
	v_fmac_f32_e32 v97, v99, v8
	v_cvt_f32_i32_sdwa v99, sext(v33) dst_sel:DWORD dst_unused:UNUSED_PAD src0_sel:BYTE_1
	v_fmac_f32_e32 v97, v100, v12
	v_cvt_f32_i32_sdwa v100, sext(v34) dst_sel:DWORD dst_unused:UNUSED_PAD src0_sel:BYTE_1
	v_fmac_f32_e32 v97, v101, v16
	v_cvt_f32_i32_sdwa v101, sext(v35) dst_sel:DWORD dst_unused:UNUSED_PAD src0_sel:BYTE_1
	v_add_u32_dpp v96, v96, v96 quad_perm:[1,0,3,2] row_mask:0xf bank_mask:0xf bound_ctrl:1
	v_fmac_f32_e32 v97, v98, v5
	v_cvt_f32_i32_sdwa v98, sext(v32) dst_sel:DWORD dst_unused:UNUSED_PAD src0_sel:BYTE_2
	v_fmac_f32_e32 v97, v99, v9
	v_cvt_f32_i32_sdwa v99, sext(v33) dst_sel:DWORD dst_unused:UNUSED_PAD src0_sel:BYTE_2
	v_fmac_f32_e32 v97, v100, v13
	v_cvt_f32_i32_sdwa v100, sext(v34) dst_sel:DWORD dst_unused:UNUSED_PAD src0_sel:BYTE_2
	v_add_u32_dpp v96, v96, v96 quad_perm:[2,3,0,1] row_mask:0xf bank_mask:0xf bound_ctrl:1
	v_fmac_f32_e32 v97, v101, v17
	v_cvt_f32_i32_sdwa v101, sext(v35) dst_sel:DWORD dst_unused:UNUSED_PAD src0_sel:BYTE_2
	v_fmac_f32_e32 v97, v98, v6
	v_cvt_f32_i32_sdwa v98, sext(v32) dst_sel:DWORD dst_unused:UNUSED_PAD src0_sel:BYTE_3
	v_fmac_f32_e32 v97, v99, v10
	v_cvt_f32_i32_sdwa v99, sext(v33) dst_sel:DWORD dst_unused:UNUSED_PAD src0_sel:BYTE_3
	v_add_u32_dpp v96, v96, v96 row_half_mirror row_mask:0xf bank_mask:0xf bound_ctrl:1
	v_fmac_f32_e32 v97, v100, v14
	v_cvt_f32_i32_sdwa v100, sext(v34) dst_sel:DWORD dst_unused:UNUSED_PAD src0_sel:BYTE_3
	v_fmac_f32_e32 v97, v101, v18
	v_cvt_f32_i32_sdwa v101, sext(v35) dst_sel:DWORD dst_unused:UNUSED_PAD src0_sel:BYTE_3
	v_fmac_f32_e32 v97, v98, v7
	v_fmac_f32_e32 v97, v99, v11
	v_fmac_f32_e32 v97, v100, v15
	v_fmac_f32_e32 v97, v101, v19
	v_cndmask_b32_e64 v102, 0, v96, s[40:41]
	s_waitcnt lgkmcnt(0)
	v_add_f32_dpp v97, v97, v97 quad_perm:[1,0,3,2] row_mask:0xf bank_mask:0xf bound_ctrl:1
	v_lshl_add_u32 v106, v104, 7, v2
	v_lshl_add_u32 v107, v105, 7, v2
	v_add_f32_dpp v97, v97, v97 quad_perm:[2,3,0,1] row_mask:0xf bank_mask:0xf bound_ctrl:1
	global_load_dwordx4 v[32:35], v106, s[18:19]
	global_load_dwordx4 v[36:39], v107, s[18:19]
	v_add_f32_dpp v97, v97, v97 row_half_mirror row_mask:0xf bank_mask:0xf bound_ctrl:1
	v_cndmask_b32_e64 v103, 0, v97, s[40:41]
	ds_bpermute_b32 v104, v3, v22 offset:32
	ds_bpermute_b32 v105, v3, v26 offset:32
	s_waitcnt vmcnt(16)
	v_mov_b32_e32 v96, 0
	v_dot4c_i32_i8_e32 v96, v40, v44
	v_cvt_f32_i32_sdwa v98, sext(v40) dst_sel:DWORD dst_unused:UNUSED_PAD src0_sel:BYTE_0
	v_cvt_f32_i32_sdwa v99, sext(v41) dst_sel:DWORD dst_unused:UNUSED_PAD src0_sel:BYTE_0
	v_dot4c_i32_i8_e32 v96, v41, v45
	v_cvt_f32_i32_sdwa v100, sext(v42) dst_sel:DWORD dst_unused:UNUSED_PAD src0_sel:BYTE_0
	v_dot4c_i32_i8_e32 v96, v42, v46
	v_cvt_f32_i32_sdwa v101, sext(v43) dst_sel:DWORD dst_unused:UNUSED_PAD src0_sel:BYTE_0
	v_dot4c_i32_i8_e32 v96, v43, v47
	v_fma_f32 v97, v98, v4, 0
	v_cvt_f32_i32_sdwa v98, sext(v40) dst_sel:DWORD dst_unused:UNUSED_PAD src0_sel:BYTE_1
	v_fmac_f32_e32 v97, v99, v8
	v_cvt_f32_i32_sdwa v99, sext(v41) dst_sel:DWORD dst_unused:UNUSED_PAD src0_sel:BYTE_1
	v_fmac_f32_e32 v97, v100, v12
	v_cvt_f32_i32_sdwa v100, sext(v42) dst_sel:DWORD dst_unused:UNUSED_PAD src0_sel:BYTE_1
	v_fmac_f32_e32 v97, v101, v16
	v_cvt_f32_i32_sdwa v101, sext(v43) dst_sel:DWORD dst_unused:UNUSED_PAD src0_sel:BYTE_1
	v_add_u32_dpp v96, v96, v96 quad_perm:[1,0,3,2] row_mask:0xf bank_mask:0xf bound_ctrl:1
	v_fmac_f32_e32 v97, v98, v5
	v_cvt_f32_i32_sdwa v98, sext(v40) dst_sel:DWORD dst_unused:UNUSED_PAD src0_sel:BYTE_2
	v_fmac_f32_e32 v97, v99, v9
	v_cvt_f32_i32_sdwa v99, sext(v41) dst_sel:DWORD dst_unused:UNUSED_PAD src0_sel:BYTE_2
	v_fmac_f32_e32 v97, v100, v13
	v_cvt_f32_i32_sdwa v100, sext(v42) dst_sel:DWORD dst_unused:UNUSED_PAD src0_sel:BYTE_2
	v_add_u32_dpp v96, v96, v96 quad_perm:[2,3,0,1] row_mask:0xf bank_mask:0xf bound_ctrl:1
	v_fmac_f32_e32 v97, v101, v17
	v_cvt_f32_i32_sdwa v101, sext(v43) dst_sel:DWORD dst_unused:UNUSED_PAD src0_sel:BYTE_2
	v_fmac_f32_e32 v97, v98, v6
	v_cvt_f32_i32_sdwa v98, sext(v40) dst_sel:DWORD dst_unused:UNUSED_PAD src0_sel:BYTE_3
	v_fmac_f32_e32 v97, v99, v10
	v_cvt_f32_i32_sdwa v99, sext(v41) dst_sel:DWORD dst_unused:UNUSED_PAD src0_sel:BYTE_3
	v_add_u32_dpp v96, v96, v96 row_half_mirror row_mask:0xf bank_mask:0xf bound_ctrl:1
	v_fmac_f32_e32 v97, v100, v14
	v_cvt_f32_i32_sdwa v100, sext(v42) dst_sel:DWORD dst_unused:UNUSED_PAD src0_sel:BYTE_3
	v_fmac_f32_e32 v97, v101, v18
	v_cvt_f32_i32_sdwa v101, sext(v43) dst_sel:DWORD dst_unused:UNUSED_PAD src0_sel:BYTE_3
	v_fmac_f32_e32 v97, v98, v7
	v_fmac_f32_e32 v97, v99, v11
	v_fmac_f32_e32 v97, v100, v15
	v_fmac_f32_e32 v97, v101, v19
	v_cndmask_b32_e64 v102, v102, v96, s[42:43]
	s_waitcnt lgkmcnt(0)
	v_add_f32_dpp v97, v97, v97 quad_perm:[1,0,3,2] row_mask:0xf bank_mask:0xf bound_ctrl:1
	v_lshl_add_u32 v106, v104, 7, v2
	v_lshl_add_u32 v107, v105, 7, v2
	v_add_f32_dpp v97, v97, v97 quad_perm:[2,3,0,1] row_mask:0xf bank_mask:0xf bound_ctrl:1
	global_load_dwordx4 v[40:43], v106, s[18:19]
	global_load_dwordx4 v[44:47], v107, s[18:19]
	v_add_f32_dpp v97, v97, v97 row_half_mirror row_mask:0xf bank_mask:0xf bound_ctrl:1
	v_cndmask_b32_e64 v103, v103, v97, s[42:43]
	ds_bpermute_b32 v104, v3, v22 offset:64
	ds_bpermute_b32 v105, v3, v26 offset:64
	s_waitcnt vmcnt(16)
	v_mov_b32_e32 v96, 0
	v_dot4c_i32_i8_e32 v96, v48, v52
	v_cvt_f32_i32_sdwa v98, sext(v48) dst_sel:DWORD dst_unused:UNUSED_PAD src0_sel:BYTE_0
	v_cvt_f32_i32_sdwa v99, sext(v49) dst_sel:DWORD dst_unused:UNUSED_PAD src0_sel:BYTE_0
	v_dot4c_i32_i8_e32 v96, v49, v53
	v_cvt_f32_i32_sdwa v100, sext(v50) dst_sel:DWORD dst_unused:UNUSED_PAD src0_sel:BYTE_0
	v_dot4c_i32_i8_e32 v96, v50, v54
	v_cvt_f32_i32_sdwa v101, sext(v51) dst_sel:DWORD dst_unused:UNUSED_PAD src0_sel:BYTE_0
	v_dot4c_i32_i8_e32 v96, v51, v55
	v_fma_f32 v97, v98, v4, 0
	v_cvt_f32_i32_sdwa v98, sext(v48) dst_sel:DWORD dst_unused:UNUSED_PAD src0_sel:BYTE_1
	v_fmac_f32_e32 v97, v99, v8
	v_cvt_f32_i32_sdwa v99, sext(v49) dst_sel:DWORD dst_unused:UNUSED_PAD src0_sel:BYTE_1
	v_fmac_f32_e32 v97, v100, v12
	v_cvt_f32_i32_sdwa v100, sext(v50) dst_sel:DWORD dst_unused:UNUSED_PAD src0_sel:BYTE_1
	v_fmac_f32_e32 v97, v101, v16
	v_cvt_f32_i32_sdwa v101, sext(v51) dst_sel:DWORD dst_unused:UNUSED_PAD src0_sel:BYTE_1
	v_add_u32_dpp v96, v96, v96 quad_perm:[1,0,3,2] row_mask:0xf bank_mask:0xf bound_ctrl:1
	v_fmac_f32_e32 v97, v98, v5
	v_cvt_f32_i32_sdwa v98, sext(v48) dst_sel:DWORD dst_unused:UNUSED_PAD src0_sel:BYTE_2
	v_fmac_f32_e32 v97, v99, v9
	v_cvt_f32_i32_sdwa v99, sext(v49) dst_sel:DWORD dst_unused:UNUSED_PAD src0_sel:BYTE_2
	v_fmac_f32_e32 v97, v100, v13
	v_cvt_f32_i32_sdwa v100, sext(v50) dst_sel:DWORD dst_unused:UNUSED_PAD src0_sel:BYTE_2
	v_add_u32_dpp v96, v96, v96 quad_perm:[2,3,0,1] row_mask:0xf bank_mask:0xf bound_ctrl:1
	v_fmac_f32_e32 v97, v101, v17
	v_cvt_f32_i32_sdwa v101, sext(v51) dst_sel:DWORD dst_unused:UNUSED_PAD src0_sel:BYTE_2
	v_fmac_f32_e32 v97, v98, v6
	v_cvt_f32_i32_sdwa v98, sext(v48) dst_sel:DWORD dst_unused:UNUSED_PAD src0_sel:BYTE_3
	v_fmac_f32_e32 v97, v99, v10
	v_cvt_f32_i32_sdwa v99, sext(v49) dst_sel:DWORD dst_unused:UNUSED_PAD src0_sel:BYTE_3
	v_add_u32_dpp v96, v96, v96 row_half_mirror row_mask:0xf bank_mask:0xf bound_ctrl:1
	v_fmac_f32_e32 v97, v100, v14
	v_cvt_f32_i32_sdwa v100, sext(v50) dst_sel:DWORD dst_unused:UNUSED_PAD src0_sel:BYTE_3
	v_fmac_f32_e32 v97, v101, v18
	v_cvt_f32_i32_sdwa v101, sext(v51) dst_sel:DWORD dst_unused:UNUSED_PAD src0_sel:BYTE_3
	v_fmac_f32_e32 v97, v98, v7
	v_fmac_f32_e32 v97, v99, v11
	v_fmac_f32_e32 v97, v100, v15
	v_fmac_f32_e32 v97, v101, v19
	v_cndmask_b32_e64 v102, v102, v96, s[44:45]
	s_waitcnt lgkmcnt(0)
	v_add_f32_dpp v97, v97, v97 quad_perm:[1,0,3,2] row_mask:0xf bank_mask:0xf bound_ctrl:1
	v_lshl_add_u32 v106, v104, 7, v2
	v_lshl_add_u32 v107, v105, 7, v2
	v_add_f32_dpp v97, v97, v97 quad_perm:[2,3,0,1] row_mask:0xf bank_mask:0xf bound_ctrl:1
	global_load_dwordx4 v[48:51], v106, s[18:19]
	global_load_dwordx4 v[52:55], v107, s[18:19]
	v_add_f32_dpp v97, v97, v97 row_half_mirror row_mask:0xf bank_mask:0xf bound_ctrl:1
	v_cndmask_b32_e64 v103, v103, v97, s[44:45]
	ds_bpermute_b32 v104, v3, v22 offset:96
	ds_bpermute_b32 v105, v3, v26 offset:96
	s_waitcnt vmcnt(16)
	v_mov_b32_e32 v96, 0
	v_dot4c_i32_i8_e32 v96, v56, v60
	v_cvt_f32_i32_sdwa v98, sext(v56) dst_sel:DWORD dst_unused:UNUSED_PAD src0_sel:BYTE_0
	v_cvt_f32_i32_sdwa v99, sext(v57) dst_sel:DWORD dst_unused:UNUSED_PAD src0_sel:BYTE_0
	v_dot4c_i32_i8_e32 v96, v57, v61
	v_cvt_f32_i32_sdwa v100, sext(v58) dst_sel:DWORD dst_unused:UNUSED_PAD src0_sel:BYTE_0
	v_dot4c_i32_i8_e32 v96, v58, v62
	v_cvt_f32_i32_sdwa v101, sext(v59) dst_sel:DWORD dst_unused:UNUSED_PAD src0_sel:BYTE_0
	v_dot4c_i32_i8_e32 v96, v59, v63
	v_fma_f32 v97, v98, v4, 0
	v_cvt_f32_i32_sdwa v98, sext(v56) dst_sel:DWORD dst_unused:UNUSED_PAD src0_sel:BYTE_1
	v_fmac_f32_e32 v97, v99, v8
	v_cvt_f32_i32_sdwa v99, sext(v57) dst_sel:DWORD dst_unused:UNUSED_PAD src0_sel:BYTE_1
	v_fmac_f32_e32 v97, v100, v12
	v_cvt_f32_i32_sdwa v100, sext(v58) dst_sel:DWORD dst_unused:UNUSED_PAD src0_sel:BYTE_1
	v_fmac_f32_e32 v97, v101, v16
	v_cvt_f32_i32_sdwa v101, sext(v59) dst_sel:DWORD dst_unused:UNUSED_PAD src0_sel:BYTE_1
	v_add_u32_dpp v96, v96, v96 quad_perm:[1,0,3,2] row_mask:0xf bank_mask:0xf bound_ctrl:1
	v_fmac_f32_e32 v97, v98, v5
	v_cvt_f32_i32_sdwa v98, sext(v56) dst_sel:DWORD dst_unused:UNUSED_PAD src0_sel:BYTE_2
	v_fmac_f32_e32 v97, v99, v9
	v_cvt_f32_i32_sdwa v99, sext(v57) dst_sel:DWORD dst_unused:UNUSED_PAD src0_sel:BYTE_2
	v_fmac_f32_e32 v97, v100, v13
	v_cvt_f32_i32_sdwa v100, sext(v58) dst_sel:DWORD dst_unused:UNUSED_PAD src0_sel:BYTE_2
	v_add_u32_dpp v96, v96, v96 quad_perm:[2,3,0,1] row_mask:0xf bank_mask:0xf bound_ctrl:1
	v_fmac_f32_e32 v97, v101, v17
	v_cvt_f32_i32_sdwa v101, sext(v59) dst_sel:DWORD dst_unused:UNUSED_PAD src0_sel:BYTE_2
	v_fmac_f32_e32 v97, v98, v6
	v_cvt_f32_i32_sdwa v98, sext(v56) dst_sel:DWORD dst_unused:UNUSED_PAD src0_sel:BYTE_3
	v_fmac_f32_e32 v97, v99, v10
	v_cvt_f32_i32_sdwa v99, sext(v57) dst_sel:DWORD dst_unused:UNUSED_PAD src0_sel:BYTE_3
	v_add_u32_dpp v96, v96, v96 row_half_mirror row_mask:0xf bank_mask:0xf bound_ctrl:1
	v_fmac_f32_e32 v97, v100, v14
	v_cvt_f32_i32_sdwa v100, sext(v58) dst_sel:DWORD dst_unused:UNUSED_PAD src0_sel:BYTE_3
	v_fmac_f32_e32 v97, v101, v18
	v_cvt_f32_i32_sdwa v101, sext(v59) dst_sel:DWORD dst_unused:UNUSED_PAD src0_sel:BYTE_3
	v_fmac_f32_e32 v97, v98, v7
	v_fmac_f32_e32 v97, v99, v11
	v_fmac_f32_e32 v97, v100, v15
	v_fmac_f32_e32 v97, v101, v19
	v_cndmask_b32_e64 v102, v102, v96, s[46:47]
	s_waitcnt lgkmcnt(0)
	v_add_f32_dpp v97, v97, v97 quad_perm:[1,0,3,2] row_mask:0xf bank_mask:0xf bound_ctrl:1
	v_lshl_add_u32 v106, v104, 7, v2
	v_lshl_add_u32 v107, v105, 7, v2
	v_add_f32_dpp v97, v97, v97 quad_perm:[2,3,0,1] row_mask:0xf bank_mask:0xf bound_ctrl:1
	global_load_dwordx4 v[56:59], v106, s[18:19]
	global_load_dwordx4 v[60:63], v107, s[18:19]
	v_add_f32_dpp v97, v97, v97 row_half_mirror row_mask:0xf bank_mask:0xf bound_ctrl:1
	v_cndmask_b32_e64 v103, v103, v97, s[46:47]
	ds_bpermute_b32 v104, v3, v22 offset:128
	ds_bpermute_b32 v105, v3, v26 offset:128
	s_waitcnt vmcnt(16)
	v_mov_b32_e32 v96, 0
	v_dot4c_i32_i8_e32 v96, v64, v68
	v_cvt_f32_i32_sdwa v98, sext(v64) dst_sel:DWORD dst_unused:UNUSED_PAD src0_sel:BYTE_0
	v_cvt_f32_i32_sdwa v99, sext(v65) dst_sel:DWORD dst_unused:UNUSED_PAD src0_sel:BYTE_0
	v_dot4c_i32_i8_e32 v96, v65, v69
	v_cvt_f32_i32_sdwa v100, sext(v66) dst_sel:DWORD dst_unused:UNUSED_PAD src0_sel:BYTE_0
	v_dot4c_i32_i8_e32 v96, v66, v70
	v_cvt_f32_i32_sdwa v101, sext(v67) dst_sel:DWORD dst_unused:UNUSED_PAD src0_sel:BYTE_0
	v_dot4c_i32_i8_e32 v96, v67, v71
	v_fma_f32 v97, v98, v4, 0
	v_cvt_f32_i32_sdwa v98, sext(v64) dst_sel:DWORD dst_unused:UNUSED_PAD src0_sel:BYTE_1
	v_fmac_f32_e32 v97, v99, v8
	v_cvt_f32_i32_sdwa v99, sext(v65) dst_sel:DWORD dst_unused:UNUSED_PAD src0_sel:BYTE_1
	v_fmac_f32_e32 v97, v100, v12
	v_cvt_f32_i32_sdwa v100, sext(v66) dst_sel:DWORD dst_unused:UNUSED_PAD src0_sel:BYTE_1
	v_fmac_f32_e32 v97, v101, v16
	v_cvt_f32_i32_sdwa v101, sext(v67) dst_sel:DWORD dst_unused:UNUSED_PAD src0_sel:BYTE_1
	v_add_u32_dpp v96, v96, v96 quad_perm:[1,0,3,2] row_mask:0xf bank_mask:0xf bound_ctrl:1
	v_fmac_f32_e32 v97, v98, v5
	v_cvt_f32_i32_sdwa v98, sext(v64) dst_sel:DWORD dst_unused:UNUSED_PAD src0_sel:BYTE_2
	v_fmac_f32_e32 v97, v99, v9
	v_cvt_f32_i32_sdwa v99, sext(v65) dst_sel:DWORD dst_unused:UNUSED_PAD src0_sel:BYTE_2
	v_fmac_f32_e32 v97, v100, v13
	v_cvt_f32_i32_sdwa v100, sext(v66) dst_sel:DWORD dst_unused:UNUSED_PAD src0_sel:BYTE_2
	v_add_u32_dpp v96, v96, v96 quad_perm:[2,3,0,1] row_mask:0xf bank_mask:0xf bound_ctrl:1
	v_fmac_f32_e32 v97, v101, v17
	v_cvt_f32_i32_sdwa v101, sext(v67) dst_sel:DWORD dst_unused:UNUSED_PAD src0_sel:BYTE_2
	v_fmac_f32_e32 v97, v98, v6
	v_cvt_f32_i32_sdwa v98, sext(v64) dst_sel:DWORD dst_unused:UNUSED_PAD src0_sel:BYTE_3
	v_fmac_f32_e32 v97, v99, v10
	v_cvt_f32_i32_sdwa v99, sext(v65) dst_sel:DWORD dst_unused:UNUSED_PAD src0_sel:BYTE_3
	v_add_u32_dpp v96, v96, v96 row_half_mirror row_mask:0xf bank_mask:0xf bound_ctrl:1
	v_fmac_f32_e32 v97, v100, v14
	v_cvt_f32_i32_sdwa v100, sext(v66) dst_sel:DWORD dst_unused:UNUSED_PAD src0_sel:BYTE_3
	v_fmac_f32_e32 v97, v101, v18
	v_cvt_f32_i32_sdwa v101, sext(v67) dst_sel:DWORD dst_unused:UNUSED_PAD src0_sel:BYTE_3
	v_fmac_f32_e32 v97, v98, v7
	v_fmac_f32_e32 v97, v99, v11
	v_fmac_f32_e32 v97, v100, v15
	v_fmac_f32_e32 v97, v101, v19
	v_cndmask_b32_e64 v102, v102, v96, s[48:49]
	s_waitcnt lgkmcnt(0)
	v_add_f32_dpp v97, v97, v97 quad_perm:[1,0,3,2] row_mask:0xf bank_mask:0xf bound_ctrl:1
	v_lshl_add_u32 v106, v104, 7, v2
	v_lshl_add_u32 v107, v105, 7, v2
	v_add_f32_dpp v97, v97, v97 quad_perm:[2,3,0,1] row_mask:0xf bank_mask:0xf bound_ctrl:1
	global_load_dwordx4 v[64:67], v106, s[18:19]
	global_load_dwordx4 v[68:71], v107, s[18:19]
	v_add_f32_dpp v97, v97, v97 row_half_mirror row_mask:0xf bank_mask:0xf bound_ctrl:1
	v_cndmask_b32_e64 v103, v103, v97, s[48:49]
	ds_bpermute_b32 v104, v3, v22 offset:160
	ds_bpermute_b32 v105, v3, v26 offset:160
	s_waitcnt vmcnt(16)
	v_mov_b32_e32 v96, 0
	v_dot4c_i32_i8_e32 v96, v72, v76
	v_cvt_f32_i32_sdwa v98, sext(v72) dst_sel:DWORD dst_unused:UNUSED_PAD src0_sel:BYTE_0
	v_cvt_f32_i32_sdwa v99, sext(v73) dst_sel:DWORD dst_unused:UNUSED_PAD src0_sel:BYTE_0
	v_dot4c_i32_i8_e32 v96, v73, v77
	v_cvt_f32_i32_sdwa v100, sext(v74) dst_sel:DWORD dst_unused:UNUSED_PAD src0_sel:BYTE_0
	v_dot4c_i32_i8_e32 v96, v74, v78
	v_cvt_f32_i32_sdwa v101, sext(v75) dst_sel:DWORD dst_unused:UNUSED_PAD src0_sel:BYTE_0
	v_dot4c_i32_i8_e32 v96, v75, v79
	v_fma_f32 v97, v98, v4, 0
	v_cvt_f32_i32_sdwa v98, sext(v72) dst_sel:DWORD dst_unused:UNUSED_PAD src0_sel:BYTE_1
	v_fmac_f32_e32 v97, v99, v8
	v_cvt_f32_i32_sdwa v99, sext(v73) dst_sel:DWORD dst_unused:UNUSED_PAD src0_sel:BYTE_1
	v_fmac_f32_e32 v97, v100, v12
	v_cvt_f32_i32_sdwa v100, sext(v74) dst_sel:DWORD dst_unused:UNUSED_PAD src0_sel:BYTE_1
	v_fmac_f32_e32 v97, v101, v16
	v_cvt_f32_i32_sdwa v101, sext(v75) dst_sel:DWORD dst_unused:UNUSED_PAD src0_sel:BYTE_1
	v_add_u32_dpp v96, v96, v96 quad_perm:[1,0,3,2] row_mask:0xf bank_mask:0xf bound_ctrl:1
	v_fmac_f32_e32 v97, v98, v5
	v_cvt_f32_i32_sdwa v98, sext(v72) dst_sel:DWORD dst_unused:UNUSED_PAD src0_sel:BYTE_2
	v_fmac_f32_e32 v97, v99, v9
	v_cvt_f32_i32_sdwa v99, sext(v73) dst_sel:DWORD dst_unused:UNUSED_PAD src0_sel:BYTE_2
	v_fmac_f32_e32 v97, v100, v13
	v_cvt_f32_i32_sdwa v100, sext(v74) dst_sel:DWORD dst_unused:UNUSED_PAD src0_sel:BYTE_2
	v_add_u32_dpp v96, v96, v96 quad_perm:[2,3,0,1] row_mask:0xf bank_mask:0xf bound_ctrl:1
	v_fmac_f32_e32 v97, v101, v17
	v_cvt_f32_i32_sdwa v101, sext(v75) dst_sel:DWORD dst_unused:UNUSED_PAD src0_sel:BYTE_2
	v_fmac_f32_e32 v97, v98, v6
	v_cvt_f32_i32_sdwa v98, sext(v72) dst_sel:DWORD dst_unused:UNUSED_PAD src0_sel:BYTE_3
	v_fmac_f32_e32 v97, v99, v10
	v_cvt_f32_i32_sdwa v99, sext(v73) dst_sel:DWORD dst_unused:UNUSED_PAD src0_sel:BYTE_3
	v_add_u32_dpp v96, v96, v96 row_half_mirror row_mask:0xf bank_mask:0xf bound_ctrl:1
	v_fmac_f32_e32 v97, v100, v14
	v_cvt_f32_i32_sdwa v100, sext(v74) dst_sel:DWORD dst_unused:UNUSED_PAD src0_sel:BYTE_3
	v_fmac_f32_e32 v97, v101, v18
	v_cvt_f32_i32_sdwa v101, sext(v75) dst_sel:DWORD dst_unused:UNUSED_PAD src0_sel:BYTE_3
	v_fmac_f32_e32 v97, v98, v7
	v_fmac_f32_e32 v97, v99, v11
	v_fmac_f32_e32 v97, v100, v15
	v_fmac_f32_e32 v97, v101, v19
	v_cndmask_b32_e64 v102, v102, v96, s[50:51]
	s_waitcnt lgkmcnt(0)
	v_add_f32_dpp v97, v97, v97 quad_perm:[1,0,3,2] row_mask:0xf bank_mask:0xf bound_ctrl:1
	v_lshl_add_u32 v106, v104, 7, v2
	v_lshl_add_u32 v107, v105, 7, v2
	v_add_f32_dpp v97, v97, v97 quad_perm:[2,3,0,1] row_mask:0xf bank_mask:0xf bound_ctrl:1
	global_load_dwordx4 v[72:75], v106, s[18:19]
	global_load_dwordx4 v[76:79], v107, s[18:19]
	v_add_f32_dpp v97, v97, v97 row_half_mirror row_mask:0xf bank_mask:0xf bound_ctrl:1
	v_cndmask_b32_e64 v103, v103, v97, s[50:51]
	ds_bpermute_b32 v104, v3, v22 offset:192
	ds_bpermute_b32 v105, v3, v26 offset:192
	s_waitcnt vmcnt(16)
	v_mov_b32_e32 v96, 0
	v_dot4c_i32_i8_e32 v96, v80, v84
	v_cvt_f32_i32_sdwa v98, sext(v80) dst_sel:DWORD dst_unused:UNUSED_PAD src0_sel:BYTE_0
	v_cvt_f32_i32_sdwa v99, sext(v81) dst_sel:DWORD dst_unused:UNUSED_PAD src0_sel:BYTE_0
	v_dot4c_i32_i8_e32 v96, v81, v85
	v_cvt_f32_i32_sdwa v100, sext(v82) dst_sel:DWORD dst_unused:UNUSED_PAD src0_sel:BYTE_0
	v_dot4c_i32_i8_e32 v96, v82, v86
	v_cvt_f32_i32_sdwa v101, sext(v83) dst_sel:DWORD dst_unused:UNUSED_PAD src0_sel:BYTE_0
	v_dot4c_i32_i8_e32 v96, v83, v87
	v_fma_f32 v97, v98, v4, 0
	v_cvt_f32_i32_sdwa v98, sext(v80) dst_sel:DWORD dst_unused:UNUSED_PAD src0_sel:BYTE_1
	v_fmac_f32_e32 v97, v99, v8
	v_cvt_f32_i32_sdwa v99, sext(v81) dst_sel:DWORD dst_unused:UNUSED_PAD src0_sel:BYTE_1
	v_fmac_f32_e32 v97, v100, v12
	v_cvt_f32_i32_sdwa v100, sext(v82) dst_sel:DWORD dst_unused:UNUSED_PAD src0_sel:BYTE_1
	v_fmac_f32_e32 v97, v101, v16
	v_cvt_f32_i32_sdwa v101, sext(v83) dst_sel:DWORD dst_unused:UNUSED_PAD src0_sel:BYTE_1
	v_add_u32_dpp v96, v96, v96 quad_perm:[1,0,3,2] row_mask:0xf bank_mask:0xf bound_ctrl:1
	v_fmac_f32_e32 v97, v98, v5
	v_cvt_f32_i32_sdwa v98, sext(v80) dst_sel:DWORD dst_unused:UNUSED_PAD src0_sel:BYTE_2
	v_fmac_f32_e32 v97, v99, v9
	v_cvt_f32_i32_sdwa v99, sext(v81) dst_sel:DWORD dst_unused:UNUSED_PAD src0_sel:BYTE_2
	v_fmac_f32_e32 v97, v100, v13
	v_cvt_f32_i32_sdwa v100, sext(v82) dst_sel:DWORD dst_unused:UNUSED_PAD src0_sel:BYTE_2
	v_add_u32_dpp v96, v96, v96 quad_perm:[2,3,0,1] row_mask:0xf bank_mask:0xf bound_ctrl:1
	v_fmac_f32_e32 v97, v101, v17
	v_cvt_f32_i32_sdwa v101, sext(v83) dst_sel:DWORD dst_unused:UNUSED_PAD src0_sel:BYTE_2
	v_fmac_f32_e32 v97, v98, v6
	v_cvt_f32_i32_sdwa v98, sext(v80) dst_sel:DWORD dst_unused:UNUSED_PAD src0_sel:BYTE_3
	v_fmac_f32_e32 v97, v99, v10
	v_cvt_f32_i32_sdwa v99, sext(v81) dst_sel:DWORD dst_unused:UNUSED_PAD src0_sel:BYTE_3
	v_add_u32_dpp v96, v96, v96 row_half_mirror row_mask:0xf bank_mask:0xf bound_ctrl:1
	v_fmac_f32_e32 v97, v100, v14
	v_cvt_f32_i32_sdwa v100, sext(v82) dst_sel:DWORD dst_unused:UNUSED_PAD src0_sel:BYTE_3
	v_fmac_f32_e32 v97, v101, v18
	v_cvt_f32_i32_sdwa v101, sext(v83) dst_sel:DWORD dst_unused:UNUSED_PAD src0_sel:BYTE_3
	v_fmac_f32_e32 v97, v98, v7
	v_fmac_f32_e32 v97, v99, v11
	v_fmac_f32_e32 v97, v100, v15
	v_fmac_f32_e32 v97, v101, v19
	v_cndmask_b32_e64 v102, v102, v96, s[52:53]
	s_waitcnt lgkmcnt(0)
	v_add_f32_dpp v97, v97, v97 quad_perm:[1,0,3,2] row_mask:0xf bank_mask:0xf bound_ctrl:1
	v_lshl_add_u32 v106, v104, 7, v2
	v_lshl_add_u32 v107, v105, 7, v2
	v_add_f32_dpp v97, v97, v97 quad_perm:[2,3,0,1] row_mask:0xf bank_mask:0xf bound_ctrl:1
	global_load_dwordx4 v[80:83], v106, s[18:19]
	global_load_dwordx4 v[84:87], v107, s[18:19]
	v_add_f32_dpp v97, v97, v97 row_half_mirror row_mask:0xf bank_mask:0xf bound_ctrl:1
	v_cndmask_b32_e64 v103, v103, v97, s[52:53]
	ds_bpermute_b32 v104, v3, v22 offset:224
	ds_bpermute_b32 v105, v3, v26 offset:224
	s_waitcnt vmcnt(16)
	v_mov_b32_e32 v96, 0
	v_dot4c_i32_i8_e32 v96, v88, v92
	v_cvt_f32_i32_sdwa v98, sext(v88) dst_sel:DWORD dst_unused:UNUSED_PAD src0_sel:BYTE_0
	v_cvt_f32_i32_sdwa v99, sext(v89) dst_sel:DWORD dst_unused:UNUSED_PAD src0_sel:BYTE_0
	v_dot4c_i32_i8_e32 v96, v89, v93
	v_cvt_f32_i32_sdwa v100, sext(v90) dst_sel:DWORD dst_unused:UNUSED_PAD src0_sel:BYTE_0
	v_dot4c_i32_i8_e32 v96, v90, v94
	v_cvt_f32_i32_sdwa v101, sext(v91) dst_sel:DWORD dst_unused:UNUSED_PAD src0_sel:BYTE_0
	v_dot4c_i32_i8_e32 v96, v91, v95
	v_fma_f32 v97, v98, v4, 0
	v_cvt_f32_i32_sdwa v98, sext(v88) dst_sel:DWORD dst_unused:UNUSED_PAD src0_sel:BYTE_1
	v_fmac_f32_e32 v97, v99, v8
	v_cvt_f32_i32_sdwa v99, sext(v89) dst_sel:DWORD dst_unused:UNUSED_PAD src0_sel:BYTE_1
	v_fmac_f32_e32 v97, v100, v12
	v_cvt_f32_i32_sdwa v100, sext(v90) dst_sel:DWORD dst_unused:UNUSED_PAD src0_sel:BYTE_1
	v_fmac_f32_e32 v97, v101, v16
	v_cvt_f32_i32_sdwa v101, sext(v91) dst_sel:DWORD dst_unused:UNUSED_PAD src0_sel:BYTE_1
	v_add_u32_dpp v96, v96, v96 quad_perm:[1,0,3,2] row_mask:0xf bank_mask:0xf bound_ctrl:1
	v_fmac_f32_e32 v97, v98, v5
	v_cvt_f32_i32_sdwa v98, sext(v88) dst_sel:DWORD dst_unused:UNUSED_PAD src0_sel:BYTE_2
	v_fmac_f32_e32 v97, v99, v9
	v_cvt_f32_i32_sdwa v99, sext(v89) dst_sel:DWORD dst_unused:UNUSED_PAD src0_sel:BYTE_2
	v_fmac_f32_e32 v97, v100, v13
	v_cvt_f32_i32_sdwa v100, sext(v90) dst_sel:DWORD dst_unused:UNUSED_PAD src0_sel:BYTE_2
	v_add_u32_dpp v96, v96, v96 quad_perm:[2,3,0,1] row_mask:0xf bank_mask:0xf bound_ctrl:1
	v_fmac_f32_e32 v97, v101, v17
	v_cvt_f32_i32_sdwa v101, sext(v91) dst_sel:DWORD dst_unused:UNUSED_PAD src0_sel:BYTE_2
	v_fmac_f32_e32 v97, v98, v6
	v_cvt_f32_i32_sdwa v98, sext(v88) dst_sel:DWORD dst_unused:UNUSED_PAD src0_sel:BYTE_3
	v_fmac_f32_e32 v97, v99, v10
	v_cvt_f32_i32_sdwa v99, sext(v89) dst_sel:DWORD dst_unused:UNUSED_PAD src0_sel:BYTE_3
	v_add_u32_dpp v96, v96, v96 row_half_mirror row_mask:0xf bank_mask:0xf bound_ctrl:1
	v_fmac_f32_e32 v97, v100, v14
	v_cvt_f32_i32_sdwa v100, sext(v90) dst_sel:DWORD dst_unused:UNUSED_PAD src0_sel:BYTE_3
	v_fmac_f32_e32 v97, v101, v18
	v_cvt_f32_i32_sdwa v101, sext(v91) dst_sel:DWORD dst_unused:UNUSED_PAD src0_sel:BYTE_3
	v_fmac_f32_e32 v97, v98, v7
	v_fmac_f32_e32 v97, v99, v11
	v_fmac_f32_e32 v97, v100, v15
	v_fmac_f32_e32 v97, v101, v19
	v_cndmask_b32_e64 v102, v102, v96, s[54:55]
	s_waitcnt lgkmcnt(0)
	v_add_f32_dpp v97, v97, v97 quad_perm:[1,0,3,2] row_mask:0xf bank_mask:0xf bound_ctrl:1
	v_lshl_add_u32 v106, v104, 7, v2
	v_lshl_add_u32 v107, v105, 7, v2
	v_add_f32_dpp v97, v97, v97 quad_perm:[2,3,0,1] row_mask:0xf bank_mask:0xf bound_ctrl:1
	global_load_dwordx4 v[88:91], v106, s[18:19]
	global_load_dwordx4 v[92:95], v107, s[18:19]
	v_add_f32_dpp v97, v97, v97 row_half_mirror row_mask:0xf bank_mask:0xf bound_ctrl:1
	v_cndmask_b32_e64 v103, v103, v97, s[54:55]
	global_store_dword v28, v102, s[20:21] offset:256
	global_store_dword v28, v103, s[22:23] offset:256
	ds_bpermute_b32 v104, v3, v23
	ds_bpermute_b32 v105, v3, v27
	s_waitcnt vmcnt(16)
	v_mov_b32_e32 v96, 0
	v_dot4c_i32_i8_e32 v96, v32, v36
	v_cvt_f32_i32_sdwa v98, sext(v32) dst_sel:DWORD dst_unused:UNUSED_PAD src0_sel:BYTE_0
	v_cvt_f32_i32_sdwa v99, sext(v33) dst_sel:DWORD dst_unused:UNUSED_PAD src0_sel:BYTE_0
	v_dot4c_i32_i8_e32 v96, v33, v37
	v_cvt_f32_i32_sdwa v100, sext(v34) dst_sel:DWORD dst_unused:UNUSED_PAD src0_sel:BYTE_0
	v_dot4c_i32_i8_e32 v96, v34, v38
	v_cvt_f32_i32_sdwa v101, sext(v35) dst_sel:DWORD dst_unused:UNUSED_PAD src0_sel:BYTE_0
	v_dot4c_i32_i8_e32 v96, v35, v39
	v_fma_f32 v97, v98, v4, 0
	v_cvt_f32_i32_sdwa v98, sext(v32) dst_sel:DWORD dst_unused:UNUSED_PAD src0_sel:BYTE_1
	v_fmac_f32_e32 v97, v99, v8
	v_cvt_f32_i32_sdwa v99, sext(v33) dst_sel:DWORD dst_unused:UNUSED_PAD src0_sel:BYTE_1
	v_fmac_f32_e32 v97, v100, v12
	v_cvt_f32_i32_sdwa v100, sext(v34) dst_sel:DWORD dst_unused:UNUSED_PAD src0_sel:BYTE_1
	v_fmac_f32_e32 v97, v101, v16
	v_cvt_f32_i32_sdwa v101, sext(v35) dst_sel:DWORD dst_unused:UNUSED_PAD src0_sel:BYTE_1
	v_add_u32_dpp v96, v96, v96 quad_perm:[1,0,3,2] row_mask:0xf bank_mask:0xf bound_ctrl:1
	v_fmac_f32_e32 v97, v98, v5
	v_cvt_f32_i32_sdwa v98, sext(v32) dst_sel:DWORD dst_unused:UNUSED_PAD src0_sel:BYTE_2
	v_fmac_f32_e32 v97, v99, v9
	v_cvt_f32_i32_sdwa v99, sext(v33) dst_sel:DWORD dst_unused:UNUSED_PAD src0_sel:BYTE_2
	v_fmac_f32_e32 v97, v100, v13
	v_cvt_f32_i32_sdwa v100, sext(v34) dst_sel:DWORD dst_unused:UNUSED_PAD src0_sel:BYTE_2
	v_add_u32_dpp v96, v96, v96 quad_perm:[2,3,0,1] row_mask:0xf bank_mask:0xf bound_ctrl:1
	v_fmac_f32_e32 v97, v101, v17
	v_cvt_f32_i32_sdwa v101, sext(v35) dst_sel:DWORD dst_unused:UNUSED_PAD src0_sel:BYTE_2
	v_fmac_f32_e32 v97, v98, v6
	v_cvt_f32_i32_sdwa v98, sext(v32) dst_sel:DWORD dst_unused:UNUSED_PAD src0_sel:BYTE_3
	v_fmac_f32_e32 v97, v99, v10
	v_cvt_f32_i32_sdwa v99, sext(v33) dst_sel:DWORD dst_unused:UNUSED_PAD src0_sel:BYTE_3
	v_add_u32_dpp v96, v96, v96 row_half_mirror row_mask:0xf bank_mask:0xf bound_ctrl:1
	v_fmac_f32_e32 v97, v100, v14
	v_cvt_f32_i32_sdwa v100, sext(v34) dst_sel:DWORD dst_unused:UNUSED_PAD src0_sel:BYTE_3
	v_fmac_f32_e32 v97, v101, v18
	v_cvt_f32_i32_sdwa v101, sext(v35) dst_sel:DWORD dst_unused:UNUSED_PAD src0_sel:BYTE_3
	v_fmac_f32_e32 v97, v98, v7
	v_fmac_f32_e32 v97, v99, v11
	v_fmac_f32_e32 v97, v100, v15
	v_fmac_f32_e32 v97, v101, v19
	v_cndmask_b32_e64 v102, 0, v96, s[40:41]
	s_waitcnt lgkmcnt(0)
	v_add_f32_dpp v97, v97, v97 quad_perm:[1,0,3,2] row_mask:0xf bank_mask:0xf bound_ctrl:1
	v_lshl_add_u32 v106, v104, 7, v2
	v_lshl_add_u32 v107, v105, 7, v2
	v_add_f32_dpp v97, v97, v97 quad_perm:[2,3,0,1] row_mask:0xf bank_mask:0xf bound_ctrl:1
	global_load_dwordx4 v[32:35], v106, s[18:19]
	global_load_dwordx4 v[36:39], v107, s[18:19]
	v_add_f32_dpp v97, v97, v97 row_half_mirror row_mask:0xf bank_mask:0xf bound_ctrl:1
	v_cndmask_b32_e64 v103, 0, v97, s[40:41]
	ds_bpermute_b32 v104, v3, v23 offset:32
	ds_bpermute_b32 v105, v3, v27 offset:32
	s_waitcnt vmcnt(16)
	v_mov_b32_e32 v96, 0
	v_dot4c_i32_i8_e32 v96, v40, v44
	v_cvt_f32_i32_sdwa v98, sext(v40) dst_sel:DWORD dst_unused:UNUSED_PAD src0_sel:BYTE_0
	v_cvt_f32_i32_sdwa v99, sext(v41) dst_sel:DWORD dst_unused:UNUSED_PAD src0_sel:BYTE_0
	v_dot4c_i32_i8_e32 v96, v41, v45
	v_cvt_f32_i32_sdwa v100, sext(v42) dst_sel:DWORD dst_unused:UNUSED_PAD src0_sel:BYTE_0
	v_dot4c_i32_i8_e32 v96, v42, v46
	v_cvt_f32_i32_sdwa v101, sext(v43) dst_sel:DWORD dst_unused:UNUSED_PAD src0_sel:BYTE_0
	v_dot4c_i32_i8_e32 v96, v43, v47
	v_fma_f32 v97, v98, v4, 0
	v_cvt_f32_i32_sdwa v98, sext(v40) dst_sel:DWORD dst_unused:UNUSED_PAD src0_sel:BYTE_1
	v_fmac_f32_e32 v97, v99, v8
	v_cvt_f32_i32_sdwa v99, sext(v41) dst_sel:DWORD dst_unused:UNUSED_PAD src0_sel:BYTE_1
	v_fmac_f32_e32 v97, v100, v12
	v_cvt_f32_i32_sdwa v100, sext(v42) dst_sel:DWORD dst_unused:UNUSED_PAD src0_sel:BYTE_1
	v_fmac_f32_e32 v97, v101, v16
	v_cvt_f32_i32_sdwa v101, sext(v43) dst_sel:DWORD dst_unused:UNUSED_PAD src0_sel:BYTE_1
	v_add_u32_dpp v96, v96, v96 quad_perm:[1,0,3,2] row_mask:0xf bank_mask:0xf bound_ctrl:1
	v_fmac_f32_e32 v97, v98, v5
	v_cvt_f32_i32_sdwa v98, sext(v40) dst_sel:DWORD dst_unused:UNUSED_PAD src0_sel:BYTE_2
	v_fmac_f32_e32 v97, v99, v9
	v_cvt_f32_i32_sdwa v99, sext(v41) dst_sel:DWORD dst_unused:UNUSED_PAD src0_sel:BYTE_2
	v_fmac_f32_e32 v97, v100, v13
	v_cvt_f32_i32_sdwa v100, sext(v42) dst_sel:DWORD dst_unused:UNUSED_PAD src0_sel:BYTE_2
	v_add_u32_dpp v96, v96, v96 quad_perm:[2,3,0,1] row_mask:0xf bank_mask:0xf bound_ctrl:1
	v_fmac_f32_e32 v97, v101, v17
	v_cvt_f32_i32_sdwa v101, sext(v43) dst_sel:DWORD dst_unused:UNUSED_PAD src0_sel:BYTE_2
	v_fmac_f32_e32 v97, v98, v6
	v_cvt_f32_i32_sdwa v98, sext(v40) dst_sel:DWORD dst_unused:UNUSED_PAD src0_sel:BYTE_3
	v_fmac_f32_e32 v97, v99, v10
	v_cvt_f32_i32_sdwa v99, sext(v41) dst_sel:DWORD dst_unused:UNUSED_PAD src0_sel:BYTE_3
	v_add_u32_dpp v96, v96, v96 row_half_mirror row_mask:0xf bank_mask:0xf bound_ctrl:1
	v_fmac_f32_e32 v97, v100, v14
	v_cvt_f32_i32_sdwa v100, sext(v42) dst_sel:DWORD dst_unused:UNUSED_PAD src0_sel:BYTE_3
	v_fmac_f32_e32 v97, v101, v18
	v_cvt_f32_i32_sdwa v101, sext(v43) dst_sel:DWORD dst_unused:UNUSED_PAD src0_sel:BYTE_3
	v_fmac_f32_e32 v97, v98, v7
	v_fmac_f32_e32 v97, v99, v11
	v_fmac_f32_e32 v97, v100, v15
	v_fmac_f32_e32 v97, v101, v19
	v_cndmask_b32_e64 v102, v102, v96, s[42:43]
	s_waitcnt lgkmcnt(0)
	v_add_f32_dpp v97, v97, v97 quad_perm:[1,0,3,2] row_mask:0xf bank_mask:0xf bound_ctrl:1
	v_lshl_add_u32 v106, v104, 7, v2
	v_lshl_add_u32 v107, v105, 7, v2
	v_add_f32_dpp v97, v97, v97 quad_perm:[2,3,0,1] row_mask:0xf bank_mask:0xf bound_ctrl:1
	global_load_dwordx4 v[40:43], v106, s[18:19]
	global_load_dwordx4 v[44:47], v107, s[18:19]
	v_add_f32_dpp v97, v97, v97 row_half_mirror row_mask:0xf bank_mask:0xf bound_ctrl:1
	v_cndmask_b32_e64 v103, v103, v97, s[42:43]
	ds_bpermute_b32 v104, v3, v23 offset:64
	ds_bpermute_b32 v105, v3, v27 offset:64
	s_waitcnt vmcnt(16)
	v_mov_b32_e32 v96, 0
	v_dot4c_i32_i8_e32 v96, v48, v52
	v_cvt_f32_i32_sdwa v98, sext(v48) dst_sel:DWORD dst_unused:UNUSED_PAD src0_sel:BYTE_0
	v_cvt_f32_i32_sdwa v99, sext(v49) dst_sel:DWORD dst_unused:UNUSED_PAD src0_sel:BYTE_0
	v_dot4c_i32_i8_e32 v96, v49, v53
	v_cvt_f32_i32_sdwa v100, sext(v50) dst_sel:DWORD dst_unused:UNUSED_PAD src0_sel:BYTE_0
	v_dot4c_i32_i8_e32 v96, v50, v54
	v_cvt_f32_i32_sdwa v101, sext(v51) dst_sel:DWORD dst_unused:UNUSED_PAD src0_sel:BYTE_0
	v_dot4c_i32_i8_e32 v96, v51, v55
	v_fma_f32 v97, v98, v4, 0
	v_cvt_f32_i32_sdwa v98, sext(v48) dst_sel:DWORD dst_unused:UNUSED_PAD src0_sel:BYTE_1
	v_fmac_f32_e32 v97, v99, v8
	v_cvt_f32_i32_sdwa v99, sext(v49) dst_sel:DWORD dst_unused:UNUSED_PAD src0_sel:BYTE_1
	v_fmac_f32_e32 v97, v100, v12
	v_cvt_f32_i32_sdwa v100, sext(v50) dst_sel:DWORD dst_unused:UNUSED_PAD src0_sel:BYTE_1
	v_fmac_f32_e32 v97, v101, v16
	v_cvt_f32_i32_sdwa v101, sext(v51) dst_sel:DWORD dst_unused:UNUSED_PAD src0_sel:BYTE_1
	v_add_u32_dpp v96, v96, v96 quad_perm:[1,0,3,2] row_mask:0xf bank_mask:0xf bound_ctrl:1
	v_fmac_f32_e32 v97, v98, v5
	v_cvt_f32_i32_sdwa v98, sext(v48) dst_sel:DWORD dst_unused:UNUSED_PAD src0_sel:BYTE_2
	v_fmac_f32_e32 v97, v99, v9
	v_cvt_f32_i32_sdwa v99, sext(v49) dst_sel:DWORD dst_unused:UNUSED_PAD src0_sel:BYTE_2
	v_fmac_f32_e32 v97, v100, v13
	v_cvt_f32_i32_sdwa v100, sext(v50) dst_sel:DWORD dst_unused:UNUSED_PAD src0_sel:BYTE_2
	v_add_u32_dpp v96, v96, v96 quad_perm:[2,3,0,1] row_mask:0xf bank_mask:0xf bound_ctrl:1
	v_fmac_f32_e32 v97, v101, v17
	v_cvt_f32_i32_sdwa v101, sext(v51) dst_sel:DWORD dst_unused:UNUSED_PAD src0_sel:BYTE_2
	v_fmac_f32_e32 v97, v98, v6
	v_cvt_f32_i32_sdwa v98, sext(v48) dst_sel:DWORD dst_unused:UNUSED_PAD src0_sel:BYTE_3
	v_fmac_f32_e32 v97, v99, v10
	v_cvt_f32_i32_sdwa v99, sext(v49) dst_sel:DWORD dst_unused:UNUSED_PAD src0_sel:BYTE_3
	v_add_u32_dpp v96, v96, v96 row_half_mirror row_mask:0xf bank_mask:0xf bound_ctrl:1
	v_fmac_f32_e32 v97, v100, v14
	v_cvt_f32_i32_sdwa v100, sext(v50) dst_sel:DWORD dst_unused:UNUSED_PAD src0_sel:BYTE_3
	v_fmac_f32_e32 v97, v101, v18
	v_cvt_f32_i32_sdwa v101, sext(v51) dst_sel:DWORD dst_unused:UNUSED_PAD src0_sel:BYTE_3
	v_fmac_f32_e32 v97, v98, v7
	v_fmac_f32_e32 v97, v99, v11
	v_fmac_f32_e32 v97, v100, v15
	v_fmac_f32_e32 v97, v101, v19
	v_cndmask_b32_e64 v102, v102, v96, s[44:45]
	s_waitcnt lgkmcnt(0)
	v_add_f32_dpp v97, v97, v97 quad_perm:[1,0,3,2] row_mask:0xf bank_mask:0xf bound_ctrl:1
	v_lshl_add_u32 v106, v104, 7, v2
	v_lshl_add_u32 v107, v105, 7, v2
	v_add_f32_dpp v97, v97, v97 quad_perm:[2,3,0,1] row_mask:0xf bank_mask:0xf bound_ctrl:1
	global_load_dwordx4 v[48:51], v106, s[18:19]
	global_load_dwordx4 v[52:55], v107, s[18:19]
	v_add_f32_dpp v97, v97, v97 row_half_mirror row_mask:0xf bank_mask:0xf bound_ctrl:1
	v_cndmask_b32_e64 v103, v103, v97, s[44:45]
	ds_bpermute_b32 v104, v3, v23 offset:96
	ds_bpermute_b32 v105, v3, v27 offset:96
	s_waitcnt vmcnt(16)
	v_mov_b32_e32 v96, 0
	v_dot4c_i32_i8_e32 v96, v56, v60
	v_cvt_f32_i32_sdwa v98, sext(v56) dst_sel:DWORD dst_unused:UNUSED_PAD src0_sel:BYTE_0
	v_cvt_f32_i32_sdwa v99, sext(v57) dst_sel:DWORD dst_unused:UNUSED_PAD src0_sel:BYTE_0
	v_dot4c_i32_i8_e32 v96, v57, v61
	v_cvt_f32_i32_sdwa v100, sext(v58) dst_sel:DWORD dst_unused:UNUSED_PAD src0_sel:BYTE_0
	v_dot4c_i32_i8_e32 v96, v58, v62
	v_cvt_f32_i32_sdwa v101, sext(v59) dst_sel:DWORD dst_unused:UNUSED_PAD src0_sel:BYTE_0
	v_dot4c_i32_i8_e32 v96, v59, v63
	v_fma_f32 v97, v98, v4, 0
	v_cvt_f32_i32_sdwa v98, sext(v56) dst_sel:DWORD dst_unused:UNUSED_PAD src0_sel:BYTE_1
	v_fmac_f32_e32 v97, v99, v8
	v_cvt_f32_i32_sdwa v99, sext(v57) dst_sel:DWORD dst_unused:UNUSED_PAD src0_sel:BYTE_1
	v_fmac_f32_e32 v97, v100, v12
	v_cvt_f32_i32_sdwa v100, sext(v58) dst_sel:DWORD dst_unused:UNUSED_PAD src0_sel:BYTE_1
	v_fmac_f32_e32 v97, v101, v16
	v_cvt_f32_i32_sdwa v101, sext(v59) dst_sel:DWORD dst_unused:UNUSED_PAD src0_sel:BYTE_1
	v_add_u32_dpp v96, v96, v96 quad_perm:[1,0,3,2] row_mask:0xf bank_mask:0xf bound_ctrl:1
	v_fmac_f32_e32 v97, v98, v5
	v_cvt_f32_i32_sdwa v98, sext(v56) dst_sel:DWORD dst_unused:UNUSED_PAD src0_sel:BYTE_2
	v_fmac_f32_e32 v97, v99, v9
	v_cvt_f32_i32_sdwa v99, sext(v57) dst_sel:DWORD dst_unused:UNUSED_PAD src0_sel:BYTE_2
	v_fmac_f32_e32 v97, v100, v13
	v_cvt_f32_i32_sdwa v100, sext(v58) dst_sel:DWORD dst_unused:UNUSED_PAD src0_sel:BYTE_2
	v_add_u32_dpp v96, v96, v96 quad_perm:[2,3,0,1] row_mask:0xf bank_mask:0xf bound_ctrl:1
	v_fmac_f32_e32 v97, v101, v17
	v_cvt_f32_i32_sdwa v101, sext(v59) dst_sel:DWORD dst_unused:UNUSED_PAD src0_sel:BYTE_2
	v_fmac_f32_e32 v97, v98, v6
	v_cvt_f32_i32_sdwa v98, sext(v56) dst_sel:DWORD dst_unused:UNUSED_PAD src0_sel:BYTE_3
	v_fmac_f32_e32 v97, v99, v10
	v_cvt_f32_i32_sdwa v99, sext(v57) dst_sel:DWORD dst_unused:UNUSED_PAD src0_sel:BYTE_3
	v_add_u32_dpp v96, v96, v96 row_half_mirror row_mask:0xf bank_mask:0xf bound_ctrl:1
	v_fmac_f32_e32 v97, v100, v14
	v_cvt_f32_i32_sdwa v100, sext(v58) dst_sel:DWORD dst_unused:UNUSED_PAD src0_sel:BYTE_3
	v_fmac_f32_e32 v97, v101, v18
	v_cvt_f32_i32_sdwa v101, sext(v59) dst_sel:DWORD dst_unused:UNUSED_PAD src0_sel:BYTE_3
	v_fmac_f32_e32 v97, v98, v7
	v_fmac_f32_e32 v97, v99, v11
	v_fmac_f32_e32 v97, v100, v15
	v_fmac_f32_e32 v97, v101, v19
	v_cndmask_b32_e64 v102, v102, v96, s[46:47]
	s_waitcnt lgkmcnt(0)
	v_add_f32_dpp v97, v97, v97 quad_perm:[1,0,3,2] row_mask:0xf bank_mask:0xf bound_ctrl:1
	v_lshl_add_u32 v106, v104, 7, v2
	v_lshl_add_u32 v107, v105, 7, v2
	v_add_f32_dpp v97, v97, v97 quad_perm:[2,3,0,1] row_mask:0xf bank_mask:0xf bound_ctrl:1
	global_load_dwordx4 v[56:59], v106, s[18:19]
	global_load_dwordx4 v[60:63], v107, s[18:19]
	v_add_f32_dpp v97, v97, v97 row_half_mirror row_mask:0xf bank_mask:0xf bound_ctrl:1
	v_cndmask_b32_e64 v103, v103, v97, s[46:47]
	ds_bpermute_b32 v104, v3, v23 offset:128
	ds_bpermute_b32 v105, v3, v27 offset:128
	s_waitcnt vmcnt(16)
	v_mov_b32_e32 v96, 0
	v_dot4c_i32_i8_e32 v96, v64, v68
	v_cvt_f32_i32_sdwa v98, sext(v64) dst_sel:DWORD dst_unused:UNUSED_PAD src0_sel:BYTE_0
	v_cvt_f32_i32_sdwa v99, sext(v65) dst_sel:DWORD dst_unused:UNUSED_PAD src0_sel:BYTE_0
	v_dot4c_i32_i8_e32 v96, v65, v69
	v_cvt_f32_i32_sdwa v100, sext(v66) dst_sel:DWORD dst_unused:UNUSED_PAD src0_sel:BYTE_0
	v_dot4c_i32_i8_e32 v96, v66, v70
	v_cvt_f32_i32_sdwa v101, sext(v67) dst_sel:DWORD dst_unused:UNUSED_PAD src0_sel:BYTE_0
	v_dot4c_i32_i8_e32 v96, v67, v71
	v_fma_f32 v97, v98, v4, 0
	v_cvt_f32_i32_sdwa v98, sext(v64) dst_sel:DWORD dst_unused:UNUSED_PAD src0_sel:BYTE_1
	v_fmac_f32_e32 v97, v99, v8
	v_cvt_f32_i32_sdwa v99, sext(v65) dst_sel:DWORD dst_unused:UNUSED_PAD src0_sel:BYTE_1
	v_fmac_f32_e32 v97, v100, v12
	v_cvt_f32_i32_sdwa v100, sext(v66) dst_sel:DWORD dst_unused:UNUSED_PAD src0_sel:BYTE_1
	v_fmac_f32_e32 v97, v101, v16
	v_cvt_f32_i32_sdwa v101, sext(v67) dst_sel:DWORD dst_unused:UNUSED_PAD src0_sel:BYTE_1
	v_add_u32_dpp v96, v96, v96 quad_perm:[1,0,3,2] row_mask:0xf bank_mask:0xf bound_ctrl:1
	v_fmac_f32_e32 v97, v98, v5
	v_cvt_f32_i32_sdwa v98, sext(v64) dst_sel:DWORD dst_unused:UNUSED_PAD src0_sel:BYTE_2
	v_fmac_f32_e32 v97, v99, v9
	v_cvt_f32_i32_sdwa v99, sext(v65) dst_sel:DWORD dst_unused:UNUSED_PAD src0_sel:BYTE_2
	v_fmac_f32_e32 v97, v100, v13
	v_cvt_f32_i32_sdwa v100, sext(v66) dst_sel:DWORD dst_unused:UNUSED_PAD src0_sel:BYTE_2
	v_add_u32_dpp v96, v96, v96 quad_perm:[2,3,0,1] row_mask:0xf bank_mask:0xf bound_ctrl:1
	v_fmac_f32_e32 v97, v101, v17
	v_cvt_f32_i32_sdwa v101, sext(v67) dst_sel:DWORD dst_unused:UNUSED_PAD src0_sel:BYTE_2
	v_fmac_f32_e32 v97, v98, v6
	v_cvt_f32_i32_sdwa v98, sext(v64) dst_sel:DWORD dst_unused:UNUSED_PAD src0_sel:BYTE_3
	v_fmac_f32_e32 v97, v99, v10
	v_cvt_f32_i32_sdwa v99, sext(v65) dst_sel:DWORD dst_unused:UNUSED_PAD src0_sel:BYTE_3
	v_add_u32_dpp v96, v96, v96 row_half_mirror row_mask:0xf bank_mask:0xf bound_ctrl:1
	v_fmac_f32_e32 v97, v100, v14
	v_cvt_f32_i32_sdwa v100, sext(v66) dst_sel:DWORD dst_unused:UNUSED_PAD src0_sel:BYTE_3
	v_fmac_f32_e32 v97, v101, v18
	v_cvt_f32_i32_sdwa v101, sext(v67) dst_sel:DWORD dst_unused:UNUSED_PAD src0_sel:BYTE_3
	v_fmac_f32_e32 v97, v98, v7
	v_fmac_f32_e32 v97, v99, v11
	v_fmac_f32_e32 v97, v100, v15
	v_fmac_f32_e32 v97, v101, v19
	v_cndmask_b32_e64 v102, v102, v96, s[48:49]
	s_waitcnt lgkmcnt(0)
	v_add_f32_dpp v97, v97, v97 quad_perm:[1,0,3,2] row_mask:0xf bank_mask:0xf bound_ctrl:1
	v_lshl_add_u32 v106, v104, 7, v2
	v_lshl_add_u32 v107, v105, 7, v2
	v_add_f32_dpp v97, v97, v97 quad_perm:[2,3,0,1] row_mask:0xf bank_mask:0xf bound_ctrl:1
	global_load_dwordx4 v[64:67], v106, s[18:19]
	global_load_dwordx4 v[68:71], v107, s[18:19]
	v_add_f32_dpp v97, v97, v97 row_half_mirror row_mask:0xf bank_mask:0xf bound_ctrl:1
	v_cndmask_b32_e64 v103, v103, v97, s[48:49]
	ds_bpermute_b32 v104, v3, v23 offset:160
	ds_bpermute_b32 v105, v3, v27 offset:160
	s_waitcnt vmcnt(16)
	v_mov_b32_e32 v96, 0
	v_dot4c_i32_i8_e32 v96, v72, v76
	v_cvt_f32_i32_sdwa v98, sext(v72) dst_sel:DWORD dst_unused:UNUSED_PAD src0_sel:BYTE_0
	v_cvt_f32_i32_sdwa v99, sext(v73) dst_sel:DWORD dst_unused:UNUSED_PAD src0_sel:BYTE_0
	v_dot4c_i32_i8_e32 v96, v73, v77
	v_cvt_f32_i32_sdwa v100, sext(v74) dst_sel:DWORD dst_unused:UNUSED_PAD src0_sel:BYTE_0
	v_dot4c_i32_i8_e32 v96, v74, v78
	v_cvt_f32_i32_sdwa v101, sext(v75) dst_sel:DWORD dst_unused:UNUSED_PAD src0_sel:BYTE_0
	v_dot4c_i32_i8_e32 v96, v75, v79
	v_fma_f32 v97, v98, v4, 0
	v_cvt_f32_i32_sdwa v98, sext(v72) dst_sel:DWORD dst_unused:UNUSED_PAD src0_sel:BYTE_1
	v_fmac_f32_e32 v97, v99, v8
	v_cvt_f32_i32_sdwa v99, sext(v73) dst_sel:DWORD dst_unused:UNUSED_PAD src0_sel:BYTE_1
	v_fmac_f32_e32 v97, v100, v12
	v_cvt_f32_i32_sdwa v100, sext(v74) dst_sel:DWORD dst_unused:UNUSED_PAD src0_sel:BYTE_1
	v_fmac_f32_e32 v97, v101, v16
	v_cvt_f32_i32_sdwa v101, sext(v75) dst_sel:DWORD dst_unused:UNUSED_PAD src0_sel:BYTE_1
	v_add_u32_dpp v96, v96, v96 quad_perm:[1,0,3,2] row_mask:0xf bank_mask:0xf bound_ctrl:1
	v_fmac_f32_e32 v97, v98, v5
	v_cvt_f32_i32_sdwa v98, sext(v72) dst_sel:DWORD dst_unused:UNUSED_PAD src0_sel:BYTE_2
	v_fmac_f32_e32 v97, v99, v9
	v_cvt_f32_i32_sdwa v99, sext(v73) dst_sel:DWORD dst_unused:UNUSED_PAD src0_sel:BYTE_2
	v_fmac_f32_e32 v97, v100, v13
	v_cvt_f32_i32_sdwa v100, sext(v74) dst_sel:DWORD dst_unused:UNUSED_PAD src0_sel:BYTE_2
	v_add_u32_dpp v96, v96, v96 quad_perm:[2,3,0,1] row_mask:0xf bank_mask:0xf bound_ctrl:1
	v_fmac_f32_e32 v97, v101, v17
	v_cvt_f32_i32_sdwa v101, sext(v75) dst_sel:DWORD dst_unused:UNUSED_PAD src0_sel:BYTE_2
	v_fmac_f32_e32 v97, v98, v6
	v_cvt_f32_i32_sdwa v98, sext(v72) dst_sel:DWORD dst_unused:UNUSED_PAD src0_sel:BYTE_3
	v_fmac_f32_e32 v97, v99, v10
	v_cvt_f32_i32_sdwa v99, sext(v73) dst_sel:DWORD dst_unused:UNUSED_PAD src0_sel:BYTE_3
	v_add_u32_dpp v96, v96, v96 row_half_mirror row_mask:0xf bank_mask:0xf bound_ctrl:1
	v_fmac_f32_e32 v97, v100, v14
	v_cvt_f32_i32_sdwa v100, sext(v74) dst_sel:DWORD dst_unused:UNUSED_PAD src0_sel:BYTE_3
	v_fmac_f32_e32 v97, v101, v18
	v_cvt_f32_i32_sdwa v101, sext(v75) dst_sel:DWORD dst_unused:UNUSED_PAD src0_sel:BYTE_3
	v_fmac_f32_e32 v97, v98, v7
	v_fmac_f32_e32 v97, v99, v11
	v_fmac_f32_e32 v97, v100, v15
	v_fmac_f32_e32 v97, v101, v19
	v_cndmask_b32_e64 v102, v102, v96, s[50:51]
	s_waitcnt lgkmcnt(0)
	v_add_f32_dpp v97, v97, v97 quad_perm:[1,0,3,2] row_mask:0xf bank_mask:0xf bound_ctrl:1
	v_lshl_add_u32 v106, v104, 7, v2
	v_lshl_add_u32 v107, v105, 7, v2
	v_add_f32_dpp v97, v97, v97 quad_perm:[2,3,0,1] row_mask:0xf bank_mask:0xf bound_ctrl:1
	global_load_dwordx4 v[72:75], v106, s[18:19]
	global_load_dwordx4 v[76:79], v107, s[18:19]
	v_add_f32_dpp v97, v97, v97 row_half_mirror row_mask:0xf bank_mask:0xf bound_ctrl:1
	v_cndmask_b32_e64 v103, v103, v97, s[50:51]
	ds_bpermute_b32 v104, v3, v23 offset:192
	ds_bpermute_b32 v105, v3, v27 offset:192
	s_waitcnt vmcnt(16)
	v_mov_b32_e32 v96, 0
	v_dot4c_i32_i8_e32 v96, v80, v84
	v_cvt_f32_i32_sdwa v98, sext(v80) dst_sel:DWORD dst_unused:UNUSED_PAD src0_sel:BYTE_0
	v_cvt_f32_i32_sdwa v99, sext(v81) dst_sel:DWORD dst_unused:UNUSED_PAD src0_sel:BYTE_0
	v_dot4c_i32_i8_e32 v96, v81, v85
	v_cvt_f32_i32_sdwa v100, sext(v82) dst_sel:DWORD dst_unused:UNUSED_PAD src0_sel:BYTE_0
	v_dot4c_i32_i8_e32 v96, v82, v86
	v_cvt_f32_i32_sdwa v101, sext(v83) dst_sel:DWORD dst_unused:UNUSED_PAD src0_sel:BYTE_0
	v_dot4c_i32_i8_e32 v96, v83, v87
	v_fma_f32 v97, v98, v4, 0
	v_cvt_f32_i32_sdwa v98, sext(v80) dst_sel:DWORD dst_unused:UNUSED_PAD src0_sel:BYTE_1
	v_fmac_f32_e32 v97, v99, v8
	v_cvt_f32_i32_sdwa v99, sext(v81) dst_sel:DWORD dst_unused:UNUSED_PAD src0_sel:BYTE_1
	v_fmac_f32_e32 v97, v100, v12
	v_cvt_f32_i32_sdwa v100, sext(v82) dst_sel:DWORD dst_unused:UNUSED_PAD src0_sel:BYTE_1
	v_fmac_f32_e32 v97, v101, v16
	v_cvt_f32_i32_sdwa v101, sext(v83) dst_sel:DWORD dst_unused:UNUSED_PAD src0_sel:BYTE_1
	v_add_u32_dpp v96, v96, v96 quad_perm:[1,0,3,2] row_mask:0xf bank_mask:0xf bound_ctrl:1
	v_fmac_f32_e32 v97, v98, v5
	v_cvt_f32_i32_sdwa v98, sext(v80) dst_sel:DWORD dst_unused:UNUSED_PAD src0_sel:BYTE_2
	v_fmac_f32_e32 v97, v99, v9
	v_cvt_f32_i32_sdwa v99, sext(v81) dst_sel:DWORD dst_unused:UNUSED_PAD src0_sel:BYTE_2
	v_fmac_f32_e32 v97, v100, v13
	v_cvt_f32_i32_sdwa v100, sext(v82) dst_sel:DWORD dst_unused:UNUSED_PAD src0_sel:BYTE_2
	v_add_u32_dpp v96, v96, v96 quad_perm:[2,3,0,1] row_mask:0xf bank_mask:0xf bound_ctrl:1
	v_fmac_f32_e32 v97, v101, v17
	v_cvt_f32_i32_sdwa v101, sext(v83) dst_sel:DWORD dst_unused:UNUSED_PAD src0_sel:BYTE_2
	v_fmac_f32_e32 v97, v98, v6
	v_cvt_f32_i32_sdwa v98, sext(v80) dst_sel:DWORD dst_unused:UNUSED_PAD src0_sel:BYTE_3
	v_fmac_f32_e32 v97, v99, v10
	v_cvt_f32_i32_sdwa v99, sext(v81) dst_sel:DWORD dst_unused:UNUSED_PAD src0_sel:BYTE_3
	v_add_u32_dpp v96, v96, v96 row_half_mirror row_mask:0xf bank_mask:0xf bound_ctrl:1
	v_fmac_f32_e32 v97, v100, v14
	v_cvt_f32_i32_sdwa v100, sext(v82) dst_sel:DWORD dst_unused:UNUSED_PAD src0_sel:BYTE_3
	v_fmac_f32_e32 v97, v101, v18
	v_cvt_f32_i32_sdwa v101, sext(v83) dst_sel:DWORD dst_unused:UNUSED_PAD src0_sel:BYTE_3
	v_fmac_f32_e32 v97, v98, v7
	v_fmac_f32_e32 v97, v99, v11
	v_fmac_f32_e32 v97, v100, v15
	v_fmac_f32_e32 v97, v101, v19
	v_cndmask_b32_e64 v102, v102, v96, s[52:53]
	s_waitcnt lgkmcnt(0)
	v_add_f32_dpp v97, v97, v97 quad_perm:[1,0,3,2] row_mask:0xf bank_mask:0xf bound_ctrl:1
	v_lshl_add_u32 v106, v104, 7, v2
	v_lshl_add_u32 v107, v105, 7, v2
	v_add_f32_dpp v97, v97, v97 quad_perm:[2,3,0,1] row_mask:0xf bank_mask:0xf bound_ctrl:1
	global_load_dwordx4 v[80:83], v106, s[18:19]
	global_load_dwordx4 v[84:87], v107, s[18:19]
	v_add_f32_dpp v97, v97, v97 row_half_mirror row_mask:0xf bank_mask:0xf bound_ctrl:1
	v_cndmask_b32_e64 v103, v103, v97, s[52:53]
	ds_bpermute_b32 v104, v3, v23 offset:224
	ds_bpermute_b32 v105, v3, v27 offset:224
	s_waitcnt vmcnt(16)
	v_mov_b32_e32 v96, 0
	v_dot4c_i32_i8_e32 v96, v88, v92
	v_cvt_f32_i32_sdwa v98, sext(v88) dst_sel:DWORD dst_unused:UNUSED_PAD src0_sel:BYTE_0
	v_cvt_f32_i32_sdwa v99, sext(v89) dst_sel:DWORD dst_unused:UNUSED_PAD src0_sel:BYTE_0
	v_dot4c_i32_i8_e32 v96, v89, v93
	v_cvt_f32_i32_sdwa v100, sext(v90) dst_sel:DWORD dst_unused:UNUSED_PAD src0_sel:BYTE_0
	v_dot4c_i32_i8_e32 v96, v90, v94
	v_cvt_f32_i32_sdwa v101, sext(v91) dst_sel:DWORD dst_unused:UNUSED_PAD src0_sel:BYTE_0
	v_dot4c_i32_i8_e32 v96, v91, v95
	v_fma_f32 v97, v98, v4, 0
	v_cvt_f32_i32_sdwa v98, sext(v88) dst_sel:DWORD dst_unused:UNUSED_PAD src0_sel:BYTE_1
	v_fmac_f32_e32 v97, v99, v8
	v_cvt_f32_i32_sdwa v99, sext(v89) dst_sel:DWORD dst_unused:UNUSED_PAD src0_sel:BYTE_1
	v_fmac_f32_e32 v97, v100, v12
	v_cvt_f32_i32_sdwa v100, sext(v90) dst_sel:DWORD dst_unused:UNUSED_PAD src0_sel:BYTE_1
	v_fmac_f32_e32 v97, v101, v16
	v_cvt_f32_i32_sdwa v101, sext(v91) dst_sel:DWORD dst_unused:UNUSED_PAD src0_sel:BYTE_1
	v_add_u32_dpp v96, v96, v96 quad_perm:[1,0,3,2] row_mask:0xf bank_mask:0xf bound_ctrl:1
	v_fmac_f32_e32 v97, v98, v5
	v_cvt_f32_i32_sdwa v98, sext(v88) dst_sel:DWORD dst_unused:UNUSED_PAD src0_sel:BYTE_2
	v_fmac_f32_e32 v97, v99, v9
	v_cvt_f32_i32_sdwa v99, sext(v89) dst_sel:DWORD dst_unused:UNUSED_PAD src0_sel:BYTE_2
	v_fmac_f32_e32 v97, v100, v13
	v_cvt_f32_i32_sdwa v100, sext(v90) dst_sel:DWORD dst_unused:UNUSED_PAD src0_sel:BYTE_2
	v_add_u32_dpp v96, v96, v96 quad_perm:[2,3,0,1] row_mask:0xf bank_mask:0xf bound_ctrl:1
	v_fmac_f32_e32 v97, v101, v17
	v_cvt_f32_i32_sdwa v101, sext(v91) dst_sel:DWORD dst_unused:UNUSED_PAD src0_sel:BYTE_2
	v_fmac_f32_e32 v97, v98, v6
	v_cvt_f32_i32_sdwa v98, sext(v88) dst_sel:DWORD dst_unused:UNUSED_PAD src0_sel:BYTE_3
	v_fmac_f32_e32 v97, v99, v10
	v_cvt_f32_i32_sdwa v99, sext(v89) dst_sel:DWORD dst_unused:UNUSED_PAD src0_sel:BYTE_3
	v_add_u32_dpp v96, v96, v96 row_half_mirror row_mask:0xf bank_mask:0xf bound_ctrl:1
	v_fmac_f32_e32 v97, v100, v14
	v_cvt_f32_i32_sdwa v100, sext(v90) dst_sel:DWORD dst_unused:UNUSED_PAD src0_sel:BYTE_3
	v_fmac_f32_e32 v97, v101, v18
	v_cvt_f32_i32_sdwa v101, sext(v91) dst_sel:DWORD dst_unused:UNUSED_PAD src0_sel:BYTE_3
	v_fmac_f32_e32 v97, v98, v7
	v_fmac_f32_e32 v97, v99, v11
	v_fmac_f32_e32 v97, v100, v15
	v_fmac_f32_e32 v97, v101, v19
	v_cndmask_b32_e64 v102, v102, v96, s[54:55]
	s_waitcnt lgkmcnt(0)
	v_add_f32_dpp v97, v97, v97 quad_perm:[1,0,3,2] row_mask:0xf bank_mask:0xf bound_ctrl:1
	v_lshl_add_u32 v106, v104, 7, v2
	v_lshl_add_u32 v107, v105, 7, v2
	v_add_f32_dpp v97, v97, v97 quad_perm:[2,3,0,1] row_mask:0xf bank_mask:0xf bound_ctrl:1
	global_load_dwordx4 v[88:91], v106, s[18:19]
	global_load_dwordx4 v[92:95], v107, s[18:19]
	v_add_f32_dpp v97, v97, v97 row_half_mirror row_mask:0xf bank_mask:0xf bound_ctrl:1
	v_cndmask_b32_e64 v103, v103, v97, s[54:55]
	global_store_dword v28, v102, s[20:21] offset:512
	global_store_dword v28, v103, s[22:23] offset:512
	s_waitcnt vmcnt(16)
	v_mov_b32_e32 v96, 0
	v_dot4c_i32_i8_e32 v96, v32, v36
	v_cvt_f32_i32_sdwa v98, sext(v32) dst_sel:DWORD dst_unused:UNUSED_PAD src0_sel:BYTE_0
	v_cvt_f32_i32_sdwa v99, sext(v33) dst_sel:DWORD dst_unused:UNUSED_PAD src0_sel:BYTE_0
	v_dot4c_i32_i8_e32 v96, v33, v37
	v_cvt_f32_i32_sdwa v100, sext(v34) dst_sel:DWORD dst_unused:UNUSED_PAD src0_sel:BYTE_0
	v_dot4c_i32_i8_e32 v96, v34, v38
	v_cvt_f32_i32_sdwa v101, sext(v35) dst_sel:DWORD dst_unused:UNUSED_PAD src0_sel:BYTE_0
	v_dot4c_i32_i8_e32 v96, v35, v39
	v_fma_f32 v97, v98, v4, 0
	v_cvt_f32_i32_sdwa v98, sext(v32) dst_sel:DWORD dst_unused:UNUSED_PAD src0_sel:BYTE_1
	v_fmac_f32_e32 v97, v99, v8
	v_cvt_f32_i32_sdwa v99, sext(v33) dst_sel:DWORD dst_unused:UNUSED_PAD src0_sel:BYTE_1
	v_fmac_f32_e32 v97, v100, v12
	v_cvt_f32_i32_sdwa v100, sext(v34) dst_sel:DWORD dst_unused:UNUSED_PAD src0_sel:BYTE_1
	v_fmac_f32_e32 v97, v101, v16
	v_cvt_f32_i32_sdwa v101, sext(v35) dst_sel:DWORD dst_unused:UNUSED_PAD src0_sel:BYTE_1
	v_add_u32_dpp v96, v96, v96 quad_perm:[1,0,3,2] row_mask:0xf bank_mask:0xf bound_ctrl:1
	v_fmac_f32_e32 v97, v98, v5
	v_cvt_f32_i32_sdwa v98, sext(v32) dst_sel:DWORD dst_unused:UNUSED_PAD src0_sel:BYTE_2
	v_fmac_f32_e32 v97, v99, v9
	v_cvt_f32_i32_sdwa v99, sext(v33) dst_sel:DWORD dst_unused:UNUSED_PAD src0_sel:BYTE_2
	v_fmac_f32_e32 v97, v100, v13
	v_cvt_f32_i32_sdwa v100, sext(v34) dst_sel:DWORD dst_unused:UNUSED_PAD src0_sel:BYTE_2
	v_add_u32_dpp v96, v96, v96 quad_perm:[2,3,0,1] row_mask:0xf bank_mask:0xf bound_ctrl:1
	v_fmac_f32_e32 v97, v101, v17
	v_cvt_f32_i32_sdwa v101, sext(v35) dst_sel:DWORD dst_unused:UNUSED_PAD src0_sel:BYTE_2
	v_fmac_f32_e32 v97, v98, v6
	v_cvt_f32_i32_sdwa v98, sext(v32) dst_sel:DWORD dst_unused:UNUSED_PAD src0_sel:BYTE_3
	v_fmac_f32_e32 v97, v99, v10
	v_cvt_f32_i32_sdwa v99, sext(v33) dst_sel:DWORD dst_unused:UNUSED_PAD src0_sel:BYTE_3
	v_add_u32_dpp v96, v96, v96 row_half_mirror row_mask:0xf bank_mask:0xf bound_ctrl:1
	v_fmac_f32_e32 v97, v100, v14
	v_cvt_f32_i32_sdwa v100, sext(v34) dst_sel:DWORD dst_unused:UNUSED_PAD src0_sel:BYTE_3
	v_fmac_f32_e32 v97, v101, v18
	v_cvt_f32_i32_sdwa v101, sext(v35) dst_sel:DWORD dst_unused:UNUSED_PAD src0_sel:BYTE_3
	v_fmac_f32_e32 v97, v98, v7
	v_fmac_f32_e32 v97, v99, v11
	v_fmac_f32_e32 v97, v100, v15
	v_fmac_f32_e32 v97, v101, v19
	v_cndmask_b32_e64 v102, 0, v96, s[40:41]
	s_nop 0
	v_add_f32_dpp v97, v97, v97 quad_perm:[1,0,3,2] row_mask:0xf bank_mask:0xf bound_ctrl:1
	s_nop 1
	v_add_f32_dpp v97, v97, v97 quad_perm:[2,3,0,1] row_mask:0xf bank_mask:0xf bound_ctrl:1
	s_nop 1
	v_add_f32_dpp v97, v97, v97 row_half_mirror row_mask:0xf bank_mask:0xf bound_ctrl:1
	v_cndmask_b32_e64 v103, 0, v97, s[40:41]
	s_waitcnt vmcnt(14)
	v_mov_b32_e32 v96, 0
	v_dot4c_i32_i8_e32 v96, v40, v44
	v_cvt_f32_i32_sdwa v98, sext(v40) dst_sel:DWORD dst_unused:UNUSED_PAD src0_sel:BYTE_0
	v_cvt_f32_i32_sdwa v99, sext(v41) dst_sel:DWORD dst_unused:UNUSED_PAD src0_sel:BYTE_0
	v_dot4c_i32_i8_e32 v96, v41, v45
	v_cvt_f32_i32_sdwa v100, sext(v42) dst_sel:DWORD dst_unused:UNUSED_PAD src0_sel:BYTE_0
	v_dot4c_i32_i8_e32 v96, v42, v46
	v_cvt_f32_i32_sdwa v101, sext(v43) dst_sel:DWORD dst_unused:UNUSED_PAD src0_sel:BYTE_0
	v_dot4c_i32_i8_e32 v96, v43, v47
	v_fma_f32 v97, v98, v4, 0
	v_cvt_f32_i32_sdwa v98, sext(v40) dst_sel:DWORD dst_unused:UNUSED_PAD src0_sel:BYTE_1
	v_fmac_f32_e32 v97, v99, v8
	v_cvt_f32_i32_sdwa v99, sext(v41) dst_sel:DWORD dst_unused:UNUSED_PAD src0_sel:BYTE_1
	v_fmac_f32_e32 v97, v100, v12
	v_cvt_f32_i32_sdwa v100, sext(v42) dst_sel:DWORD dst_unused:UNUSED_PAD src0_sel:BYTE_1
	v_fmac_f32_e32 v97, v101, v16
	v_cvt_f32_i32_sdwa v101, sext(v43) dst_sel:DWORD dst_unused:UNUSED_PAD src0_sel:BYTE_1
	v_add_u32_dpp v96, v96, v96 quad_perm:[1,0,3,2] row_mask:0xf bank_mask:0xf bound_ctrl:1
	v_fmac_f32_e32 v97, v98, v5
	v_cvt_f32_i32_sdwa v98, sext(v40) dst_sel:DWORD dst_unused:UNUSED_PAD src0_sel:BYTE_2
	v_fmac_f32_e32 v97, v99, v9
	v_cvt_f32_i32_sdwa v99, sext(v41) dst_sel:DWORD dst_unused:UNUSED_PAD src0_sel:BYTE_2
	v_fmac_f32_e32 v97, v100, v13
	v_cvt_f32_i32_sdwa v100, sext(v42) dst_sel:DWORD dst_unused:UNUSED_PAD src0_sel:BYTE_2
	v_add_u32_dpp v96, v96, v96 quad_perm:[2,3,0,1] row_mask:0xf bank_mask:0xf bound_ctrl:1
	v_fmac_f32_e32 v97, v101, v17
	v_cvt_f32_i32_sdwa v101, sext(v43) dst_sel:DWORD dst_unused:UNUSED_PAD src0_sel:BYTE_2
	v_fmac_f32_e32 v97, v98, v6
	v_cvt_f32_i32_sdwa v98, sext(v40) dst_sel:DWORD dst_unused:UNUSED_PAD src0_sel:BYTE_3
	v_fmac_f32_e32 v97, v99, v10
	v_cvt_f32_i32_sdwa v99, sext(v41) dst_sel:DWORD dst_unused:UNUSED_PAD src0_sel:BYTE_3
	v_add_u32_dpp v96, v96, v96 row_half_mirror row_mask:0xf bank_mask:0xf bound_ctrl:1
	v_fmac_f32_e32 v97, v100, v14
	v_cvt_f32_i32_sdwa v100, sext(v42) dst_sel:DWORD dst_unused:UNUSED_PAD src0_sel:BYTE_3
	v_fmac_f32_e32 v97, v101, v18
	v_cvt_f32_i32_sdwa v101, sext(v43) dst_sel:DWORD dst_unused:UNUSED_PAD src0_sel:BYTE_3
	v_fmac_f32_e32 v97, v98, v7
	v_fmac_f32_e32 v97, v99, v11
	v_fmac_f32_e32 v97, v100, v15
	v_fmac_f32_e32 v97, v101, v19
	v_cndmask_b32_e64 v102, v102, v96, s[42:43]
	s_nop 0
	v_add_f32_dpp v97, v97, v97 quad_perm:[1,0,3,2] row_mask:0xf bank_mask:0xf bound_ctrl:1
	s_nop 1
	v_add_f32_dpp v97, v97, v97 quad_perm:[2,3,0,1] row_mask:0xf bank_mask:0xf bound_ctrl:1
	s_nop 1
	v_add_f32_dpp v97, v97, v97 row_half_mirror row_mask:0xf bank_mask:0xf bound_ctrl:1
	v_cndmask_b32_e64 v103, v103, v97, s[42:43]
	s_waitcnt vmcnt(12)
	v_mov_b32_e32 v96, 0
	v_dot4c_i32_i8_e32 v96, v48, v52
	v_cvt_f32_i32_sdwa v98, sext(v48) dst_sel:DWORD dst_unused:UNUSED_PAD src0_sel:BYTE_0
	v_cvt_f32_i32_sdwa v99, sext(v49) dst_sel:DWORD dst_unused:UNUSED_PAD src0_sel:BYTE_0
	v_dot4c_i32_i8_e32 v96, v49, v53
	v_cvt_f32_i32_sdwa v100, sext(v50) dst_sel:DWORD dst_unused:UNUSED_PAD src0_sel:BYTE_0
	v_dot4c_i32_i8_e32 v96, v50, v54
	v_cvt_f32_i32_sdwa v101, sext(v51) dst_sel:DWORD dst_unused:UNUSED_PAD src0_sel:BYTE_0
	v_dot4c_i32_i8_e32 v96, v51, v55
	v_fma_f32 v97, v98, v4, 0
	v_cvt_f32_i32_sdwa v98, sext(v48) dst_sel:DWORD dst_unused:UNUSED_PAD src0_sel:BYTE_1
	v_fmac_f32_e32 v97, v99, v8
	v_cvt_f32_i32_sdwa v99, sext(v49) dst_sel:DWORD dst_unused:UNUSED_PAD src0_sel:BYTE_1
	v_fmac_f32_e32 v97, v100, v12
	v_cvt_f32_i32_sdwa v100, sext(v50) dst_sel:DWORD dst_unused:UNUSED_PAD src0_sel:BYTE_1
	v_fmac_f32_e32 v97, v101, v16
	v_cvt_f32_i32_sdwa v101, sext(v51) dst_sel:DWORD dst_unused:UNUSED_PAD src0_sel:BYTE_1
	v_add_u32_dpp v96, v96, v96 quad_perm:[1,0,3,2] row_mask:0xf bank_mask:0xf bound_ctrl:1
	v_fmac_f32_e32 v97, v98, v5
	v_cvt_f32_i32_sdwa v98, sext(v48) dst_sel:DWORD dst_unused:UNUSED_PAD src0_sel:BYTE_2
	v_fmac_f32_e32 v97, v99, v9
	v_cvt_f32_i32_sdwa v99, sext(v49) dst_sel:DWORD dst_unused:UNUSED_PAD src0_sel:BYTE_2
	v_fmac_f32_e32 v97, v100, v13
	v_cvt_f32_i32_sdwa v100, sext(v50) dst_sel:DWORD dst_unused:UNUSED_PAD src0_sel:BYTE_2
	v_add_u32_dpp v96, v96, v96 quad_perm:[2,3,0,1] row_mask:0xf bank_mask:0xf bound_ctrl:1
	v_fmac_f32_e32 v97, v101, v17
	v_cvt_f32_i32_sdwa v101, sext(v51) dst_sel:DWORD dst_unused:UNUSED_PAD src0_sel:BYTE_2
	v_fmac_f32_e32 v97, v98, v6
	v_cvt_f32_i32_sdwa v98, sext(v48) dst_sel:DWORD dst_unused:UNUSED_PAD src0_sel:BYTE_3
	v_fmac_f32_e32 v97, v99, v10
	v_cvt_f32_i32_sdwa v99, sext(v49) dst_sel:DWORD dst_unused:UNUSED_PAD src0_sel:BYTE_3
	v_add_u32_dpp v96, v96, v96 row_half_mirror row_mask:0xf bank_mask:0xf bound_ctrl:1
	v_fmac_f32_e32 v97, v100, v14
	v_cvt_f32_i32_sdwa v100, sext(v50) dst_sel:DWORD dst_unused:UNUSED_PAD src0_sel:BYTE_3
	v_fmac_f32_e32 v97, v101, v18
	v_cvt_f32_i32_sdwa v101, sext(v51) dst_sel:DWORD dst_unused:UNUSED_PAD src0_sel:BYTE_3
	v_fmac_f32_e32 v97, v98, v7
	v_fmac_f32_e32 v97, v99, v11
	v_fmac_f32_e32 v97, v100, v15
	v_fmac_f32_e32 v97, v101, v19
	v_cndmask_b32_e64 v102, v102, v96, s[44:45]
	s_nop 0
	v_add_f32_dpp v97, v97, v97 quad_perm:[1,0,3,2] row_mask:0xf bank_mask:0xf bound_ctrl:1
	s_nop 1
	v_add_f32_dpp v97, v97, v97 quad_perm:[2,3,0,1] row_mask:0xf bank_mask:0xf bound_ctrl:1
	s_nop 1
	v_add_f32_dpp v97, v97, v97 row_half_mirror row_mask:0xf bank_mask:0xf bound_ctrl:1
	v_cndmask_b32_e64 v103, v103, v97, s[44:45]
	s_waitcnt vmcnt(10)
	v_mov_b32_e32 v96, 0
	v_dot4c_i32_i8_e32 v96, v56, v60
	v_cvt_f32_i32_sdwa v98, sext(v56) dst_sel:DWORD dst_unused:UNUSED_PAD src0_sel:BYTE_0
	v_cvt_f32_i32_sdwa v99, sext(v57) dst_sel:DWORD dst_unused:UNUSED_PAD src0_sel:BYTE_0
	v_dot4c_i32_i8_e32 v96, v57, v61
	v_cvt_f32_i32_sdwa v100, sext(v58) dst_sel:DWORD dst_unused:UNUSED_PAD src0_sel:BYTE_0
	v_dot4c_i32_i8_e32 v96, v58, v62
	v_cvt_f32_i32_sdwa v101, sext(v59) dst_sel:DWORD dst_unused:UNUSED_PAD src0_sel:BYTE_0
	v_dot4c_i32_i8_e32 v96, v59, v63
	v_fma_f32 v97, v98, v4, 0
	v_cvt_f32_i32_sdwa v98, sext(v56) dst_sel:DWORD dst_unused:UNUSED_PAD src0_sel:BYTE_1
	v_fmac_f32_e32 v97, v99, v8
	v_cvt_f32_i32_sdwa v99, sext(v57) dst_sel:DWORD dst_unused:UNUSED_PAD src0_sel:BYTE_1
	v_fmac_f32_e32 v97, v100, v12
	v_cvt_f32_i32_sdwa v100, sext(v58) dst_sel:DWORD dst_unused:UNUSED_PAD src0_sel:BYTE_1
	v_fmac_f32_e32 v97, v101, v16
	v_cvt_f32_i32_sdwa v101, sext(v59) dst_sel:DWORD dst_unused:UNUSED_PAD src0_sel:BYTE_1
	v_add_u32_dpp v96, v96, v96 quad_perm:[1,0,3,2] row_mask:0xf bank_mask:0xf bound_ctrl:1
	v_fmac_f32_e32 v97, v98, v5
	v_cvt_f32_i32_sdwa v98, sext(v56) dst_sel:DWORD dst_unused:UNUSED_PAD src0_sel:BYTE_2
	v_fmac_f32_e32 v97, v99, v9
	v_cvt_f32_i32_sdwa v99, sext(v57) dst_sel:DWORD dst_unused:UNUSED_PAD src0_sel:BYTE_2
	v_fmac_f32_e32 v97, v100, v13
	v_cvt_f32_i32_sdwa v100, sext(v58) dst_sel:DWORD dst_unused:UNUSED_PAD src0_sel:BYTE_2
	v_add_u32_dpp v96, v96, v96 quad_perm:[2,3,0,1] row_mask:0xf bank_mask:0xf bound_ctrl:1
	v_fmac_f32_e32 v97, v101, v17
	v_cvt_f32_i32_sdwa v101, sext(v59) dst_sel:DWORD dst_unused:UNUSED_PAD src0_sel:BYTE_2
	v_fmac_f32_e32 v97, v98, v6
	v_cvt_f32_i32_sdwa v98, sext(v56) dst_sel:DWORD dst_unused:UNUSED_PAD src0_sel:BYTE_3
	v_fmac_f32_e32 v97, v99, v10
	v_cvt_f32_i32_sdwa v99, sext(v57) dst_sel:DWORD dst_unused:UNUSED_PAD src0_sel:BYTE_3
	v_add_u32_dpp v96, v96, v96 row_half_mirror row_mask:0xf bank_mask:0xf bound_ctrl:1
	v_fmac_f32_e32 v97, v100, v14
	v_cvt_f32_i32_sdwa v100, sext(v58) dst_sel:DWORD dst_unused:UNUSED_PAD src0_sel:BYTE_3
	v_fmac_f32_e32 v97, v101, v18
	v_cvt_f32_i32_sdwa v101, sext(v59) dst_sel:DWORD dst_unused:UNUSED_PAD src0_sel:BYTE_3
	v_fmac_f32_e32 v97, v98, v7
	v_fmac_f32_e32 v97, v99, v11
	v_fmac_f32_e32 v97, v100, v15
	v_fmac_f32_e32 v97, v101, v19
	v_cndmask_b32_e64 v102, v102, v96, s[46:47]
	s_nop 0
	v_add_f32_dpp v97, v97, v97 quad_perm:[1,0,3,2] row_mask:0xf bank_mask:0xf bound_ctrl:1
	s_nop 1
	v_add_f32_dpp v97, v97, v97 quad_perm:[2,3,0,1] row_mask:0xf bank_mask:0xf bound_ctrl:1
	s_nop 1
	v_add_f32_dpp v97, v97, v97 row_half_mirror row_mask:0xf bank_mask:0xf bound_ctrl:1
	v_cndmask_b32_e64 v103, v103, v97, s[46:47]
	s_waitcnt vmcnt(8)
	v_mov_b32_e32 v96, 0
	v_dot4c_i32_i8_e32 v96, v64, v68
	v_cvt_f32_i32_sdwa v98, sext(v64) dst_sel:DWORD dst_unused:UNUSED_PAD src0_sel:BYTE_0
	v_cvt_f32_i32_sdwa v99, sext(v65) dst_sel:DWORD dst_unused:UNUSED_PAD src0_sel:BYTE_0
	v_dot4c_i32_i8_e32 v96, v65, v69
	v_cvt_f32_i32_sdwa v100, sext(v66) dst_sel:DWORD dst_unused:UNUSED_PAD src0_sel:BYTE_0
	v_dot4c_i32_i8_e32 v96, v66, v70
	v_cvt_f32_i32_sdwa v101, sext(v67) dst_sel:DWORD dst_unused:UNUSED_PAD src0_sel:BYTE_0
	v_dot4c_i32_i8_e32 v96, v67, v71
	v_fma_f32 v97, v98, v4, 0
	v_cvt_f32_i32_sdwa v98, sext(v64) dst_sel:DWORD dst_unused:UNUSED_PAD src0_sel:BYTE_1
	v_fmac_f32_e32 v97, v99, v8
	v_cvt_f32_i32_sdwa v99, sext(v65) dst_sel:DWORD dst_unused:UNUSED_PAD src0_sel:BYTE_1
	v_fmac_f32_e32 v97, v100, v12
	v_cvt_f32_i32_sdwa v100, sext(v66) dst_sel:DWORD dst_unused:UNUSED_PAD src0_sel:BYTE_1
	v_fmac_f32_e32 v97, v101, v16
	v_cvt_f32_i32_sdwa v101, sext(v67) dst_sel:DWORD dst_unused:UNUSED_PAD src0_sel:BYTE_1
	v_add_u32_dpp v96, v96, v96 quad_perm:[1,0,3,2] row_mask:0xf bank_mask:0xf bound_ctrl:1
	v_fmac_f32_e32 v97, v98, v5
	v_cvt_f32_i32_sdwa v98, sext(v64) dst_sel:DWORD dst_unused:UNUSED_PAD src0_sel:BYTE_2
	v_fmac_f32_e32 v97, v99, v9
	v_cvt_f32_i32_sdwa v99, sext(v65) dst_sel:DWORD dst_unused:UNUSED_PAD src0_sel:BYTE_2
	v_fmac_f32_e32 v97, v100, v13
	v_cvt_f32_i32_sdwa v100, sext(v66) dst_sel:DWORD dst_unused:UNUSED_PAD src0_sel:BYTE_2
	v_add_u32_dpp v96, v96, v96 quad_perm:[2,3,0,1] row_mask:0xf bank_mask:0xf bound_ctrl:1
	v_fmac_f32_e32 v97, v101, v17
	v_cvt_f32_i32_sdwa v101, sext(v67) dst_sel:DWORD dst_unused:UNUSED_PAD src0_sel:BYTE_2
	v_fmac_f32_e32 v97, v98, v6
	v_cvt_f32_i32_sdwa v98, sext(v64) dst_sel:DWORD dst_unused:UNUSED_PAD src0_sel:BYTE_3
	v_fmac_f32_e32 v97, v99, v10
	v_cvt_f32_i32_sdwa v99, sext(v65) dst_sel:DWORD dst_unused:UNUSED_PAD src0_sel:BYTE_3
	v_add_u32_dpp v96, v96, v96 row_half_mirror row_mask:0xf bank_mask:0xf bound_ctrl:1
	v_fmac_f32_e32 v97, v100, v14
	v_cvt_f32_i32_sdwa v100, sext(v66) dst_sel:DWORD dst_unused:UNUSED_PAD src0_sel:BYTE_3
	v_fmac_f32_e32 v97, v101, v18
	v_cvt_f32_i32_sdwa v101, sext(v67) dst_sel:DWORD dst_unused:UNUSED_PAD src0_sel:BYTE_3
	v_fmac_f32_e32 v97, v98, v7
	v_fmac_f32_e32 v97, v99, v11
	v_fmac_f32_e32 v97, v100, v15
	v_fmac_f32_e32 v97, v101, v19
	v_cndmask_b32_e64 v102, v102, v96, s[48:49]
	s_nop 0
	v_add_f32_dpp v97, v97, v97 quad_perm:[1,0,3,2] row_mask:0xf bank_mask:0xf bound_ctrl:1
	s_nop 1
	v_add_f32_dpp v97, v97, v97 quad_perm:[2,3,0,1] row_mask:0xf bank_mask:0xf bound_ctrl:1
	s_nop 1
	v_add_f32_dpp v97, v97, v97 row_half_mirror row_mask:0xf bank_mask:0xf bound_ctrl:1
	v_cndmask_b32_e64 v103, v103, v97, s[48:49]
	s_waitcnt vmcnt(6)
	v_mov_b32_e32 v96, 0
	v_dot4c_i32_i8_e32 v96, v72, v76
	v_cvt_f32_i32_sdwa v98, sext(v72) dst_sel:DWORD dst_unused:UNUSED_PAD src0_sel:BYTE_0
	v_cvt_f32_i32_sdwa v99, sext(v73) dst_sel:DWORD dst_unused:UNUSED_PAD src0_sel:BYTE_0
	v_dot4c_i32_i8_e32 v96, v73, v77
	v_cvt_f32_i32_sdwa v100, sext(v74) dst_sel:DWORD dst_unused:UNUSED_PAD src0_sel:BYTE_0
	v_dot4c_i32_i8_e32 v96, v74, v78
	v_cvt_f32_i32_sdwa v101, sext(v75) dst_sel:DWORD dst_unused:UNUSED_PAD src0_sel:BYTE_0
	v_dot4c_i32_i8_e32 v96, v75, v79
	v_fma_f32 v97, v98, v4, 0
	v_cvt_f32_i32_sdwa v98, sext(v72) dst_sel:DWORD dst_unused:UNUSED_PAD src0_sel:BYTE_1
	v_fmac_f32_e32 v97, v99, v8
	v_cvt_f32_i32_sdwa v99, sext(v73) dst_sel:DWORD dst_unused:UNUSED_PAD src0_sel:BYTE_1
	v_fmac_f32_e32 v97, v100, v12
	v_cvt_f32_i32_sdwa v100, sext(v74) dst_sel:DWORD dst_unused:UNUSED_PAD src0_sel:BYTE_1
	v_fmac_f32_e32 v97, v101, v16
	v_cvt_f32_i32_sdwa v101, sext(v75) dst_sel:DWORD dst_unused:UNUSED_PAD src0_sel:BYTE_1
	v_add_u32_dpp v96, v96, v96 quad_perm:[1,0,3,2] row_mask:0xf bank_mask:0xf bound_ctrl:1
	v_fmac_f32_e32 v97, v98, v5
	v_cvt_f32_i32_sdwa v98, sext(v72) dst_sel:DWORD dst_unused:UNUSED_PAD src0_sel:BYTE_2
	v_fmac_f32_e32 v97, v99, v9
	v_cvt_f32_i32_sdwa v99, sext(v73) dst_sel:DWORD dst_unused:UNUSED_PAD src0_sel:BYTE_2
	v_fmac_f32_e32 v97, v100, v13
	v_cvt_f32_i32_sdwa v100, sext(v74) dst_sel:DWORD dst_unused:UNUSED_PAD src0_sel:BYTE_2
	v_add_u32_dpp v96, v96, v96 quad_perm:[2,3,0,1] row_mask:0xf bank_mask:0xf bound_ctrl:1
	v_fmac_f32_e32 v97, v101, v17
	v_cvt_f32_i32_sdwa v101, sext(v75) dst_sel:DWORD dst_unused:UNUSED_PAD src0_sel:BYTE_2
	v_fmac_f32_e32 v97, v98, v6
	v_cvt_f32_i32_sdwa v98, sext(v72) dst_sel:DWORD dst_unused:UNUSED_PAD src0_sel:BYTE_3
	v_fmac_f32_e32 v97, v99, v10
	v_cvt_f32_i32_sdwa v99, sext(v73) dst_sel:DWORD dst_unused:UNUSED_PAD src0_sel:BYTE_3
	v_add_u32_dpp v96, v96, v96 row_half_mirror row_mask:0xf bank_mask:0xf bound_ctrl:1
	v_fmac_f32_e32 v97, v100, v14
	v_cvt_f32_i32_sdwa v100, sext(v74) dst_sel:DWORD dst_unused:UNUSED_PAD src0_sel:BYTE_3
	v_fmac_f32_e32 v97, v101, v18
	v_cvt_f32_i32_sdwa v101, sext(v75) dst_sel:DWORD dst_unused:UNUSED_PAD src0_sel:BYTE_3
	v_fmac_f32_e32 v97, v98, v7
	v_fmac_f32_e32 v97, v99, v11
	v_fmac_f32_e32 v97, v100, v15
	v_fmac_f32_e32 v97, v101, v19
	v_cndmask_b32_e64 v102, v102, v96, s[50:51]
	s_nop 0
	v_add_f32_dpp v97, v97, v97 quad_perm:[1,0,3,2] row_mask:0xf bank_mask:0xf bound_ctrl:1
	s_nop 1
	v_add_f32_dpp v97, v97, v97 quad_perm:[2,3,0,1] row_mask:0xf bank_mask:0xf bound_ctrl:1
	s_nop 1
	v_add_f32_dpp v97, v97, v97 row_half_mirror row_mask:0xf bank_mask:0xf bound_ctrl:1
	v_cndmask_b32_e64 v103, v103, v97, s[50:51]
	s_waitcnt vmcnt(4)
	v_mov_b32_e32 v96, 0
	v_dot4c_i32_i8_e32 v96, v80, v84
	v_cvt_f32_i32_sdwa v98, sext(v80) dst_sel:DWORD dst_unused:UNUSED_PAD src0_sel:BYTE_0
	v_cvt_f32_i32_sdwa v99, sext(v81) dst_sel:DWORD dst_unused:UNUSED_PAD src0_sel:BYTE_0
	v_dot4c_i32_i8_e32 v96, v81, v85
	v_cvt_f32_i32_sdwa v100, sext(v82) dst_sel:DWORD dst_unused:UNUSED_PAD src0_sel:BYTE_0
	v_dot4c_i32_i8_e32 v96, v82, v86
	v_cvt_f32_i32_sdwa v101, sext(v83) dst_sel:DWORD dst_unused:UNUSED_PAD src0_sel:BYTE_0
	v_dot4c_i32_i8_e32 v96, v83, v87
	v_fma_f32 v97, v98, v4, 0
	v_cvt_f32_i32_sdwa v98, sext(v80) dst_sel:DWORD dst_unused:UNUSED_PAD src0_sel:BYTE_1
	v_fmac_f32_e32 v97, v99, v8
	v_cvt_f32_i32_sdwa v99, sext(v81) dst_sel:DWORD dst_unused:UNUSED_PAD src0_sel:BYTE_1
	v_fmac_f32_e32 v97, v100, v12
	v_cvt_f32_i32_sdwa v100, sext(v82) dst_sel:DWORD dst_unused:UNUSED_PAD src0_sel:BYTE_1
	v_fmac_f32_e32 v97, v101, v16
	v_cvt_f32_i32_sdwa v101, sext(v83) dst_sel:DWORD dst_unused:UNUSED_PAD src0_sel:BYTE_1
	v_add_u32_dpp v96, v96, v96 quad_perm:[1,0,3,2] row_mask:0xf bank_mask:0xf bound_ctrl:1
	v_fmac_f32_e32 v97, v98, v5
	v_cvt_f32_i32_sdwa v98, sext(v80) dst_sel:DWORD dst_unused:UNUSED_PAD src0_sel:BYTE_2
	v_fmac_f32_e32 v97, v99, v9
	v_cvt_f32_i32_sdwa v99, sext(v81) dst_sel:DWORD dst_unused:UNUSED_PAD src0_sel:BYTE_2
	v_fmac_f32_e32 v97, v100, v13
	v_cvt_f32_i32_sdwa v100, sext(v82) dst_sel:DWORD dst_unused:UNUSED_PAD src0_sel:BYTE_2
	v_add_u32_dpp v96, v96, v96 quad_perm:[2,3,0,1] row_mask:0xf bank_mask:0xf bound_ctrl:1
	v_fmac_f32_e32 v97, v101, v17
	v_cvt_f32_i32_sdwa v101, sext(v83) dst_sel:DWORD dst_unused:UNUSED_PAD src0_sel:BYTE_2
	v_fmac_f32_e32 v97, v98, v6
	v_cvt_f32_i32_sdwa v98, sext(v80) dst_sel:DWORD dst_unused:UNUSED_PAD src0_sel:BYTE_3
	v_fmac_f32_e32 v97, v99, v10
	v_cvt_f32_i32_sdwa v99, sext(v81) dst_sel:DWORD dst_unused:UNUSED_PAD src0_sel:BYTE_3
	v_add_u32_dpp v96, v96, v96 row_half_mirror row_mask:0xf bank_mask:0xf bound_ctrl:1
	v_fmac_f32_e32 v97, v100, v14
	v_cvt_f32_i32_sdwa v100, sext(v82) dst_sel:DWORD dst_unused:UNUSED_PAD src0_sel:BYTE_3
	v_fmac_f32_e32 v97, v101, v18
	v_cvt_f32_i32_sdwa v101, sext(v83) dst_sel:DWORD dst_unused:UNUSED_PAD src0_sel:BYTE_3
	v_fmac_f32_e32 v97, v98, v7
	v_fmac_f32_e32 v97, v99, v11
	v_fmac_f32_e32 v97, v100, v15
	v_fmac_f32_e32 v97, v101, v19
	v_cndmask_b32_e64 v102, v102, v96, s[52:53]
	s_nop 0
	v_add_f32_dpp v97, v97, v97 quad_perm:[1,0,3,2] row_mask:0xf bank_mask:0xf bound_ctrl:1
	s_nop 1
	v_add_f32_dpp v97, v97, v97 quad_perm:[2,3,0,1] row_mask:0xf bank_mask:0xf bound_ctrl:1
	s_nop 1
	v_add_f32_dpp v97, v97, v97 row_half_mirror row_mask:0xf bank_mask:0xf bound_ctrl:1
	v_cndmask_b32_e64 v103, v103, v97, s[52:53]
	s_waitcnt vmcnt(2)
	v_mov_b32_e32 v96, 0
	v_dot4c_i32_i8_e32 v96, v88, v92
	v_cvt_f32_i32_sdwa v98, sext(v88) dst_sel:DWORD dst_unused:UNUSED_PAD src0_sel:BYTE_0
	v_cvt_f32_i32_sdwa v99, sext(v89) dst_sel:DWORD dst_unused:UNUSED_PAD src0_sel:BYTE_0
	v_dot4c_i32_i8_e32 v96, v89, v93
	v_cvt_f32_i32_sdwa v100, sext(v90) dst_sel:DWORD dst_unused:UNUSED_PAD src0_sel:BYTE_0
	v_dot4c_i32_i8_e32 v96, v90, v94
	v_cvt_f32_i32_sdwa v101, sext(v91) dst_sel:DWORD dst_unused:UNUSED_PAD src0_sel:BYTE_0
	v_dot4c_i32_i8_e32 v96, v91, v95
	v_fma_f32 v97, v98, v4, 0
	v_cvt_f32_i32_sdwa v98, sext(v88) dst_sel:DWORD dst_unused:UNUSED_PAD src0_sel:BYTE_1
	v_fmac_f32_e32 v97, v99, v8
	v_cvt_f32_i32_sdwa v99, sext(v89) dst_sel:DWORD dst_unused:UNUSED_PAD src0_sel:BYTE_1
	v_fmac_f32_e32 v97, v100, v12
	v_cvt_f32_i32_sdwa v100, sext(v90) dst_sel:DWORD dst_unused:UNUSED_PAD src0_sel:BYTE_1
	v_fmac_f32_e32 v97, v101, v16
	v_cvt_f32_i32_sdwa v101, sext(v91) dst_sel:DWORD dst_unused:UNUSED_PAD src0_sel:BYTE_1
	v_add_u32_dpp v96, v96, v96 quad_perm:[1,0,3,2] row_mask:0xf bank_mask:0xf bound_ctrl:1
	v_fmac_f32_e32 v97, v98, v5
	v_cvt_f32_i32_sdwa v98, sext(v88) dst_sel:DWORD dst_unused:UNUSED_PAD src0_sel:BYTE_2
	v_fmac_f32_e32 v97, v99, v9
	v_cvt_f32_i32_sdwa v99, sext(v89) dst_sel:DWORD dst_unused:UNUSED_PAD src0_sel:BYTE_2
	v_fmac_f32_e32 v97, v100, v13
	v_cvt_f32_i32_sdwa v100, sext(v90) dst_sel:DWORD dst_unused:UNUSED_PAD src0_sel:BYTE_2
	v_add_u32_dpp v96, v96, v96 quad_perm:[2,3,0,1] row_mask:0xf bank_mask:0xf bound_ctrl:1
	v_fmac_f32_e32 v97, v101, v17
	v_cvt_f32_i32_sdwa v101, sext(v91) dst_sel:DWORD dst_unused:UNUSED_PAD src0_sel:BYTE_2
	v_fmac_f32_e32 v97, v98, v6
	v_cvt_f32_i32_sdwa v98, sext(v88) dst_sel:DWORD dst_unused:UNUSED_PAD src0_sel:BYTE_3
	v_fmac_f32_e32 v97, v99, v10
	v_cvt_f32_i32_sdwa v99, sext(v89) dst_sel:DWORD dst_unused:UNUSED_PAD src0_sel:BYTE_3
	v_add_u32_dpp v96, v96, v96 row_half_mirror row_mask:0xf bank_mask:0xf bound_ctrl:1
	v_fmac_f32_e32 v97, v100, v14
	v_cvt_f32_i32_sdwa v100, sext(v90) dst_sel:DWORD dst_unused:UNUSED_PAD src0_sel:BYTE_3
	v_fmac_f32_e32 v97, v101, v18
	v_cvt_f32_i32_sdwa v101, sext(v91) dst_sel:DWORD dst_unused:UNUSED_PAD src0_sel:BYTE_3
	v_fmac_f32_e32 v97, v98, v7
	v_fmac_f32_e32 v97, v99, v11
	v_fmac_f32_e32 v97, v100, v15
	v_fmac_f32_e32 v97, v101, v19
	v_cndmask_b32_e64 v102, v102, v96, s[54:55]
	s_nop 0
	v_add_f32_dpp v97, v97, v97 quad_perm:[1,0,3,2] row_mask:0xf bank_mask:0xf bound_ctrl:1
	s_nop 1
	v_add_f32_dpp v97, v97, v97 quad_perm:[2,3,0,1] row_mask:0xf bank_mask:0xf bound_ctrl:1
	s_nop 1
	v_add_f32_dpp v97, v97, v97 row_half_mirror row_mask:0xf bank_mask:0xf bound_ctrl:1
	v_cndmask_b32_e64 v103, v103, v97, s[54:55]
	global_store_dword v28, v102, s[20:21] offset:768
	global_store_dword v28, v103, s[22:23] offset:768
	s_endpgm

	.amdhsa_kernel _Z15k3_pairs_slicedPKDv4_jPKfPKiS5_PiPf
		.amdhsa_group_segment_fixed_size 0
		.amdhsa_private_segment_fixed_size 0
		.amdhsa_kernarg_size 48
		.amdhsa_user_sgpr_count 2
		.amdhsa_user_sgpr_dispatch_ptr 0
		.amdhsa_user_sgpr_queue_ptr 0
		.amdhsa_user_sgpr_kernarg_segment_ptr 1
		.amdhsa_user_sgpr_dispatch_id 0
		.amdhsa_user_sgpr_kernarg_preload_length 0
		.amdhsa_user_sgpr_kernarg_preload_offset 0
		.amdhsa_user_sgpr_private_segment_size 0
		.amdhsa_uses_dynamic_stack 0
		.amdhsa_enable_private_segment 0
		.amdhsa_system_sgpr_workgroup_id_x 1
		.amdhsa_system_sgpr_workgroup_id_y 0
		.amdhsa_system_sgpr_workgroup_id_z 0
		.amdhsa_system_sgpr_workgroup_info 0
		.amdhsa_system_vgpr_workitem_id 0
		.amdhsa_next_free_vgpr 108
		.amdhsa_next_free_sgpr 56
		.amdhsa_accum_offset 108
		.amdhsa_reserve_vcc 1
		.amdhsa_float_round_mode_32 0
		.amdhsa_float_round_mode_16_64 0
		.amdhsa_float_denorm_mode_32 3
		.amdhsa_float_denorm_mode_16_64 3
		.amdhsa_dx10_clamp 1
		.amdhsa_ieee_mode 1
		.amdhsa_fp16_overflow 0
		.amdhsa_tg_split 0
		.amdhsa_exception_fp_ieee_invalid_op 0
		.amdhsa_exception_fp_denorm_src 0
		.amdhsa_exception_fp_ieee_div_zero 0
		.amdhsa_exception_fp_ieee_overflow 0
		.amdhsa_exception_fp_ieee_underflow 0
		.amdhsa_exception_fp_ieee_inexact 0
		.amdhsa_exception_int_div_zero 0
	.end_amdhsa_kernel
